# plus nt on GEMM epilogue stores (P1,P9,P10) and P6 residual loads/out stores
# baseline (speedup 1.0000x reference)
; #define LAS __attribute__((address_space(3)))
; DI unsigned cvtpk(float lo, float hi) { f32x2 v = {lo, hi}; bf16x2_t b = __builtin_convertvector(v, bf16x2_t); return __builtin_bit_cast(unsigned, b); }
;     DI void operator()(const f32x4 (&acc)[2][2][4][2], const Unit& u, int wr, int wc, int fr, int fq, const LAS unsigned char* st) const {
;     ...
;         const bool isk = u.pn >= 4; const float* gp = (isk ? kg : qg) + wc * 32 + 8 * fq; const float sc = isk ? 1.0f : QSCALE * 1.4426950408889634f;
;         const f32x4 gA = *(const f32x4*)gp, gB = *(const f32x4*)(gp + 4);
; #pragma unroll
;         for (int ai = 0; ai < 2; ++ai)
; #pragma unroll
;             for (int m = 0; m < 4; ++m) { const int rl = ai * HALF + wr * 64 + m * 16 + fr; const int row = u.pm * BM + rl;
;                 bf16* rowp = HM + (isk ? HM_PLANE : (size_t)0) + ((size_t)((row >> 14) * 8 + ((2 * u.pn) & 7)) * SEQ + (row & (SEQ - 1))) * 128 + wc * 32 + 8 * fq;
;                 f32x4 cA = {1.f, 1.f, 1.f, 1.f}, cB = cA, sA = {0.f, 0.f, 0.f, 0.f}, sB = sA;
;                 if (wc == 0) { const int it = 4 * ai + m; if (it + 2 < 8) EPR_LOAD(it + 2);
;                     cA = rc[it % 3][0]; cB = rc[it % 3][1]; sA = rc[it % 3][2]; sB = rc[it % 3][3]; if (fq < 2) { sA = -sA; sB = -sB; } }
; #pragma unroll
;                 for (int bj = 0; bj < 2; ++bj) { const f32x4 pp = *(const LAS f32x4*)(P + (rl * 2 + bj) * 4);
;                     const float rstd = 1.0f / sqrtf(((pp[0] + pp[1]) + (pp[2] + pp[3])) * (1.f / 128.f) + EPS);
;                     f32x4 y0 = acc[ai][bj][m][0] * rstd * gA, y1 = acc[ai][bj][m][1] * rstd * gB;
;                     if (wc == 0) { f32x4 o0, o1;
; #pragma unroll
;                         for (int j = 0; j < 4; ++j) { o0[j] = __shfl_xor(y0[j], 32); o1[j] = __shfl_xor(y1[j], 32); }
;                         y0 = y0 * cA + o0 * sA; y1 = y1 * cB + o1 * sB; }
;                     y0 = y0 * sc; y1 = y1 * sc;
;                     u32x4 w; w.x = cvtpk(y0[0], y0[1]); w.y = cvtpk(y0[2], y0[3]); w.z = cvtpk(y1[0], y1[1]); w.w = cvtpk(y1[2], y1[3]);
;                     *(u32x4*)(rowp + (size_t)bj * SEQ * 128) = w; } }
.LBB0_162:
	s_and_b64 s[0:1], s[46:47], exec
	s_cselect_b32 s1, 0x4000000, 0
	s_lshl_b32 s0, s36, 1
	v_add_u32_e32 v186, s39, v244
	s_and_b32 s0, s0, 6
	v_ashrrev_i32_e32 v212, 11, v186
	v_and_or_b32 v212, v212, -8, s0
	v_cndmask_b32_e64 v194, v237, 1.0, s[46:47]
	s_add_u32 s46, s57, s1
	v_ashrrev_i32_e32 v213, 31, v212
	s_addc_u32 s47, s58, 0
	v_lshlrev_b64 v[212:213], 22, v[212:213]
	v_lshlrev_b32_e32 v186, 8, v186
	v_lshl_add_u64 v[212:213], s[46:47], 0, v[212:213]
	v_and_b32_e32 v186, 0x3fcf00, v186
	v_lshl_add_u64 v[212:213], v[212:213], 0, v[186:187]
	s_lshl_b32 s72, s61, 1
	v_lshl_add_u64 v[212:213], v[212:213], 0, s[72:73]
	v_pk_mul_f32 v[222:223], v[194:195], v[214:215] op_sel_hi:[0,1]
	v_pk_mul_f32 v[214:215], v[194:195], v[216:217] op_sel_hi:[0,1]
	v_pk_mul_f32 v[218:219], v[194:195], v[218:219] op_sel_hi:[0,1]
	v_pk_mul_f32 v[216:217], v[194:195], v[220:221] op_sel_hi:[0,1]
	v_lshl_add_u64 v[212:213], v[192:193], 1, v[212:213]
	v_cvt_pk_bf16_f32 v214, v214, v215
	v_cvt_pk_bf16_f32 v215, v222, v223
	v_cvt_pk_bf16_f32 v216, v216, v217
	v_cvt_pk_bf16_f32 v217, v218, v219
	global_store_dwordx4 v[212:213], v[214:217], off nt
	ds_read_b128 v[214:217], v195 offset:16
	s_waitcnt lgkmcnt(0)
	v_mov_b32_e32 v218, v215
	v_mov_b32_e32 v219, v216
	v_mov_b32_e32 v215, v217
	v_pk_add_f32 v[214:215], v[218:219], v[214:215]
	s_nop 0
	v_add_f32_e32 v186, v214, v215
	v_fmamk_f32 v186, v186, 0x3c000000, v234
	v_cmp_gt_f32_e32 vcc, s86, v186
	v_mul_f32_e32 v195, 0x4f800000, v186
	s_nop 0
	v_cndmask_b32_e32 v186, v186, v195, vcc
	v_sqrt_f32_e32 v195, v186
	s_nop 0
	v_add_u32_e32 v214, -1, v195
	v_fma_f32 v215, -v214, v195, v186
	v_cmp_ge_f32_e64 s[8:9], 0, v215
	v_add_u32_e32 v215, 1, v195
	s_nop 0
	v_cndmask_b32_e64 v214, v195, v214, s[8:9]
	v_fma_f32 v195, -v215, v195, v186
	v_cmp_lt_f32_e64 s[8:9], 0, v195
	s_nop 1
	v_cndmask_b32_e64 v195, v214, v215, s[8:9]
	v_mul_f32_e32 v214, 0x37800000, v195
	v_cndmask_b32_e32 v195, v195, v214, vcc
	v_cmp_class_f32_e32 vcc, v186, v235
	s_nop 1
	v_cndmask_b32_e32 v186, v195, v186, vcc
	v_div_scale_f32 v195, s[8:9], v186, v186, 1.0
	v_rcp_f32_e32 v214, v195
	s_nop 0
	v_fma_f32 v215, -v195, v214, 1.0
	v_fmac_f32_e32 v214, v215, v214
	v_div_scale_f32 v215, vcc, 1.0, v186, 1.0
	v_mul_f32_e32 v216, v215, v214
	v_fma_f32 v217, -v195, v216, v215
	v_fmac_f32_e32 v216, v217, v214
	v_fma_f32 v195, -v195, v216, v215
	v_div_fmas_f32 v195, v195, v214, v216
	v_div_fixup_f32 v186, v195, v186, 1.0
	v_pk_mul_f32 v[216:217], v[114:115], v[186:187] op_sel_hi:[1,0]
	v_pk_mul_f32 v[214:215], v[116:117], v[186:187] op_sel_hi:[1,0]
	v_pk_mul_f32 v[220:221], v[106:107], v[186:187] op_sel_hi:[1,0]
	v_pk_mul_f32 v[218:219], v[108:109], v[186:187] op_sel_hi:[1,0]
	v_pk_mul_f32 v[214:215], v[160:161], v[214:215]
	v_pk_mul_f32 v[216:217], v[158:159], v[216:217]
	v_pk_mul_f32 v[218:219], v[156:157], v[218:219]
	v_pk_mul_f32 v[220:221], v[154:155], v[220:221]
	s_and_b64 vcc, exec, s[4:5]
	s_cbranch_vccnz .LBB0_164
	ds_bpermute_b32 v222, v243, v216
	ds_bpermute_b32 v246, v243, v220
	ds_bpermute_b32 v223, v243, v217
	ds_bpermute_b32 v248, v243, v214
	ds_bpermute_b32 v249, v243, v215
	ds_bpermute_b32 v247, v243, v221
	ds_bpermute_b32 v250, v243, v218
	ds_bpermute_b32 v251, v243, v219
	s_waitcnt lgkmcnt(5)
	v_pk_mul_f32 v[200:201], v[200:201], v[222:223]
	s_waitcnt lgkmcnt(3)
	v_pk_mul_f32 v[208:209], v[208:209], v[248:249]
	s_waitcnt lgkmcnt(2)
	v_pk_mul_f32 v[198:199], v[198:199], v[246:247]
	v_pk_fma_f32 v[214:215], v[210:211], v[214:215], v[208:209]
	s_waitcnt lgkmcnt(0)
	v_pk_mul_f32 v[196:197], v[196:197], v[250:251]
	v_pk_fma_f32 v[216:217], v[202:203], v[216:217], v[200:201]
	v_pk_fma_f32 v[218:219], v[206:207], v[218:219], v[196:197]
	v_pk_fma_f32 v[220:221], v[204:205], v[220:221], v[198:199]
.LBB0_164:
	v_mov_b32_e32 v195, v194
	v_mov_b32_e32 v196, v194
	v_mov_b32_e32 v197, v194
	v_pk_mul_f32 v[200:201], v[194:195], v[216:217]
	v_pk_mul_f32 v[198:199], v[196:197], v[214:215]
	v_pk_mul_f32 v[202:203], v[196:197], v[218:219]
	v_cvt_pk_bf16_f32 v196, v200, v201
	v_add_co_u32_e32 v200, vcc, 0x400000, v212
	v_pk_mul_f32 v[204:205], v[194:195], v[220:221]
	s_nop 0
	v_addc_co_u32_e32 v201, vcc, 0, v213, vcc
	v_cvt_pk_bf16_f32 v197, v198, v199
	v_cvt_pk_bf16_f32 v198, v204, v205
	v_cvt_pk_bf16_f32 v199, v202, v203
	s_and_b64 vcc, exec, s[4:5]
	global_store_dwordx4 v[200:201], v[196:199], off nt
	s_cbranch_vccz .LBB0_166
	v_mov_b32_e32 v200, 0
	v_mov_b32_e32 v202, 1.0
	v_mov_b32_e32 v203, v202
	v_mov_b32_e32 v210, v202
	v_mov_b32_e32 v211, v202
	v_mov_b32_e32 v204, v202
	v_mov_b32_e32 v205, v202
	v_mov_b32_e32 v206, v202
	v_mov_b32_e32 v207, v202
	v_mov_b32_e32 v201, v200
	v_mov_b32_e32 v208, v200
	v_mov_b32_e32 v209, v200
	v_mov_b32_e32 v198, v200
	v_mov_b32_e32 v199, v200
	v_mov_b32_e32 v196, v200
	v_mov_b32_e32 v197, v200
	s_branch .LBB0_167

; #define LAS __attribute__((address_space(3)))
; DI unsigned cvtpk(float lo, float hi) { f32x2 v = {lo, hi}; bf16x2_t b = __builtin_convertvector(v, bf16x2_t); return __builtin_bit_cast(unsigned, b); }
; #define EPR_LOAD(it_) do { const int rl_ = ((it_) >> 2) * HALF + wr * 64 + ((it_) & 3) * 16 + fr; const float* tp_ = rope + (size_t)((u.pm * BM + rl_) & (SEQ - 1)) * 32 + 8 * (fq & 1); \
;             rc[(it_) % 3][0] = *(const f32x4*)tp_; rc[(it_) % 3][1] = *(const f32x4*)(tp_ + 4); rc[(it_) % 3][2] = *(const f32x4*)(tp_ + 16); rc[(it_) % 3][3] = *(const f32x4*)(tp_ + 20); } while (0)
;     DI void operator()(const f32x4 (&acc)[2][2][4][2], const Unit& u, int wr, int wc, int fr, int fq, const LAS unsigned char* st) const {
;     ...
;         for (int ai = 0; ai < 2; ++ai)
; #pragma unroll
;             for (int m = 0; m < 4; ++m) { const int rl = ai * HALF + wr * 64 + m * 16 + fr; const int row = u.pm * BM + rl;
;                 bf16* rowp = HM + (isk ? HM_PLANE : (size_t)0) + ((size_t)((row >> 14) * 8 + ((2 * u.pn) & 7)) * SEQ + (row & (SEQ - 1))) * 128 + wc * 32 + 8 * fq;
;                 f32x4 cA = {1.f, 1.f, 1.f, 1.f}, cB = cA, sA = {0.f, 0.f, 0.f, 0.f}, sB = sA;
;                 if (wc == 0) { const int it = 4 * ai + m; if (it + 2 < 8) EPR_LOAD(it + 2);
;                     cA = rc[it % 3][0]; cB = rc[it % 3][1]; sA = rc[it % 3][2]; sB = rc[it % 3][3]; if (fq < 2) { sA = -sA; sB = -sB; } }
; #pragma unroll
;                 for (int bj = 0; bj < 2; ++bj) { const f32x4 pp = *(const LAS f32x4*)(P + (rl * 2 + bj) * 4);
;                     const float rstd = 1.0f / sqrtf(((pp[0] + pp[1]) + (pp[2] + pp[3])) * (1.f / 128.f) + EPS);
;                     f32x4 y0 = acc[ai][bj][m][0] * rstd * gA, y1 = acc[ai][bj][m][1] * rstd * gB;
;                     if (wc == 0) { f32x4 o0, o1;
; #pragma unroll
;                         for (int j = 0; j < 4; ++j) { o0[j] = __shfl_xor(y0[j], 32); o1[j] = __shfl_xor(y1[j], 32); }
;                         y0 = y0 * cA + o0 * sA; y1 = y1 * cB + o1 * sB; }
;                     y0 = y0 * sc; y1 = y1 * sc;
;                     u32x4 w; w.x = cvtpk(y0[0], y0[1]); w.y = cvtpk(y0[2], y0[3]); w.z = cvtpk(y1[0], y1[1]); w.w = cvtpk(y1[2], y1[3]);
;                     *(u32x4*)(rowp + (size_t)bj * SEQ * 128) = w; } }
.LBB0_169:
	v_add_u32_e32 v186, s39, v186
	v_ashrrev_i32_e32 v212, 11, v186
	v_and_or_b32 v212, v212, -8, s0
	v_ashrrev_i32_e32 v213, 31, v212
	v_lshlrev_b64 v[212:213], 22, v[212:213]
	v_lshlrev_b32_e32 v186, 8, v186
	v_lshl_add_u64 v[212:213], s[46:47], 0, v[212:213]
	v_and_b32_e32 v186, 0x3fdf00, v186
	v_lshl_add_u64 v[212:213], v[212:213], 0, v[186:187]
	v_mov_b32_e32 v214, v194
	v_mov_b32_e32 v215, v194
	v_lshl_add_u64 v[212:213], v[212:213], 0, s[72:73]
	v_pk_mul_f32 v[248:249], v[214:215], v[216:217]
	v_pk_mul_f32 v[216:217], v[194:195], v[218:219]
	v_pk_mul_f32 v[220:221], v[214:215], v[220:221]
	v_pk_mul_f32 v[218:219], v[194:195], v[222:223]
	v_lshl_add_u64 v[212:213], v[192:193], 1, v[212:213]
	v_cvt_pk_bf16_f32 v216, v216, v217
	v_cvt_pk_bf16_f32 v217, v248, v249
	v_cvt_pk_bf16_f32 v218, v218, v219
	v_cvt_pk_bf16_f32 v219, v220, v221
	v_add_u32_e32 v186, s77, v246
	global_store_dwordx4 v[212:213], v[216:219], off nt
	ds_read_b128 v[216:219], v186 offset:16
	s_waitcnt lgkmcnt(0)
	v_mov_b32_e32 v220, v217
	v_mov_b32_e32 v221, v218
	v_mov_b32_e32 v217, v219
	v_pk_add_f32 v[216:217], v[220:221], v[216:217]
	s_nop 0
	v_add_f32_e32 v186, v216, v217
	v_fmamk_f32 v186, v186, 0x3c000000, v234
	v_cmp_gt_f32_e32 vcc, s86, v186
	v_mul_f32_e32 v216, 0x4f800000, v186
	s_nop 0
	v_cndmask_b32_e32 v186, v186, v216, vcc
	v_sqrt_f32_e32 v216, v186
	s_nop 0
	v_add_u32_e32 v217, -1, v216
	v_fma_f32 v218, -v217, v216, v186
	v_cmp_ge_f32_e64 s[8:9], 0, v218
	v_add_u32_e32 v218, 1, v216
	s_nop 0
	v_cndmask_b32_e64 v217, v216, v217, s[8:9]
	v_fma_f32 v216, -v218, v216, v186
	v_cmp_lt_f32_e64 s[8:9], 0, v216
	s_nop 1
	v_cndmask_b32_e64 v216, v217, v218, s[8:9]
	v_mul_f32_e32 v217, 0x37800000, v216
	v_cndmask_b32_e32 v216, v216, v217, vcc
	v_cmp_class_f32_e32 vcc, v186, v235
	s_nop 1
	v_cndmask_b32_e32 v186, v216, v186, vcc
	v_div_scale_f32 v216, s[8:9], v186, v186, 1.0
	v_rcp_f32_e32 v217, v216
	s_nop 0
	v_fma_f32 v218, -v216, v217, 1.0
	v_fmac_f32_e32 v217, v218, v217
	v_div_scale_f32 v218, vcc, 1.0, v186, 1.0
	v_mul_f32_e32 v219, v218, v217
	v_fma_f32 v220, -v216, v219, v218
	v_fmac_f32_e32 v219, v220, v217
	v_fma_f32 v216, -v216, v219, v218
	v_div_fmas_f32 v216, v216, v217, v219
	v_div_fixup_f32 v186, v216, v186, 1.0
	v_pk_mul_f32 v[218:219], v[98:99], v[186:187] op_sel_hi:[1,0]
	v_pk_mul_f32 v[216:217], v[100:101], v[186:187] op_sel_hi:[1,0]
	v_pk_mul_f32 v[222:223], v[90:91], v[186:187] op_sel_hi:[1,0]
	v_pk_mul_f32 v[220:221], v[92:93], v[186:187] op_sel_hi:[1,0]
	v_pk_mul_f32 v[216:217], v[160:161], v[216:217]
	v_pk_mul_f32 v[218:219], v[158:159], v[218:219]
	v_pk_mul_f32 v[220:221], v[156:157], v[220:221]
	v_pk_mul_f32 v[222:223], v[154:155], v[222:223]
	s_and_b64 vcc, exec, s[4:5]
	s_cbranch_vccnz .LBB0_171
	ds_bpermute_b32 v246, v243, v218
	ds_bpermute_b32 v248, v243, v222
	ds_bpermute_b32 v247, v243, v219
	ds_bpermute_b32 v250, v243, v216
	ds_bpermute_b32 v251, v243, v217
	ds_bpermute_b32 v249, v243, v223
	ds_bpermute_b32 v252, v243, v220
	ds_bpermute_b32 v253, v243, v221
	s_waitcnt lgkmcnt(5)
	v_pk_mul_f32 v[200:201], v[200:201], v[246:247]
	s_waitcnt lgkmcnt(3)
	v_pk_mul_f32 v[208:209], v[208:209], v[250:251]
	s_waitcnt lgkmcnt(2)
	v_pk_mul_f32 v[198:199], v[198:199], v[248:249]
	v_pk_fma_f32 v[216:217], v[210:211], v[216:217], v[208:209]
	s_waitcnt lgkmcnt(0)
	v_pk_mul_f32 v[196:197], v[196:197], v[252:253]
	v_pk_fma_f32 v[218:219], v[202:203], v[218:219], v[200:201]
	v_pk_fma_f32 v[220:221], v[206:207], v[220:221], v[196:197]
	v_pk_fma_f32 v[222:223], v[204:205], v[222:223], v[198:199]
.LBB0_171:
	v_pk_mul_f32 v[198:199], v[214:215], v[216:217]
	v_pk_mul_f32 v[196:197], v[194:195], v[218:219]
	v_pk_mul_f32 v[200:201], v[214:215], v[220:221]
	v_cvt_pk_bf16_f32 v196, v196, v197
	v_cvt_pk_bf16_f32 v197, v198, v199
	v_cvt_pk_bf16_f32 v199, v200, v201
	v_add_co_u32_e32 v200, vcc, 0x400000, v212
	v_pk_mul_f32 v[202:203], v[194:195], v[222:223]
	s_nop 0
	v_addc_co_u32_e32 v201, vcc, 0, v213, vcc
	v_cvt_pk_bf16_f32 v198, v202, v203
	s_and_b64 vcc, exec, s[4:5]
	global_store_dwordx4 v[200:201], v[196:199], off nt
	s_cbranch_vccz .LBB0_173
	v_mov_b32_e32 v200, 0
	v_mov_b32_e32 v202, 1.0
	v_mov_b32_e32 v203, v202
	v_mov_b32_e32 v210, v202
	v_mov_b32_e32 v211, v202
	v_mov_b32_e32 v204, v202
	v_mov_b32_e32 v205, v202
	v_mov_b32_e32 v206, v202
	v_mov_b32_e32 v207, v202
	v_mov_b32_e32 v201, v200
	v_mov_b32_e32 v208, v200
	v_mov_b32_e32 v209, v200
	v_mov_b32_e32 v198, v200
	v_mov_b32_e32 v199, v200
	v_mov_b32_e32 v196, v200
	v_mov_b32_e32 v197, v200
	s_branch .LBB0_174

; #define LAS __attribute__((address_space(3)))
; DI unsigned cvtpk(float lo, float hi) { f32x2 v = {lo, hi}; bf16x2_t b = __builtin_convertvector(v, bf16x2_t); return __builtin_bit_cast(unsigned, b); }
; #define EPR_LOAD(it_) do { const int rl_ = ((it_) >> 2) * HALF + wr * 64 + ((it_) & 3) * 16 + fr; const float* tp_ = rope + (size_t)((u.pm * BM + rl_) & (SEQ - 1)) * 32 + 8 * (fq & 1); \
;             rc[(it_) % 3][0] = *(const f32x4*)tp_; rc[(it_) % 3][1] = *(const f32x4*)(tp_ + 4); rc[(it_) % 3][2] = *(const f32x4*)(tp_ + 16); rc[(it_) % 3][3] = *(const f32x4*)(tp_ + 20); } while (0)
;     DI void operator()(const f32x4 (&acc)[2][2][4][2], const Unit& u, int wr, int wc, int fr, int fq, const LAS unsigned char* st) const {
;     ...
;         for (int ai = 0; ai < 2; ++ai)
; #pragma unroll
;             for (int m = 0; m < 4; ++m) { const int rl = ai * HALF + wr * 64 + m * 16 + fr; const int row = u.pm * BM + rl;
;                 bf16* rowp = HM + (isk ? HM_PLANE : (size_t)0) + ((size_t)((row >> 14) * 8 + ((2 * u.pn) & 7)) * SEQ + (row & (SEQ - 1))) * 128 + wc * 32 + 8 * fq;
;                 f32x4 cA = {1.f, 1.f, 1.f, 1.f}, cB = cA, sA = {0.f, 0.f, 0.f, 0.f}, sB = sA;
;                 if (wc == 0) { const int it = 4 * ai + m; if (it + 2 < 8) EPR_LOAD(it + 2);
;                     cA = rc[it % 3][0]; cB = rc[it % 3][1]; sA = rc[it % 3][2]; sB = rc[it % 3][3]; if (fq < 2) { sA = -sA; sB = -sB; } }
; #pragma unroll
;                 for (int bj = 0; bj < 2; ++bj) { const f32x4 pp = *(const LAS f32x4*)(P + (rl * 2 + bj) * 4);
;                     const float rstd = 1.0f / sqrtf(((pp[0] + pp[1]) + (pp[2] + pp[3])) * (1.f / 128.f) + EPS);
;                     f32x4 y0 = acc[ai][bj][m][0] * rstd * gA, y1 = acc[ai][bj][m][1] * rstd * gB;
;                     if (wc == 0) { f32x4 o0, o1;
; #pragma unroll
;                         for (int j = 0; j < 4; ++j) { o0[j] = __shfl_xor(y0[j], 32); o1[j] = __shfl_xor(y1[j], 32); }
;                         y0 = y0 * cA + o0 * sA; y1 = y1 * cB + o1 * sB; }
;                     y0 = y0 * sc; y1 = y1 * sc;
;                     u32x4 w; w.x = cvtpk(y0[0], y0[1]); w.y = cvtpk(y0[2], y0[3]); w.z = cvtpk(y1[0], y1[1]); w.w = cvtpk(y1[2], y1[3]);
;                     *(u32x4*)(rowp + (size_t)bj * SEQ * 128) = w; } }
.LBB0_176:
	v_add_u32_e32 v186, s39, v186
	v_ashrrev_i32_e32 v212, 11, v186
	v_and_or_b32 v212, v212, -8, s0
	v_ashrrev_i32_e32 v213, 31, v212
	v_lshlrev_b64 v[212:213], 22, v[212:213]
	v_lshlrev_b32_e32 v186, 8, v186
	v_lshl_add_u64 v[212:213], s[46:47], 0, v[212:213]
	v_and_b32_e32 v186, 0x3fef00, v186
	v_lshl_add_u64 v[212:213], v[212:213], 0, v[186:187]
	v_mov_b32_e32 v214, v194
	v_mov_b32_e32 v215, v194
	v_lshl_add_u64 v[212:213], v[212:213], 0, s[72:73]
	v_pk_mul_f32 v[248:249], v[214:215], v[216:217]
	v_pk_mul_f32 v[216:217], v[194:195], v[218:219]
	v_pk_mul_f32 v[220:221], v[214:215], v[220:221]
	v_pk_mul_f32 v[218:219], v[194:195], v[222:223]
	v_lshl_add_u64 v[212:213], v[192:193], 1, v[212:213]
	v_cvt_pk_bf16_f32 v216, v216, v217
	v_cvt_pk_bf16_f32 v217, v248, v249
	v_cvt_pk_bf16_f32 v218, v218, v219
	v_cvt_pk_bf16_f32 v219, v220, v221
	v_add_u32_e32 v186, s77, v246
	global_store_dwordx4 v[212:213], v[216:219], off nt
	ds_read_b128 v[216:219], v186 offset:16
	s_waitcnt lgkmcnt(0)
	v_mov_b32_e32 v220, v217
	v_mov_b32_e32 v221, v218
	v_mov_b32_e32 v217, v219
	v_pk_add_f32 v[216:217], v[220:221], v[216:217]
	s_nop 0
	v_add_f32_e32 v186, v216, v217
	v_fmamk_f32 v186, v186, 0x3c000000, v234
	v_cmp_gt_f32_e32 vcc, s86, v186
	v_mul_f32_e32 v216, 0x4f800000, v186
	s_nop 0
	v_cndmask_b32_e32 v186, v186, v216, vcc
	v_sqrt_f32_e32 v216, v186
	s_nop 0
	v_add_u32_e32 v217, -1, v216
	v_fma_f32 v218, -v217, v216, v186
	v_cmp_ge_f32_e64 s[8:9], 0, v218
	v_add_u32_e32 v218, 1, v216
	s_nop 0
	v_cndmask_b32_e64 v217, v216, v217, s[8:9]
	v_fma_f32 v216, -v218, v216, v186
	v_cmp_lt_f32_e64 s[8:9], 0, v216
	s_nop 1
	v_cndmask_b32_e64 v216, v217, v218, s[8:9]
	v_mul_f32_e32 v217, 0x37800000, v216
	v_cndmask_b32_e32 v216, v216, v217, vcc
	v_cmp_class_f32_e32 vcc, v186, v235
	s_nop 1
	v_cndmask_b32_e32 v186, v216, v186, vcc
	v_div_scale_f32 v216, s[8:9], v186, v186, 1.0
	v_rcp_f32_e32 v217, v216
	s_nop 0
	v_fma_f32 v218, -v216, v217, 1.0
	v_fmac_f32_e32 v217, v218, v217
	v_div_scale_f32 v218, vcc, 1.0, v186, 1.0
	v_mul_f32_e32 v219, v218, v217
	v_fma_f32 v220, -v216, v219, v218
	v_fmac_f32_e32 v219, v220, v217
	v_fma_f32 v216, -v216, v219, v218
	v_div_fmas_f32 v216, v216, v217, v219
	v_div_fixup_f32 v186, v216, v186, 1.0
	v_pk_mul_f32 v[218:219], v[82:83], v[186:187] op_sel_hi:[1,0]
	v_pk_mul_f32 v[216:217], v[84:85], v[186:187] op_sel_hi:[1,0]
	v_pk_mul_f32 v[222:223], v[74:75], v[186:187] op_sel_hi:[1,0]
	v_pk_mul_f32 v[220:221], v[76:77], v[186:187] op_sel_hi:[1,0]
	v_pk_mul_f32 v[216:217], v[160:161], v[216:217]
	v_pk_mul_f32 v[218:219], v[158:159], v[218:219]
	v_pk_mul_f32 v[220:221], v[156:157], v[220:221]
	v_pk_mul_f32 v[222:223], v[154:155], v[222:223]
	s_and_b64 vcc, exec, s[4:5]
	s_cbranch_vccnz .LBB0_178
	ds_bpermute_b32 v246, v243, v218
	ds_bpermute_b32 v248, v243, v222
	ds_bpermute_b32 v247, v243, v219
	ds_bpermute_b32 v250, v243, v216
	ds_bpermute_b32 v251, v243, v217
	ds_bpermute_b32 v249, v243, v223
	ds_bpermute_b32 v252, v243, v220
	ds_bpermute_b32 v253, v243, v221
	s_waitcnt lgkmcnt(5)
	v_pk_mul_f32 v[200:201], v[200:201], v[246:247]
	s_waitcnt lgkmcnt(3)
	v_pk_mul_f32 v[208:209], v[208:209], v[250:251]
	s_waitcnt lgkmcnt(2)
	v_pk_mul_f32 v[198:199], v[198:199], v[248:249]
	v_pk_fma_f32 v[216:217], v[210:211], v[216:217], v[208:209]
	s_waitcnt lgkmcnt(0)
	v_pk_mul_f32 v[196:197], v[196:197], v[252:253]
	v_pk_fma_f32 v[218:219], v[202:203], v[218:219], v[200:201]
	v_pk_fma_f32 v[220:221], v[206:207], v[220:221], v[196:197]
	v_pk_fma_f32 v[222:223], v[204:205], v[222:223], v[198:199]

; #define LAS __attribute__((address_space(3)))
; DI unsigned cvtpk(float lo, float hi) { f32x2 v = {lo, hi}; bf16x2_t b = __builtin_convertvector(v, bf16x2_t); return __builtin_bit_cast(unsigned, b); }
; #define EPR_LOAD(it_) do { const int rl_ = ((it_) >> 2) * HALF + wr * 64 + ((it_) & 3) * 16 + fr; const float* tp_ = rope + (size_t)((u.pm * BM + rl_) & (SEQ - 1)) * 32 + 8 * (fq & 1); \
;             rc[(it_) % 3][0] = *(const f32x4*)tp_; rc[(it_) % 3][1] = *(const f32x4*)(tp_ + 4); rc[(it_) % 3][2] = *(const f32x4*)(tp_ + 16); rc[(it_) % 3][3] = *(const f32x4*)(tp_ + 20); } while (0)
;     DI void operator()(const f32x4 (&acc)[2][2][4][2], const Unit& u, int wr, int wc, int fr, int fq, const LAS unsigned char* st) const {
;     ...
;         for (int ai = 0; ai < 2; ++ai)
; #pragma unroll
;             for (int m = 0; m < 4; ++m) { const int rl = ai * HALF + wr * 64 + m * 16 + fr; const int row = u.pm * BM + rl;
;                 bf16* rowp = HM + (isk ? HM_PLANE : (size_t)0) + ((size_t)((row >> 14) * 8 + ((2 * u.pn) & 7)) * SEQ + (row & (SEQ - 1))) * 128 + wc * 32 + 8 * fq;
;                 f32x4 cA = {1.f, 1.f, 1.f, 1.f}, cB = cA, sA = {0.f, 0.f, 0.f, 0.f}, sB = sA;
;                 if (wc == 0) { const int it = 4 * ai + m; if (it + 2 < 8) EPR_LOAD(it + 2);
;                     cA = rc[it % 3][0]; cB = rc[it % 3][1]; sA = rc[it % 3][2]; sB = rc[it % 3][3]; if (fq < 2) { sA = -sA; sB = -sB; } }
; #pragma unroll
;                 for (int bj = 0; bj < 2; ++bj) { const f32x4 pp = *(const LAS f32x4*)(P + (rl * 2 + bj) * 4);
;                     const float rstd = 1.0f / sqrtf(((pp[0] + pp[1]) + (pp[2] + pp[3])) * (1.f / 128.f) + EPS);
;                     f32x4 y0 = acc[ai][bj][m][0] * rstd * gA, y1 = acc[ai][bj][m][1] * rstd * gB;
;                     if (wc == 0) { f32x4 o0, o1;
; #pragma unroll
;                         for (int j = 0; j < 4; ++j) { o0[j] = __shfl_xor(y0[j], 32); o1[j] = __shfl_xor(y1[j], 32); }
;                         y0 = y0 * cA + o0 * sA; y1 = y1 * cB + o1 * sB; }
;                     y0 = y0 * sc; y1 = y1 * sc;
;                     u32x4 w; w.x = cvtpk(y0[0], y0[1]); w.y = cvtpk(y0[2], y0[3]); w.z = cvtpk(y1[0], y1[1]); w.w = cvtpk(y1[2], y1[3]);
;                     *(u32x4*)(rowp + (size_t)bj * SEQ * 128) = w; } }
.LBB0_183:
	v_add_u32_e32 v186, s39, v186
	v_ashrrev_i32_e32 v212, 11, v186
	v_and_or_b32 v212, v212, -8, s0
	v_ashrrev_i32_e32 v213, 31, v212
	v_lshlrev_b64 v[212:213], 22, v[212:213]
	v_lshlrev_b32_e32 v186, 8, v186
	v_lshl_add_u64 v[212:213], s[46:47], 0, v[212:213]
	v_and_b32_e32 v186, 0x3fff00, v186
	v_lshl_add_u64 v[212:213], v[212:213], 0, v[186:187]
	v_mov_b32_e32 v214, v194
	v_mov_b32_e32 v215, v194
	v_lshl_add_u64 v[212:213], v[212:213], 0, s[72:73]
	v_pk_mul_f32 v[248:249], v[214:215], v[216:217]
	v_pk_mul_f32 v[216:217], v[194:195], v[218:219]
	v_pk_mul_f32 v[220:221], v[214:215], v[220:221]
	v_pk_mul_f32 v[218:219], v[194:195], v[222:223]
	v_lshl_add_u64 v[212:213], v[192:193], 1, v[212:213]
	v_cvt_pk_bf16_f32 v216, v216, v217
	v_cvt_pk_bf16_f32 v217, v248, v249
	v_cvt_pk_bf16_f32 v218, v218, v219
	v_cvt_pk_bf16_f32 v219, v220, v221
	v_add_u32_e32 v186, s77, v246
	global_store_dwordx4 v[212:213], v[216:219], off nt
	ds_read_b128 v[216:219], v186 offset:16
	s_waitcnt lgkmcnt(0)
	v_mov_b32_e32 v220, v217
	v_mov_b32_e32 v221, v218
	v_mov_b32_e32 v217, v219
	v_pk_add_f32 v[216:217], v[220:221], v[216:217]
	s_nop 0
	v_add_f32_e32 v186, v216, v217
	v_fmamk_f32 v186, v186, 0x3c000000, v234
	v_cmp_gt_f32_e32 vcc, s86, v186
	v_mul_f32_e32 v216, 0x4f800000, v186
	s_nop 0
	v_cndmask_b32_e32 v186, v186, v216, vcc
	v_sqrt_f32_e32 v216, v186
	s_nop 0
	v_add_u32_e32 v217, -1, v216
	v_fma_f32 v218, -v217, v216, v186
	v_cmp_ge_f32_e64 s[8:9], 0, v218
	v_add_u32_e32 v218, 1, v216
	s_nop 0
	v_cndmask_b32_e64 v217, v216, v217, s[8:9]
	v_fma_f32 v216, -v218, v216, v186
	v_cmp_lt_f32_e64 s[8:9], 0, v216
	s_nop 1
	v_cndmask_b32_e64 v216, v217, v218, s[8:9]
	v_mul_f32_e32 v217, 0x37800000, v216
	v_cndmask_b32_e32 v216, v216, v217, vcc
	v_cmp_class_f32_e32 vcc, v186, v235
	s_nop 1
	v_cndmask_b32_e32 v186, v216, v186, vcc
	v_div_scale_f32 v216, s[8:9], v186, v186, 1.0
	v_rcp_f32_e32 v217, v216
	s_nop 0
	v_fma_f32 v218, -v216, v217, 1.0
	v_fmac_f32_e32 v217, v218, v217
	v_div_scale_f32 v218, vcc, 1.0, v186, 1.0
	v_mul_f32_e32 v219, v218, v217
	v_fma_f32 v220, -v216, v219, v218
	v_fmac_f32_e32 v219, v220, v217
	v_fma_f32 v216, -v216, v219, v218
	v_div_fmas_f32 v216, v216, v217, v219
	v_div_fixup_f32 v186, v216, v186, 1.0
	v_pk_mul_f32 v[218:219], v[70:71], v[186:187] op_sel_hi:[1,0]
	v_pk_mul_f32 v[216:217], v[72:73], v[186:187] op_sel_hi:[1,0]
	v_pk_mul_f32 v[222:223], v[66:67], v[186:187] op_sel_hi:[1,0]
	v_pk_mul_f32 v[220:221], v[68:69], v[186:187] op_sel_hi:[1,0]
	v_pk_mul_f32 v[216:217], v[160:161], v[216:217]
	v_pk_mul_f32 v[218:219], v[158:159], v[218:219]
	v_pk_mul_f32 v[220:221], v[156:157], v[220:221]
	v_pk_mul_f32 v[222:223], v[154:155], v[222:223]
	s_and_b64 vcc, exec, s[4:5]
	s_cbranch_vccnz .LBB0_185
	ds_bpermute_b32 v246, v243, v218
	ds_bpermute_b32 v248, v243, v222
	ds_bpermute_b32 v247, v243, v219
	ds_bpermute_b32 v250, v243, v216
	ds_bpermute_b32 v251, v243, v217
	ds_bpermute_b32 v249, v243, v223
	ds_bpermute_b32 v252, v243, v220
	ds_bpermute_b32 v253, v243, v221
	s_waitcnt lgkmcnt(5)
	v_pk_mul_f32 v[200:201], v[200:201], v[246:247]
	s_waitcnt lgkmcnt(3)
	v_pk_mul_f32 v[208:209], v[208:209], v[250:251]
	s_waitcnt lgkmcnt(2)
	v_pk_mul_f32 v[198:199], v[198:199], v[248:249]
	v_pk_fma_f32 v[216:217], v[210:211], v[216:217], v[208:209]
	s_waitcnt lgkmcnt(0)
	v_pk_mul_f32 v[196:197], v[196:197], v[252:253]
	v_pk_fma_f32 v[218:219], v[202:203], v[218:219], v[200:201]
	v_pk_fma_f32 v[220:221], v[206:207], v[220:221], v[196:197]
	v_pk_fma_f32 v[222:223], v[204:205], v[222:223], v[198:199]

; #define LAS __attribute__((address_space(3)))
; DI unsigned cvtpk(float lo, float hi) { f32x2 v = {lo, hi}; bf16x2_t b = __builtin_convertvector(v, bf16x2_t); return __builtin_bit_cast(unsigned, b); }
; #define EPR_LOAD(it_) do { const int rl_ = ((it_) >> 2) * HALF + wr * 64 + ((it_) & 3) * 16 + fr; const float* tp_ = rope + (size_t)((u.pm * BM + rl_) & (SEQ - 1)) * 32 + 8 * (fq & 1); \
;             rc[(it_) % 3][0] = *(const f32x4*)tp_; rc[(it_) % 3][1] = *(const f32x4*)(tp_ + 4); rc[(it_) % 3][2] = *(const f32x4*)(tp_ + 16); rc[(it_) % 3][3] = *(const f32x4*)(tp_ + 20); } while (0)
;     DI void operator()(const f32x4 (&acc)[2][2][4][2], const Unit& u, int wr, int wc, int fr, int fq, const LAS unsigned char* st) const {
;     ...
;         for (int ai = 0; ai < 2; ++ai)
; #pragma unroll
;             for (int m = 0; m < 4; ++m) { const int rl = ai * HALF + wr * 64 + m * 16 + fr; const int row = u.pm * BM + rl;
;                 bf16* rowp = HM + (isk ? HM_PLANE : (size_t)0) + ((size_t)((row >> 14) * 8 + ((2 * u.pn) & 7)) * SEQ + (row & (SEQ - 1))) * 128 + wc * 32 + 8 * fq;
;                 f32x4 cA = {1.f, 1.f, 1.f, 1.f}, cB = cA, sA = {0.f, 0.f, 0.f, 0.f}, sB = sA;
;                 if (wc == 0) { const int it = 4 * ai + m; if (it + 2 < 8) EPR_LOAD(it + 2);
;                     cA = rc[it % 3][0]; cB = rc[it % 3][1]; sA = rc[it % 3][2]; sB = rc[it % 3][3]; if (fq < 2) { sA = -sA; sB = -sB; } }
; #pragma unroll
;                 for (int bj = 0; bj < 2; ++bj) { const f32x4 pp = *(const LAS f32x4*)(P + (rl * 2 + bj) * 4);
;                     const float rstd = 1.0f / sqrtf(((pp[0] + pp[1]) + (pp[2] + pp[3])) * (1.f / 128.f) + EPS);
;                     f32x4 y0 = acc[ai][bj][m][0] * rstd * gA, y1 = acc[ai][bj][m][1] * rstd * gB;
;                     if (wc == 0) { f32x4 o0, o1;
; #pragma unroll
;                         for (int j = 0; j < 4; ++j) { o0[j] = __shfl_xor(y0[j], 32); o1[j] = __shfl_xor(y1[j], 32); }
;                         y0 = y0 * cA + o0 * sA; y1 = y1 * cB + o1 * sB; }
;                     y0 = y0 * sc; y1 = y1 * sc;
;                     u32x4 w; w.x = cvtpk(y0[0], y0[1]); w.y = cvtpk(y0[2], y0[3]); w.z = cvtpk(y1[0], y1[1]); w.w = cvtpk(y1[2], y1[3]);
;                     *(u32x4*)(rowp + (size_t)bj * SEQ * 128) = w; } }
.LBB0_190:
	v_add_u32_e32 v186, s39, v186
	v_ashrrev_i32_e32 v212, 11, v186
	v_and_or_b32 v212, v212, -8, s0
	v_ashrrev_i32_e32 v213, 31, v212
	v_lshlrev_b64 v[212:213], 22, v[212:213]
	v_lshlrev_b32_e32 v186, 8, v186
	v_lshl_add_u64 v[212:213], s[46:47], 0, v[212:213]
	v_and_b32_e32 v186, 0x3fcf00, v186
	v_lshl_add_u64 v[212:213], v[212:213], 0, v[186:187]
	v_mov_b32_e32 v214, v194
	v_mov_b32_e32 v215, v194
	v_lshl_add_u64 v[212:213], v[212:213], 0, s[72:73]
	v_pk_mul_f32 v[248:249], v[214:215], v[216:217]
	v_pk_mul_f32 v[216:217], v[194:195], v[218:219]
	v_pk_mul_f32 v[220:221], v[214:215], v[220:221]
	v_pk_mul_f32 v[218:219], v[194:195], v[222:223]
	v_lshl_add_u64 v[212:213], v[192:193], 1, v[212:213]
	v_cvt_pk_bf16_f32 v216, v216, v217
	v_cvt_pk_bf16_f32 v217, v248, v249
	v_cvt_pk_bf16_f32 v218, v218, v219
	v_cvt_pk_bf16_f32 v219, v220, v221
	v_add_u32_e32 v186, s77, v246
	global_store_dwordx4 v[212:213], v[216:219], off nt
	ds_read_b128 v[216:219], v186 offset:16
	s_waitcnt lgkmcnt(0)
	v_mov_b32_e32 v220, v217
	v_mov_b32_e32 v221, v218
	v_mov_b32_e32 v217, v219
	v_pk_add_f32 v[216:217], v[220:221], v[216:217]
	s_nop 0
	v_add_f32_e32 v186, v216, v217
	v_fmamk_f32 v186, v186, 0x3c000000, v234
	v_cmp_gt_f32_e32 vcc, s86, v186
	v_mul_f32_e32 v216, 0x4f800000, v186
	s_nop 0
	v_cndmask_b32_e32 v186, v186, v216, vcc
	v_sqrt_f32_e32 v216, v186
	s_nop 0
	v_add_u32_e32 v217, -1, v216
	v_fma_f32 v218, -v217, v216, v186
	v_cmp_ge_f32_e64 s[8:9], 0, v218
	v_add_u32_e32 v218, 1, v216
	s_nop 0
	v_cndmask_b32_e64 v217, v216, v217, s[8:9]
	v_fma_f32 v216, -v218, v216, v186
	v_cmp_lt_f32_e64 s[8:9], 0, v216
	s_nop 1
	v_cndmask_b32_e64 v216, v217, v218, s[8:9]
	v_mul_f32_e32 v217, 0x37800000, v216
	v_cndmask_b32_e32 v216, v216, v217, vcc
	v_cmp_class_f32_e32 vcc, v186, v235
	s_nop 1
	v_cndmask_b32_e32 v186, v216, v186, vcc
	v_div_scale_f32 v216, s[8:9], v186, v186, 1.0
	v_rcp_f32_e32 v217, v216
	s_nop 0
	v_fma_f32 v218, -v216, v217, 1.0
	v_fmac_f32_e32 v217, v218, v217
	v_div_scale_f32 v218, vcc, 1.0, v186, 1.0
	v_mul_f32_e32 v219, v218, v217
	v_fma_f32 v220, -v216, v219, v218
	v_fmac_f32_e32 v219, v220, v217
	v_fma_f32 v216, -v216, v219, v218
	v_div_fmas_f32 v216, v216, v217, v219
	v_div_fixup_f32 v186, v216, v186, 1.0
	v_pk_mul_f32 v[218:219], v[50:51], v[186:187] op_sel_hi:[1,0]
	v_pk_mul_f32 v[216:217], v[52:53], v[186:187] op_sel_hi:[1,0]
	v_pk_mul_f32 v[222:223], v[42:43], v[186:187] op_sel_hi:[1,0]
	v_pk_mul_f32 v[220:221], v[44:45], v[186:187] op_sel_hi:[1,0]
	v_pk_mul_f32 v[216:217], v[160:161], v[216:217]
	v_pk_mul_f32 v[218:219], v[158:159], v[218:219]
	v_pk_mul_f32 v[220:221], v[156:157], v[220:221]
	v_pk_mul_f32 v[222:223], v[154:155], v[222:223]
	s_and_b64 vcc, exec, s[4:5]
	s_cbranch_vccnz .LBB0_192
	ds_bpermute_b32 v246, v243, v218
	ds_bpermute_b32 v248, v243, v222
	ds_bpermute_b32 v247, v243, v219
	ds_bpermute_b32 v250, v243, v216
	ds_bpermute_b32 v251, v243, v217
	ds_bpermute_b32 v249, v243, v223
	ds_bpermute_b32 v252, v243, v220
	ds_bpermute_b32 v253, v243, v221
	s_waitcnt lgkmcnt(5)
	v_pk_mul_f32 v[200:201], v[200:201], v[246:247]
	s_waitcnt lgkmcnt(3)
	v_pk_mul_f32 v[208:209], v[208:209], v[250:251]
	s_waitcnt lgkmcnt(2)
	v_pk_mul_f32 v[198:199], v[198:199], v[248:249]
	v_pk_fma_f32 v[216:217], v[210:211], v[216:217], v[208:209]
	s_waitcnt lgkmcnt(0)
	v_pk_mul_f32 v[196:197], v[196:197], v[252:253]
	v_pk_fma_f32 v[218:219], v[202:203], v[218:219], v[200:201]
	v_pk_fma_f32 v[220:221], v[206:207], v[220:221], v[196:197]
	v_pk_fma_f32 v[222:223], v[204:205], v[222:223], v[198:199]
.LBB0_192:
	v_pk_mul_f32 v[198:199], v[214:215], v[216:217]
	v_pk_mul_f32 v[196:197], v[194:195], v[218:219]
	v_pk_mul_f32 v[200:201], v[214:215], v[220:221]
	v_cvt_pk_bf16_f32 v196, v196, v197
	v_cvt_pk_bf16_f32 v197, v198, v199
	v_cvt_pk_bf16_f32 v199, v200, v201
	v_add_co_u32_e32 v200, vcc, 0x400000, v212
	v_pk_mul_f32 v[202:203], v[194:195], v[222:223]
	s_nop 0
	v_addc_co_u32_e32 v201, vcc, 0, v213, vcc
	v_cvt_pk_bf16_f32 v198, v202, v203
	s_and_b64 vcc, exec, s[4:5]
	global_store_dwordx4 v[200:201], v[196:199], off nt
	s_cbranch_vccz .LBB0_194
	s_waitcnt vmcnt(6)
	v_mov_b32_e32 v178, 0
	s_waitcnt vmcnt(4)
	v_mov_b32_e32 v174, 1.0
	v_mov_b32_e32 v175, v174
	v_mov_b32_e32 v176, v174
	v_mov_b32_e32 v177, v174
	v_mov_b32_e32 v170, v174
	v_mov_b32_e32 v171, v174
	v_mov_b32_e32 v172, v174
	v_mov_b32_e32 v173, v174
	v_mov_b32_e32 v179, v178
	v_mov_b32_e32 v180, v178
	v_mov_b32_e32 v181, v178
	v_mov_b32_e32 v196, v178
	v_mov_b32_e32 v197, v178
	v_mov_b32_e32 v182, v178
	v_mov_b32_e32 v183, v178
	s_branch .LBB0_195

; #define LAS __attribute__((address_space(3)))
; DI unsigned cvtpk(float lo, float hi) { f32x2 v = {lo, hi}; bf16x2_t b = __builtin_convertvector(v, bf16x2_t); return __builtin_bit_cast(unsigned, b); }
; #define EPR_LOAD(it_) do { const int rl_ = ((it_) >> 2) * HALF + wr * 64 + ((it_) & 3) * 16 + fr; const float* tp_ = rope + (size_t)((u.pm * BM + rl_) & (SEQ - 1)) * 32 + 8 * (fq & 1); \
;             rc[(it_) % 3][0] = *(const f32x4*)tp_; rc[(it_) % 3][1] = *(const f32x4*)(tp_ + 4); rc[(it_) % 3][2] = *(const f32x4*)(tp_ + 16); rc[(it_) % 3][3] = *(const f32x4*)(tp_ + 20); } while (0)
;     DI void operator()(const f32x4 (&acc)[2][2][4][2], const Unit& u, int wr, int wc, int fr, int fq, const LAS unsigned char* st) const {
;     ...
;         for (int ai = 0; ai < 2; ++ai)
; #pragma unroll
;             for (int m = 0; m < 4; ++m) { const int rl = ai * HALF + wr * 64 + m * 16 + fr; const int row = u.pm * BM + rl;
;                 bf16* rowp = HM + (isk ? HM_PLANE : (size_t)0) + ((size_t)((row >> 14) * 8 + ((2 * u.pn) & 7)) * SEQ + (row & (SEQ - 1))) * 128 + wc * 32 + 8 * fq;
;                 f32x4 cA = {1.f, 1.f, 1.f, 1.f}, cB = cA, sA = {0.f, 0.f, 0.f, 0.f}, sB = sA;
;                 if (wc == 0) { const int it = 4 * ai + m; if (it + 2 < 8) EPR_LOAD(it + 2);
;                     cA = rc[it % 3][0]; cB = rc[it % 3][1]; sA = rc[it % 3][2]; sB = rc[it % 3][3]; if (fq < 2) { sA = -sA; sB = -sB; } }
; #pragma unroll
;                 for (int bj = 0; bj < 2; ++bj) { const f32x4 pp = *(const LAS f32x4*)(P + (rl * 2 + bj) * 4);
;                     const float rstd = 1.0f / sqrtf(((pp[0] + pp[1]) + (pp[2] + pp[3])) * (1.f / 128.f) + EPS);
;                     f32x4 y0 = acc[ai][bj][m][0] * rstd * gA, y1 = acc[ai][bj][m][1] * rstd * gB;
;                     if (wc == 0) { f32x4 o0, o1;
; #pragma unroll
;                         for (int j = 0; j < 4; ++j) { o0[j] = __shfl_xor(y0[j], 32); o1[j] = __shfl_xor(y1[j], 32); }
;                         y0 = y0 * cA + o0 * sA; y1 = y1 * cB + o1 * sB; }
;                     y0 = y0 * sc; y1 = y1 * sc;
;                     u32x4 w; w.x = cvtpk(y0[0], y0[1]); w.y = cvtpk(y0[2], y0[3]); w.z = cvtpk(y1[0], y1[1]); w.w = cvtpk(y1[2], y1[3]);
;                     *(u32x4*)(rowp + (size_t)bj * SEQ * 128) = w; } }
.LBB0_197:
	v_add_u32_e32 v186, s39, v184
	v_ashrrev_i32_e32 v184, 11, v186
	v_and_or_b32 v184, v184, -8, s0
	v_ashrrev_i32_e32 v185, 31, v184
	v_lshlrev_b64 v[184:185], 22, v[184:185]
	v_lshlrev_b32_e32 v186, 8, v186
	v_lshl_add_u64 v[184:185], s[46:47], 0, v[184:185]
	v_and_b32_e32 v186, 0x3fdf00, v186
	v_lshl_add_u64 v[184:185], v[184:185], 0, v[186:187]
	v_mov_b32_e32 v198, v194
	v_mov_b32_e32 v199, v194
	v_lshl_add_u64 v[184:185], v[184:185], 0, s[72:73]
	v_pk_mul_f32 v[210:211], v[198:199], v[200:201]
	v_pk_mul_f32 v[200:201], v[194:195], v[202:203]
	v_pk_mul_f32 v[204:205], v[198:199], v[204:205]
	v_pk_mul_f32 v[202:203], v[194:195], v[206:207]
	v_lshl_add_u64 v[184:185], v[192:193], 1, v[184:185]
	v_cvt_pk_bf16_f32 v200, v200, v201
	v_cvt_pk_bf16_f32 v201, v210, v211
	v_cvt_pk_bf16_f32 v202, v202, v203
	v_cvt_pk_bf16_f32 v203, v204, v205
	v_add_u32_e32 v186, s77, v208
	global_store_dwordx4 v[184:185], v[200:203], off nt
	ds_read_b128 v[200:203], v186 offset:16
	s_waitcnt lgkmcnt(0)
	v_mov_b32_e32 v204, v201
	v_mov_b32_e32 v205, v202
	v_mov_b32_e32 v201, v203
	v_pk_add_f32 v[200:201], v[204:205], v[200:201]
	s_nop 0
	v_add_f32_e32 v186, v200, v201
	v_fmamk_f32 v186, v186, 0x3c000000, v234
	v_cmp_gt_f32_e32 vcc, s86, v186
	v_mul_f32_e32 v200, 0x4f800000, v186
	s_nop 0
	v_cndmask_b32_e32 v186, v186, v200, vcc
	v_sqrt_f32_e32 v200, v186
	s_nop 0
	v_add_u32_e32 v201, -1, v200
	v_fma_f32 v202, -v201, v200, v186
	v_cmp_ge_f32_e64 s[8:9], 0, v202
	v_add_u32_e32 v202, 1, v200
	s_nop 0
	v_cndmask_b32_e64 v201, v200, v201, s[8:9]
	v_fma_f32 v200, -v202, v200, v186
	v_cmp_lt_f32_e64 s[8:9], 0, v200
	s_nop 1
	v_cndmask_b32_e64 v200, v201, v202, s[8:9]
	v_mul_f32_e32 v201, 0x37800000, v200
	v_cndmask_b32_e32 v200, v200, v201, vcc
	v_cmp_class_f32_e32 vcc, v186, v235
	s_nop 1
	v_cndmask_b32_e32 v186, v200, v186, vcc
	v_div_scale_f32 v200, s[8:9], v186, v186, 1.0
	v_rcp_f32_e32 v201, v200
	s_nop 0
	v_fma_f32 v202, -v200, v201, 1.0
	v_fmac_f32_e32 v201, v202, v201
	v_div_scale_f32 v202, vcc, 1.0, v186, 1.0
	v_mul_f32_e32 v203, v202, v201
	v_fma_f32 v204, -v200, v203, v202
	v_fmac_f32_e32 v203, v204, v201
	v_fma_f32 v200, -v200, v203, v202
	v_div_fmas_f32 v200, v200, v201, v203
	v_div_fixup_f32 v186, v200, v186, 1.0
	v_pk_mul_f32 v[202:203], v[34:35], v[186:187] op_sel_hi:[1,0]
	v_pk_mul_f32 v[200:201], v[36:37], v[186:187] op_sel_hi:[1,0]
	v_pk_mul_f32 v[206:207], v[26:27], v[186:187] op_sel_hi:[1,0]
	v_pk_mul_f32 v[204:205], v[28:29], v[186:187] op_sel_hi:[1,0]
	v_pk_mul_f32 v[200:201], v[160:161], v[200:201]
	v_pk_mul_f32 v[202:203], v[158:159], v[202:203]
	v_pk_mul_f32 v[204:205], v[156:157], v[204:205]
	v_pk_mul_f32 v[206:207], v[154:155], v[206:207]
	s_and_b64 vcc, exec, s[4:5]
	s_cbranch_vccnz .LBB0_199
	ds_bpermute_b32 v208, v243, v202
	ds_bpermute_b32 v209, v243, v203
	ds_bpermute_b32 v212, v243, v200
	ds_bpermute_b32 v213, v243, v201
	ds_bpermute_b32 v210, v243, v206
	ds_bpermute_b32 v211, v243, v207
	ds_bpermute_b32 v214, v243, v204
	ds_bpermute_b32 v215, v243, v205
	s_waitcnt lgkmcnt(6)
	v_pk_mul_f32 v[178:179], v[178:179], v[208:209]
	s_waitcnt lgkmcnt(4)
	v_pk_mul_f32 v[180:181], v[180:181], v[212:213]
	s_waitcnt vmcnt(9)
	v_pk_fma_f32 v[202:203], v[174:175], v[202:203], v[178:179]
	v_pk_fma_f32 v[200:201], v[176:177], v[200:201], v[180:181]
	s_waitcnt lgkmcnt(2)
	v_pk_mul_f32 v[174:175], v[196:197], v[210:211]
	s_waitcnt lgkmcnt(0)
	v_pk_mul_f32 v[176:177], v[182:183], v[214:215]
	v_pk_fma_f32 v[206:207], v[170:171], v[206:207], v[174:175]
	v_pk_fma_f32 v[204:205], v[172:173], v[204:205], v[176:177]
.LBB0_199:
	s_waitcnt vmcnt(10)
	v_pk_mul_f32 v[172:173], v[198:199], v[200:201]
	v_pk_mul_f32 v[170:171], v[194:195], v[202:203]
	s_waitcnt vmcnt(9)
	v_pk_mul_f32 v[174:175], v[198:199], v[204:205]
	v_cvt_pk_bf16_f32 v170, v170, v171
	v_cvt_pk_bf16_f32 v171, v172, v173
	v_cvt_pk_bf16_f32 v173, v174, v175
	v_add_co_u32_e32 v174, vcc, 0x400000, v184
	v_pk_mul_f32 v[176:177], v[194:195], v[206:207]
	s_nop 0
	v_addc_co_u32_e32 v175, vcc, 0, v185, vcc
	v_cvt_pk_bf16_f32 v172, v176, v177
	s_and_b64 vcc, exec, s[4:5]
	global_store_dwordx4 v[174:175], v[170:173], off nt
	s_cbranch_vccz .LBB0_201
	v_mov_b32_e32 v166, 0
	s_waitcnt vmcnt(4)
	v_mov_b32_e32 v150, 1.0
	v_mov_b32_e32 v151, v150
	v_mov_b32_e32 v152, v150
	v_mov_b32_e32 v153, v150
	v_mov_b32_e32 v146, v150
	v_mov_b32_e32 v147, v150
	v_mov_b32_e32 v148, v150
	v_mov_b32_e32 v149, v150
	v_mov_b32_e32 v167, v166
	v_mov_b32_e32 v170, v166
	v_mov_b32_e32 v171, v166
	v_mov_b32_e32 v168, v166
	v_mov_b32_e32 v169, v166
	v_mov_b32_e32 v162, v166
	v_mov_b32_e32 v163, v166
	s_branch .LBB0_202

; #define LAS __attribute__((address_space(3)))
; DI unsigned cvtpk(float lo, float hi) { f32x2 v = {lo, hi}; bf16x2_t b = __builtin_convertvector(v, bf16x2_t); return __builtin_bit_cast(unsigned, b); }
; #define EPR_LOAD(it_) do { const int rl_ = ((it_) >> 2) * HALF + wr * 64 + ((it_) & 3) * 16 + fr; const float* tp_ = rope + (size_t)((u.pm * BM + rl_) & (SEQ - 1)) * 32 + 8 * (fq & 1); \
;             rc[(it_) % 3][0] = *(const f32x4*)tp_; rc[(it_) % 3][1] = *(const f32x4*)(tp_ + 4); rc[(it_) % 3][2] = *(const f32x4*)(tp_ + 16); rc[(it_) % 3][3] = *(const f32x4*)(tp_ + 20); } while (0)
;     DI void operator()(const f32x4 (&acc)[2][2][4][2], const Unit& u, int wr, int wc, int fr, int fq, const LAS unsigned char* st) const {
;     ...
;         for (int ai = 0; ai < 2; ++ai)
; #pragma unroll
;             for (int m = 0; m < 4; ++m) { const int rl = ai * HALF + wr * 64 + m * 16 + fr; const int row = u.pm * BM + rl;
;                 bf16* rowp = HM + (isk ? HM_PLANE : (size_t)0) + ((size_t)((row >> 14) * 8 + ((2 * u.pn) & 7)) * SEQ + (row & (SEQ - 1))) * 128 + wc * 32 + 8 * fq;
;                 f32x4 cA = {1.f, 1.f, 1.f, 1.f}, cB = cA, sA = {0.f, 0.f, 0.f, 0.f}, sB = sA;
;                 if (wc == 0) { const int it = 4 * ai + m; if (it + 2 < 8) EPR_LOAD(it + 2);
;                     cA = rc[it % 3][0]; cB = rc[it % 3][1]; sA = rc[it % 3][2]; sB = rc[it % 3][3]; if (fq < 2) { sA = -sA; sB = -sB; } }
; #pragma unroll
;                 for (int bj = 0; bj < 2; ++bj) { const f32x4 pp = *(const LAS f32x4*)(P + (rl * 2 + bj) * 4);
;                     const float rstd = 1.0f / sqrtf(((pp[0] + pp[1]) + (pp[2] + pp[3])) * (1.f / 128.f) + EPS);
;                     f32x4 y0 = acc[ai][bj][m][0] * rstd * gA, y1 = acc[ai][bj][m][1] * rstd * gB;
;                     if (wc == 0) { f32x4 o0, o1;
; #pragma unroll
;                         for (int j = 0; j < 4; ++j) { o0[j] = __shfl_xor(y0[j], 32); o1[j] = __shfl_xor(y1[j], 32); }
;                         y0 = y0 * cA + o0 * sA; y1 = y1 * cB + o1 * sB; }
;                     y0 = y0 * sc; y1 = y1 * sc;
;                     u32x4 w; w.x = cvtpk(y0[0], y0[1]); w.y = cvtpk(y0[2], y0[3]); w.z = cvtpk(y1[0], y1[1]); w.w = cvtpk(y1[2], y1[3]);
;                     *(u32x4*)(rowp + (size_t)bj * SEQ * 128) = w; } }
.LBB0_204:
	v_add_u32_e32 v172, s39, v164
	v_ashrrev_i32_e32 v164, 11, v172
	v_and_or_b32 v164, v164, -8, s0
	v_ashrrev_i32_e32 v165, 31, v164
	v_lshlrev_b64 v[164:165], 22, v[164:165]
	v_lshlrev_b32_e32 v172, 8, v172
	v_lshl_add_u64 v[164:165], s[46:47], 0, v[164:165]
	v_and_b32_e32 v186, 0x3fef00, v172
	v_lshl_add_u64 v[164:165], v[164:165], 0, v[186:187]
	v_mov_b32_e32 v172, v194
	v_mov_b32_e32 v173, v194
	v_lshl_add_u64 v[164:165], v[164:165], 0, s[72:73]
	v_pk_mul_f32 v[184:185], v[172:173], v[174:175]
	v_pk_mul_f32 v[174:175], v[194:195], v[176:177]
	v_pk_mul_f32 v[178:179], v[172:173], v[178:179]
	v_pk_mul_f32 v[176:177], v[194:195], v[180:181]
	v_lshl_add_u64 v[164:165], v[192:193], 1, v[164:165]
	v_cvt_pk_bf16_f32 v174, v174, v175
	v_cvt_pk_bf16_f32 v175, v184, v185
	v_cvt_pk_bf16_f32 v176, v176, v177
	v_cvt_pk_bf16_f32 v177, v178, v179
	global_store_dwordx4 v[164:165], v[174:177], off nt
	s_nop 1
	v_add_u32_e32 v174, s77, v182
	ds_read_b128 v[174:177], v174 offset:16
	s_waitcnt lgkmcnt(0)
	v_mov_b32_e32 v178, v175
	v_mov_b32_e32 v179, v176
	v_mov_b32_e32 v175, v177
	v_pk_add_f32 v[174:175], v[178:179], v[174:175]
	s_nop 0
	v_add_f32_e32 v174, v174, v175
	v_fmamk_f32 v174, v174, 0x3c000000, v234
	v_cmp_gt_f32_e32 vcc, s86, v174
	v_mul_f32_e32 v175, 0x4f800000, v174
	s_nop 0
	v_cndmask_b32_e32 v174, v174, v175, vcc
	v_sqrt_f32_e32 v175, v174
	s_nop 0
	v_add_u32_e32 v176, -1, v175
	v_fma_f32 v177, -v176, v175, v174
	v_cmp_ge_f32_e64 s[8:9], 0, v177
	v_add_u32_e32 v177, 1, v175
	s_nop 0
	v_cndmask_b32_e64 v176, v175, v176, s[8:9]
	v_fma_f32 v175, -v177, v175, v174
	v_cmp_lt_f32_e64 s[8:9], 0, v175
	s_nop 1
	v_cndmask_b32_e64 v175, v176, v177, s[8:9]
	v_mul_f32_e32 v176, 0x37800000, v175
	v_cndmask_b32_e32 v175, v175, v176, vcc
	v_cmp_class_f32_e32 vcc, v174, v235
	s_nop 1
	v_cndmask_b32_e32 v174, v175, v174, vcc
	v_div_scale_f32 v175, s[8:9], v174, v174, 1.0
	v_rcp_f32_e32 v176, v175
	s_nop 0
	v_fma_f32 v177, -v175, v176, 1.0
	v_fmac_f32_e32 v176, v177, v176
	v_div_scale_f32 v177, vcc, 1.0, v174, 1.0
	v_mul_f32_e32 v178, v177, v176
	v_fma_f32 v179, -v175, v178, v177
	v_fmac_f32_e32 v178, v179, v176
	v_fma_f32 v175, -v175, v178, v177
	v_div_fmas_f32 v175, v175, v176, v178
	v_div_fixup_f32 v178, v175, v174, 1.0
	v_pk_mul_f32 v[176:177], v[18:19], v[178:179] op_sel_hi:[1,0]
	v_pk_mul_f32 v[174:175], v[20:21], v[178:179] op_sel_hi:[1,0]
	v_pk_mul_f32 v[180:181], v[10:11], v[178:179] op_sel_hi:[1,0]
	v_pk_mul_f32 v[178:179], v[12:13], v[178:179] op_sel_hi:[1,0]
	v_pk_mul_f32 v[174:175], v[160:161], v[174:175]
	v_pk_mul_f32 v[176:177], v[158:159], v[176:177]
	v_pk_mul_f32 v[178:179], v[156:157], v[178:179]
	v_pk_mul_f32 v[180:181], v[154:155], v[180:181]
	s_and_b64 vcc, exec, s[4:5]
	s_cbranch_vccnz .LBB0_206
	ds_bpermute_b32 v182, v243, v176
	ds_bpermute_b32 v183, v243, v177
	ds_bpermute_b32 v196, v243, v174
	ds_bpermute_b32 v197, v243, v175
	ds_bpermute_b32 v184, v243, v180
	ds_bpermute_b32 v185, v243, v181
	ds_bpermute_b32 v198, v243, v178
	ds_bpermute_b32 v199, v243, v179
	s_waitcnt lgkmcnt(6)
	v_pk_mul_f32 v[166:167], v[166:167], v[182:183]
	s_waitcnt lgkmcnt(4)
	v_pk_mul_f32 v[170:171], v[170:171], v[196:197]
	s_waitcnt vmcnt(5)
	v_pk_fma_f32 v[176:177], v[150:151], v[176:177], v[166:167]
	v_pk_fma_f32 v[174:175], v[152:153], v[174:175], v[170:171]
	s_waitcnt lgkmcnt(2)
	v_pk_mul_f32 v[150:151], v[168:169], v[184:185]
	s_waitcnt lgkmcnt(0)
	v_pk_mul_f32 v[152:153], v[162:163], v[198:199]
	v_pk_fma_f32 v[180:181], v[146:147], v[180:181], v[150:151]
	v_pk_fma_f32 v[178:179], v[148:149], v[178:179], v[152:153]
.LBB0_206:
	s_waitcnt vmcnt(6)
	v_pk_mul_f32 v[148:149], v[172:173], v[174:175]
	v_pk_mul_f32 v[146:147], v[194:195], v[176:177]
	s_waitcnt vmcnt(5)
	v_pk_mul_f32 v[150:151], v[172:173], v[178:179]
	v_cvt_pk_bf16_f32 v146, v146, v147
	v_cvt_pk_bf16_f32 v147, v148, v149
	v_cvt_pk_bf16_f32 v149, v150, v151
	v_add_co_u32_e32 v150, vcc, 0x400000, v164
	v_pk_mul_f32 v[152:153], v[194:195], v[180:181]
	s_nop 0
	v_addc_co_u32_e32 v151, vcc, 0, v165, vcc
	v_cvt_pk_bf16_f32 v148, v152, v153
	s_and_b64 vcc, exec, s[4:5]
	global_store_dwordx4 v[150:151], v[146:149], off nt
	s_cbranch_vccz .LBB0_208
	v_mov_b32_e32 v142, 0
	s_waitcnt vmcnt(4)
	v_mov_b32_e32 v134, 1.0
	v_mov_b32_e32 v135, v134
	v_mov_b32_e32 v136, v134
	v_mov_b32_e32 v137, v134
	v_mov_b32_e32 v130, v134
	v_mov_b32_e32 v131, v134
	v_mov_b32_e32 v132, v134
	v_mov_b32_e32 v133, v134
	v_mov_b32_e32 v143, v142
	v_mov_b32_e32 v146, v142
	v_mov_b32_e32 v147, v142
	v_mov_b32_e32 v144, v142
	v_mov_b32_e32 v145, v142
	v_mov_b32_e32 v138, v142
	v_mov_b32_e32 v139, v142
	s_branch .LBB0_209

;     DI void operator()(const f32x4 (&acc)[2][2][4][2], const Unit& u, int wr, int wc, int fr, int fq, const LAS unsigned char* st) const {
;     ...
;         if (u.pn >= 8) {
; #pragma unroll
;             for (int ai = 0; ai < 2; ++ai)
; #pragma unroll
;                 for (int m = 0; m < 4; ++m) { const int row = row0 + ai * HALF + m * 16; bf16* rowp = O + (size_t)row * ldc + col0;
;                     if (u.pn < 12) rowp = HM + 2 * HM_PLANE + ((size_t)((row >> 14) * 8 + ((2 * u.pn) & 7)) * SEQ + (row & (SEQ - 1))) * 128 + wc * 32 + 8 * fq;
; #pragma unroll
;                     for (int bj = 0; bj < 2; ++bj) { const f32x4 v0 = acc[ai][bj][m][0], v1 = acc[ai][bj][m][1];
;                         u32x4 w; w.x = cvtpk(v0[0], v0[1]); w.y = cvtpk(v0[2], v0[3]); w.z = cvtpk(v1[0], v1[1]); w.w = cvtpk(v1[2], v1[3]);
;     ...
;         for (int ai = 0; ai < 2; ++ai)
; #pragma unroll
;             for (int m = 0; m < 4; ++m) { const int rl = ai * HALF + wr * 64 + m * 16 + fr; const int row = u.pm * BM + rl;
;                 bf16* rowp = HM + (isk ? HM_PLANE : (size_t)0) + ((size_t)((row >> 14) * 8 + ((2 * u.pn) & 7)) * SEQ + (row & (SEQ - 1))) * 128 + wc * 32 + 8 * fq;
;                 f32x4 cA = {1.f, 1.f, 1.f, 1.f}, cB = cA, sA = {0.f, 0.f, 0.f, 0.f}, sB = sA;
;                 if (wc == 0) { const int it = 4 * ai + m; if (it + 2 < 8) EPR_LOAD(it + 2);
;                     cA = rc[it % 3][0]; cB = rc[it % 3][1]; sA = rc[it % 3][2]; sB = rc[it % 3][3]; if (fq < 2) { sA = -sA; sB = -sB; } }
; #pragma unroll
;                 for (int bj = 0; bj < 2; ++bj) { const f32x4 pp = *(const LAS f32x4*)(P + (rl * 2 + bj) * 4);
;                     const float rstd = 1.0f / sqrtf(((pp[0] + pp[1]) + (pp[2] + pp[3])) * (1.f / 128.f) + EPS);
;                     f32x4 y0 = acc[ai][bj][m][0] * rstd * gA, y1 = acc[ai][bj][m][1] * rstd * gB;
;                     if (wc == 0) { f32x4 o0, o1;
; #pragma unroll
;                         for (int j = 0; j < 4; ++j) { o0[j] = __shfl_xor(y0[j], 32); o1[j] = __shfl_xor(y1[j], 32); }
;                         y0 = y0 * cA + o0 * sA; y1 = y1 * cB + o1 * sB; }
;                     y0 = y0 * sc; y1 = y1 * sc;
;                     u32x4 w; w.x = cvtpk(y0[0], y0[1]); w.y = cvtpk(y0[2], y0[3]); w.z = cvtpk(y1[0], y1[1]); w.w = cvtpk(y1[2], y1[3]);
;                     *(u32x4*)(rowp + (size_t)bj * SEQ * 128) = w; } }
.LBB0_211:
	v_add_u32_e32 v148, s39, v140
	v_ashrrev_i32_e32 v140, 11, v148
	v_and_or_b32 v140, v140, -8, s0
	v_ashrrev_i32_e32 v141, 31, v140
	v_lshlrev_b64 v[140:141], 22, v[140:141]
	v_lshlrev_b32_e32 v148, 8, v148
	v_lshl_add_u64 v[140:141], s[46:47], 0, v[140:141]
	v_and_b32_e32 v186, 0x3fff00, v148
	v_lshl_add_u64 v[140:141], v[140:141], 0, v[186:187]
	v_mov_b32_e32 v148, v194
	v_mov_b32_e32 v149, v194
	v_lshl_add_u64 v[140:141], v[140:141], 0, s[72:73]
	v_pk_mul_f32 v[168:169], v[148:149], v[150:151]
	v_pk_mul_f32 v[150:151], v[194:195], v[152:153]
	v_pk_mul_f32 v[162:163], v[148:149], v[162:163]
	v_pk_mul_f32 v[152:153], v[194:195], v[164:165]
	v_lshl_add_u64 v[140:141], v[192:193], 1, v[140:141]
	v_cvt_pk_bf16_f32 v150, v150, v151
	v_cvt_pk_bf16_f32 v151, v168, v169
	v_cvt_pk_bf16_f32 v152, v152, v153
	v_cvt_pk_bf16_f32 v153, v162, v163
	global_store_dwordx4 v[140:141], v[150:153], off nt
	s_nop 1
	v_add_u32_e32 v150, s77, v166
	ds_read_b128 v[150:153], v150 offset:16
	s_waitcnt lgkmcnt(0)
	v_mov_b32_e32 v162, v151
	v_mov_b32_e32 v163, v152
	v_mov_b32_e32 v151, v153
	v_pk_add_f32 v[150:151], v[162:163], v[150:151]
	s_nop 0
	v_add_f32_e32 v150, v150, v151
	v_fmamk_f32 v150, v150, 0x3c000000, v234
	v_cmp_gt_f32_e32 vcc, s86, v150
	v_mul_f32_e32 v151, 0x4f800000, v150
	s_nop 0
	v_cndmask_b32_e32 v150, v150, v151, vcc
	v_sqrt_f32_e32 v151, v150
	s_nop 0
	v_add_u32_e32 v152, -1, v151
	v_fma_f32 v153, -v152, v151, v150
	v_cmp_ge_f32_e64 s[6:7], 0, v153
	v_add_u32_e32 v153, 1, v151
	s_nop 0
	v_cndmask_b32_e64 v152, v151, v152, s[6:7]
	v_fma_f32 v151, -v153, v151, v150
	v_cmp_lt_f32_e64 s[6:7], 0, v151
	s_nop 1
	v_cndmask_b32_e64 v151, v152, v153, s[6:7]
	v_mul_f32_e32 v152, 0x37800000, v151
	v_cndmask_b32_e32 v151, v151, v152, vcc
	v_cmp_class_f32_e32 vcc, v150, v235
	s_nop 1
	v_cndmask_b32_e32 v150, v151, v150, vcc
	v_div_scale_f32 v151, s[0:1], v150, v150, 1.0
	v_rcp_f32_e32 v152, v151
	s_nop 0
	v_fma_f32 v153, -v151, v152, 1.0
	v_fmac_f32_e32 v152, v153, v152
	v_div_scale_f32 v153, vcc, 1.0, v150, 1.0
	v_mul_f32_e32 v162, v153, v152
	v_fma_f32 v163, -v151, v162, v153
	v_fmac_f32_e32 v162, v163, v152
	v_fma_f32 v151, -v151, v162, v153
	v_div_fmas_f32 v151, v151, v152, v162
	v_div_fixup_f32 v162, v151, v150, 1.0
	v_pk_mul_f32 v[152:153], v[6:7], v[162:163] op_sel_hi:[1,0]
	v_pk_mul_f32 v[150:151], v[8:9], v[162:163] op_sel_hi:[1,0]
	v_pk_mul_f32 v[152:153], v[158:159], v[152:153]
	v_pk_mul_f32 v[150:151], v[160:161], v[150:151]
	v_pk_mul_f32 v[158:159], v[2:3], v[162:163] op_sel_hi:[1,0]
	v_pk_mul_f32 v[160:161], v[4:5], v[162:163] op_sel_hi:[1,0]
	v_pk_mul_f32 v[154:155], v[154:155], v[158:159]
	v_pk_mul_f32 v[156:157], v[156:157], v[160:161]
	s_and_b64 vcc, exec, s[4:5]
	s_cbranch_vccnz .LBB0_213
	ds_bpermute_b32 v158, v243, v152
	ds_bpermute_b32 v159, v243, v153
	ds_bpermute_b32 v162, v243, v150
	ds_bpermute_b32 v163, v243, v151
	ds_bpermute_b32 v160, v243, v154
	ds_bpermute_b32 v161, v243, v155
	ds_bpermute_b32 v164, v243, v156
	ds_bpermute_b32 v165, v243, v157
	s_waitcnt lgkmcnt(6)
	v_pk_mul_f32 v[142:143], v[142:143], v[158:159]
	s_waitcnt lgkmcnt(4)
	v_pk_mul_f32 v[146:147], v[146:147], v[162:163]
	s_waitcnt vmcnt(5)
	v_pk_fma_f32 v[152:153], v[134:135], v[152:153], v[142:143]
	v_pk_fma_f32 v[150:151], v[136:137], v[150:151], v[146:147]
	s_waitcnt lgkmcnt(2)
	v_pk_mul_f32 v[134:135], v[144:145], v[160:161]
	s_waitcnt lgkmcnt(0)
	v_pk_mul_f32 v[136:137], v[138:139], v[164:165]
	v_pk_fma_f32 v[154:155], v[130:131], v[154:155], v[134:135]
	v_pk_fma_f32 v[156:157], v[132:133], v[156:157], v[136:137]
.LBB0_213:
	s_waitcnt vmcnt(6)
	v_pk_mul_f32 v[132:133], v[148:149], v[150:151]
	v_pk_mul_f32 v[130:131], v[194:195], v[152:153]
	s_waitcnt vmcnt(5)
	v_pk_mul_f32 v[134:135], v[148:149], v[156:157]
	v_pk_mul_f32 v[136:137], v[194:195], v[154:155]
	v_cvt_pk_bf16_f32 v130, v130, v131
	v_cvt_pk_bf16_f32 v131, v132, v133
	v_cvt_pk_bf16_f32 v133, v134, v135
	v_add_co_u32_e32 v134, vcc, 0x400000, v140
	v_cvt_pk_bf16_f32 v132, v136, v137
	s_nop 0
	v_addc_co_u32_e32 v135, vcc, 0, v141, vcc
	global_store_dwordx4 v[134:135], v[130:133], off nt
	s_branch .LBB0_120
.LBB0_214:
	s_lshl_b32 s0, s36, 8
	s_or_b32 s0, s0, s61
	v_add_u32_e32 v130, s0, v192
	s_lshl_b32 s0, s36, 1
	s_and_b32 s8, s0, 6
	s_ashr_i32 s0, s33, 11
	s_and_b32 s0, s0, -8
	s_or_b32 s0, s8, s0
	s_ashr_i32 s1, s0, 31
	s_lshl_b64 s[0:1], s[0:1], 22
	s_add_u32 s4, s34, s0
	s_addc_u32 s5, s35, s1
	s_lshl_b32 s72, s61, 1
	v_lshlrev_b32_e32 v136, 8, v242
	s_cmp_lt_u32 s36, 12
	v_and_b32_e32 v186, 0x3fcf00, v136
	v_ashrrev_i32_e32 v131, 31, v130
	v_ashrrev_i32_e32 v193, 31, v192
	v_mov_b64_e32 v[132:133], s[20:21]
	v_lshl_add_u64 v[136:137], s[4:5], 0, v[186:187]
	s_cselect_b64 vcc, -1, 0
	v_mad_i64_i32 v[134:135], s[0:1], v242, s87, v[132:133]
	v_lshlrev_b64 v[130:131], 1, v[130:131]
	v_lshl_add_u64 v[136:137], v[136:137], 0, s[72:73]
	v_lshlrev_b64 v[138:139], 1, v[192:193]
	s_and_b64 s[0:1], vcc, exec
	v_lshl_add_u64 v[134:135], v[134:135], 0, v[130:131]
	v_lshl_add_u64 v[136:137], v[136:137], 0, v[138:139]
	s_mov_b32 s0, 0x400000
	v_cndmask_b32_e32 v135, v135, v137, vcc
	s_cselect_b32 s0, s0, 0x100
	s_mov_b32 s1, s73
	v_cndmask_b32_e32 v134, v134, v136, vcc
	v_cvt_pk_bf16_f32 v114, v114, v115
	v_cvt_pk_bf16_f32 v115, v116, v117
	v_cvt_pk_bf16_f32 v116, v106, v107
	v_cvt_pk_bf16_f32 v117, v108, v109
	v_lshl_add_u64 v[106:107], v[134:135], 0, s[0:1]
	v_or_b32_e32 v108, 16, v242
	global_store_dwordx4 v[106:107], v[114:117], off nt
	v_mad_i64_i32 v[106:107], s[6:7], v108, s87, v[132:133]
	v_lshlrev_b32_e32 v108, 8, v108
	v_and_b32_e32 v186, 0x3fdf00, v108
	v_lshl_add_u64 v[108:109], s[4:5], 0, v[186:187]
; DI unsigned cvtpk(float lo, float hi) { f32x2 v = {lo, hi}; bf16x2_t b = __builtin_convertvector(v, bf16x2_t); return __builtin_bit_cast(unsigned, b); }
;     DI void operator()(const f32x4 (&acc)[2][2][4][2], const Unit& u, int wr, int wc, int fr, int fq, const LAS unsigned char* st) const {
;     ...
;         if (u.pn >= 8) {
; #pragma unroll
;             for (int ai = 0; ai < 2; ++ai)
; #pragma unroll
;                 for (int m = 0; m < 4; ++m) { const int row = row0 + ai * HALF + m * 16; bf16* rowp = O + (size_t)row * ldc + col0;
;                     if (u.pn < 12) rowp = HM + 2 * HM_PLANE + ((size_t)((row >> 14) * 8 + ((2 * u.pn) & 7)) * SEQ + (row & (SEQ - 1))) * 128 + wc * 32 + 8 * fq;
; #pragma unroll
;                     for (int bj = 0; bj < 2; ++bj) { const f32x4 v0 = acc[ai][bj][m][0], v1 = acc[ai][bj][m][1];
;                         u32x4 w; w.x = cvtpk(v0[0], v0[1]); w.y = cvtpk(v0[2], v0[3]); w.z = cvtpk(v1[0], v1[1]); w.w = cvtpk(v1[2], v1[3]);
;                         *(u32x4*)(rowp + (u.pn < 12 ? (size_t)bj * SEQ * 128 : (size_t)bj * HALF)) = w; } }
;             return;
	v_lshl_add_u64 v[108:109], v[108:109], 0, s[72:73]
	v_lshl_add_u64 v[106:107], v[106:107], 0, v[130:131]
	v_lshl_add_u64 v[108:109], v[108:109], 0, v[138:139]
	v_cndmask_b32_e32 v115, v107, v109, vcc
	v_cndmask_b32_e32 v114, v106, v108, vcc
	v_cvt_pk_bf16_f32 v126, v126, v127
	v_cvt_pk_bf16_f32 v127, v128, v129
	v_cvt_pk_bf16_f32 v128, v122, v123
	v_cvt_pk_bf16_f32 v129, v124, v125
	v_cvt_pk_bf16_f32 v98, v98, v99
	v_cvt_pk_bf16_f32 v99, v100, v101
	v_cvt_pk_bf16_f32 v100, v90, v91
	v_cvt_pk_bf16_f32 v101, v92, v93
	v_lshl_add_u64 v[90:91], v[114:115], 0, s[0:1]
	v_or_b32_e32 v92, 32, v242
	global_store_dwordx4 v[134:135], v[126:129], off nt
	global_store_dwordx4 v[90:91], v[98:101], off nt
	v_mad_i64_i32 v[90:91], s[6:7], v92, s87, v[132:133]
	v_lshlrev_b32_e32 v92, 8, v92
	v_and_b32_e32 v186, 0x3fef00, v92
	v_lshl_add_u64 v[92:93], s[4:5], 0, v[186:187]
	v_lshl_add_u64 v[92:93], v[92:93], 0, s[72:73]
	v_lshl_add_u64 v[90:91], v[90:91], 0, v[130:131]
	v_lshl_add_u64 v[92:93], v[92:93], 0, v[138:139]
	v_cndmask_b32_e32 v99, v91, v93, vcc
	v_cndmask_b32_e32 v98, v90, v92, vcc
	v_cvt_pk_bf16_f32 v106, v118, v119
	v_cvt_pk_bf16_f32 v107, v120, v121
	v_cvt_pk_bf16_f32 v108, v110, v111
	v_cvt_pk_bf16_f32 v109, v112, v113
	v_cvt_pk_bf16_f32 v82, v82, v83
	v_cvt_pk_bf16_f32 v83, v84, v85
	v_cvt_pk_bf16_f32 v84, v74, v75
	v_cvt_pk_bf16_f32 v85, v76, v77
	v_lshl_add_u64 v[74:75], v[98:99], 0, s[0:1]
	v_or_b32_e32 v76, 48, v242
	global_store_dwordx4 v[114:115], v[106:109], off nt
	global_store_dwordx4 v[74:75], v[82:85], off nt
	v_mad_i64_i32 v[74:75], s[6:7], v76, s87, v[132:133]
	v_lshlrev_b32_e32 v76, 8, v76
	v_and_b32_e32 v186, 0x3fff00, v76
	v_lshl_add_u64 v[76:77], s[4:5], 0, v[186:187]
	v_lshl_add_u64 v[76:77], v[76:77], 0, s[72:73]
	v_lshl_add_u64 v[74:75], v[74:75], 0, v[130:131]
	v_lshl_add_u64 v[76:77], v[76:77], 0, v[138:139]
	v_cndmask_b32_e32 v83, v75, v77, vcc
	v_cndmask_b32_e32 v82, v74, v76, vcc
	v_cvt_pk_bf16_f32 v90, v102, v103
	v_cvt_pk_bf16_f32 v91, v104, v105
	v_cvt_pk_bf16_f32 v92, v94, v95
	v_cvt_pk_bf16_f32 v93, v96, v97
	v_cvt_pk_bf16_f32 v70, v70, v71
	v_cvt_pk_bf16_f32 v71, v72, v73
	v_cvt_pk_bf16_f32 v72, v66, v67
	v_cvt_pk_bf16_f32 v73, v68, v69
	v_lshl_add_u64 v[66:67], v[82:83], 0, s[0:1]
	global_store_dwordx4 v[98:99], v[90:93], off nt
	global_store_dwordx4 v[66:67], v[70:73], off nt
	v_cvt_pk_bf16_f32 v74, v86, v87
	v_cvt_pk_bf16_f32 v75, v88, v89
	v_add_u32_e32 v70, 0x80, v242
	v_ashrrev_i32_e32 v66, 11, v70
	v_and_or_b32 v66, v66, -8, s8
	v_ashrrev_i32_e32 v67, 31, v66
	v_lshlrev_b64 v[66:67], 22, v[66:67]
	v_mad_i64_i32 v[68:69], s[4:5], v70, s87, v[132:133]
	v_lshlrev_b32_e32 v70, 8, v70
	v_lshl_add_u64 v[66:67], s[34:35], 0, v[66:67]
	v_and_b32_e32 v186, 0x3fcf00, v70
	v_lshl_add_u64 v[70:71], v[66:67], 0, v[186:187]
	v_lshl_add_u64 v[70:71], v[70:71], 0, s[72:73]
	v_lshl_add_u64 v[68:69], v[68:69], 0, v[130:131]
	v_lshl_add_u64 v[70:71], v[70:71], 0, v[138:139]
	v_cndmask_b32_e32 v69, v69, v71, vcc
	v_cndmask_b32_e32 v68, v68, v70, vcc
	v_cvt_pk_bf16_f32 v76, v78, v79
	v_cvt_pk_bf16_f32 v77, v80, v81
	v_cvt_pk_bf16_f32 v50, v50, v51
	v_cvt_pk_bf16_f32 v51, v52, v53
	v_cvt_pk_bf16_f32 v52, v42, v43
	v_cvt_pk_bf16_f32 v53, v44, v45
	v_lshl_add_u64 v[42:43], v[68:69], 0, s[0:1]
	v_add_u32_e32 v44, 0x90, v242
	global_store_dwordx4 v[82:83], v[74:77], off nt
	global_store_dwordx4 v[42:43], v[50:53], off nt
	v_mad_i64_i32 v[42:43], s[4:5], v44, s87, v[132:133]
	v_lshlrev_b32_e32 v44, 8, v44
	v_and_b32_e32 v186, 0x3fdf00, v44
	v_lshl_add_u64 v[44:45], v[66:67], 0, v[186:187]
	v_lshl_add_u64 v[44:45], v[44:45], 0, s[72:73]
	v_lshl_add_u64 v[42:43], v[42:43], 0, v[130:131]
	v_lshl_add_u64 v[44:45], v[44:45], 0, v[138:139]
	v_cndmask_b32_e32 v51, v43, v45, vcc
	v_cndmask_b32_e32 v50, v42, v44, vcc
	v_cvt_pk_bf16_f32 v62, v62, v63
	v_cvt_pk_bf16_f32 v63, v64, v65
	v_cvt_pk_bf16_f32 v64, v58, v59
	v_cvt_pk_bf16_f32 v65, v60, v61
	v_cvt_pk_bf16_f32 v34, v34, v35
	v_cvt_pk_bf16_f32 v35, v36, v37
	v_cvt_pk_bf16_f32 v36, v26, v27
	v_cvt_pk_bf16_f32 v37, v28, v29
	v_lshl_add_u64 v[26:27], v[50:51], 0, s[0:1]
	v_add_u32_e32 v28, 0xa0, v242
	global_store_dwordx4 v[68:69], v[62:65], off nt
	global_store_dwordx4 v[26:27], v[34:37], off nt
	v_mad_i64_i32 v[26:27], s[4:5], v28, s87, v[132:133]
	v_lshlrev_b32_e32 v28, 8, v28
	v_and_b32_e32 v186, 0x3fef00, v28
	v_lshl_add_u64 v[28:29], v[66:67], 0, v[186:187]
	v_lshl_add_u64 v[28:29], v[28:29], 0, s[72:73]
	v_lshl_add_u64 v[26:27], v[26:27], 0, v[130:131]
	v_lshl_add_u64 v[28:29], v[28:29], 0, v[138:139]
	v_cndmask_b32_e32 v35, v27, v29, vcc
	v_cndmask_b32_e32 v34, v26, v28, vcc
	v_cvt_pk_bf16_f32 v42, v54, v55
	v_cvt_pk_bf16_f32 v43, v56, v57
	v_cvt_pk_bf16_f32 v44, v46, v47
	v_cvt_pk_bf16_f32 v45, v48, v49
	v_cvt_pk_bf16_f32 v18, v18, v19
	v_cvt_pk_bf16_f32 v19, v20, v21
	v_cvt_pk_bf16_f32 v20, v10, v11
	v_cvt_pk_bf16_f32 v21, v12, v13
	v_lshl_add_u64 v[10:11], v[34:35], 0, s[0:1]
	v_add_u32_e32 v12, 0xb0, v242
	global_store_dwordx4 v[50:51], v[42:45], off nt
	global_store_dwordx4 v[10:11], v[18:21], off nt
	v_mad_i64_i32 v[10:11], s[4:5], v12, s87, v[132:133]
	v_lshlrev_b32_e32 v12, 8, v12
	v_and_b32_e32 v186, 0x3fff00, v12
	v_lshl_add_u64 v[12:13], v[66:67], 0, v[186:187]
	v_lshl_add_u64 v[12:13], v[12:13], 0, s[72:73]
	v_lshl_add_u64 v[10:11], v[10:11], 0, v[130:131]
	v_lshl_add_u64 v[12:13], v[12:13], 0, v[138:139]
	v_cndmask_b32_e32 v19, v11, v13, vcc
	v_cndmask_b32_e32 v18, v10, v12, vcc
	v_cvt_pk_bf16_f32 v26, v38, v39
	v_cvt_pk_bf16_f32 v27, v40, v41
	v_cvt_pk_bf16_f32 v28, v30, v31
	v_cvt_pk_bf16_f32 v29, v32, v33
	v_cvt_pk_bf16_f32 v10, v22, v23
	v_cvt_pk_bf16_f32 v11, v24, v25
	v_cvt_pk_bf16_f32 v12, v14, v15
	v_cvt_pk_bf16_f32 v13, v16, v17
	v_cvt_pk_bf16_f32 v6, v6, v7
	v_cvt_pk_bf16_f32 v7, v8, v9
	v_cvt_pk_bf16_f32 v8, v2, v3
	v_cvt_pk_bf16_f32 v9, v4, v5
	v_lshl_add_u64 v[2:3], v[18:19], 0, s[0:1]
	global_store_dwordx4 v[34:35], v[26:29], off nt
	global_store_dwordx4 v[18:19], v[10:13], off nt
	global_store_dwordx4 v[2:3], v[6:9], off nt
	s_andn2_b64 vcc, exec, s[2:3]
	s_mov_b64 s[0:1], -1
	s_cbranch_vccnz .LBB0_111

; #define EPS_LOAD(g_) do { const size_t off_ = (size_t)(row0 + ((g_) >> 2) * HALF + ((g_) & 3) * 16) * ldc + col0; \
;             _Pragma("unroll") for (int bj = 0; bj < 2; ++bj) _Pragma("unroll") for (int n = 0; n < 2; ++n) rb[(g_) & 3][2 * bj + n] = *(const f32x4*)(base + off_ + bj * HALF + n * 16); } while (0)
;     DI void operator()(const f32x4 (&acc)[2][2][4][2], const Unit& u, int wr, int wc, int fr, int fq, const LAS unsigned char* st) const {
;         const int row0 = u.pm * BM + wr * 64 + fr, col0 = u.pn * BM + wc * 32 + 4 * fq;
;         f32x4 rb[4][4];
;     ...
;         EPS_LOAD(0); EPS_LOAD(1); EPS_LOAD(2);
; #pragma unroll
;         for (int ai = 0; ai < 2; ++ai)
; #pragma unroll
;             for (int m = 0; m < 4; ++m) { const int g = 4 * ai + m; const size_t off = (size_t)(row0 + ai * HALF + m * 16) * ldc + col0;
;                 if (g + 3 < 8) EPS_LOAD(g + 3);
; #pragma unroll
;                 for (int bj = 0; bj < 2; ++bj)
; #pragma unroll
;                     for (int n = 0; n < 2; ++n) *(f32x4*)(C + off + bj * HALF + n * 16) = rb[g & 3][2 * bj + n] + acc[ai][bj][m][n]; }
.LBB0_796:
	v_mov_b32_e32 v130, v224
	s_lshl_b32 s0, s28, 8
	s_add_i32 s0, s0, s45
	v_and_or_b32 v140, v130, 15, s0
	s_lshl_b32 s0, s54, 8
	v_ashrrev_i32_e32 v130, 2, v130
	s_or_b32 s0, s0, s46
	v_and_b32_e32 v130, -4, v130
	v_add_u32_e32 v136, s0, v130
	v_ashrrev_i32_e32 v141, 31, v140
	v_readlane_b32 s0, v254, 3
	v_or_b32_e32 v168, 16, v140
	v_or_b32_e32 v184, 32, v140
	v_ashrrev_i32_e32 v137, 31, v136
	v_lshlrev_b64 v[138:139], 13, v[140:141]
	v_readlane_b32 s1, v254, 4
	v_ashrrev_i32_e32 v169, 31, v168
	v_ashrrev_i32_e32 v185, 31, v184
	v_lshl_add_u64 v[152:153], s[0:1], 0, v[138:139]
	v_lshlrev_b64 v[136:137], 2, v[136:137]
	v_lshlrev_b64 v[216:217], 13, v[168:169]
	v_lshlrev_b64 v[218:219], 13, v[184:185]
	v_lshl_add_u64 v[164:165], v[152:153], 0, v[136:137]
	v_lshl_add_u64 v[168:169], s[0:1], 0, v[216:217]
	v_lshl_add_u64 v[184:185], s[0:1], 0, v[218:219]
	global_load_dwordx4 v[152:155], v[164:165], off nt
	global_load_dwordx4 v[156:159], v[164:165], off offset:64 nt
	global_load_dwordx4 v[160:163], v[164:165], off offset:512 nt
	s_nop 0
	global_load_dwordx4 v[164:167], v[164:165], off offset:576 nt
	v_lshl_add_u64 v[180:181], v[168:169], 0, v[136:137]
	v_lshl_add_u64 v[196:197], v[184:185], 0, v[136:137]
	global_load_dwordx4 v[168:171], v[180:181], off nt
	global_load_dwordx4 v[172:175], v[180:181], off offset:64 nt
	global_load_dwordx4 v[176:179], v[180:181], off offset:512 nt
	s_nop 0
	global_load_dwordx4 v[180:183], v[180:181], off offset:576 nt
	s_nop 0
	global_load_dwordx4 v[184:187], v[196:197], off nt
	global_load_dwordx4 v[188:191], v[196:197], off offset:64 nt
	global_load_dwordx4 v[192:195], v[196:197], off offset:512 nt
	s_nop 0
	global_load_dwordx4 v[196:199], v[196:197], off offset:576 nt
	v_or_b32_e32 v200, 48, v140
	v_ashrrev_i32_e32 v201, 31, v200
	v_lshlrev_b64 v[220:221], 13, v[200:201]
	v_lshl_add_u64 v[200:201], s[0:1], 0, v[220:221]
	v_lshl_add_u64 v[212:213], v[200:201], 0, v[136:137]
	global_load_dwordx4 v[200:203], v[212:213], off nt
	global_load_dwordx4 v[204:207], v[212:213], off offset:64 nt
	global_load_dwordx4 v[208:211], v[212:213], off offset:512 nt
	s_nop 0
	global_load_dwordx4 v[212:215], v[212:213], off offset:576 nt
	v_lshl_add_u64 v[222:223], s[92:93], 0, v[138:139]
	v_lshl_add_u64 v[226:227], v[138:139], 0, s[74:75]
	v_lshl_add_u64 v[228:229], v[138:139], 0, s[76:77]
	v_lshl_add_u64 v[230:231], s[0:1], 0, v[226:227]
	v_lshl_add_u64 v[216:217], s[92:93], 0, v[216:217]
	v_lshl_add_u64 v[138:139], v[222:223], 0, v[136:137]
	v_lshl_add_u64 v[232:233], s[0:1], 0, v[228:229]
	v_lshl_add_u64 v[218:219], s[92:93], 0, v[218:219]
	v_lshl_add_u64 v[222:223], v[230:231], 0, v[136:137]
	v_lshl_add_u64 v[216:217], v[216:217], 0, v[136:137]
	v_lshl_add_u64 v[230:231], v[232:233], 0, v[136:137]
	v_readlane_b32 s2, v254, 5
	v_readlane_b32 s3, v254, 6
	v_readlane_b32 s4, v254, 7
	v_readlane_b32 s5, v254, 8
	v_readlane_b32 s6, v254, 9
	v_readlane_b32 s7, v254, 10
	v_readlane_b32 s8, v254, 11
	v_readlane_b32 s9, v254, 12
	v_readlane_b32 s10, v254, 13
	v_readlane_b32 s11, v254, 14
	v_readlane_b32 s12, v254, 15
	v_readlane_b32 s13, v254, 16
	v_readlane_b32 s14, v254, 17
	v_readlane_b32 s15, v254, 18
	s_waitcnt vmcnt(0)
	v_pk_add_f32 v[128:129], v[128:129], v[154:155]
	v_pk_add_f32 v[126:127], v[126:127], v[152:153]
	v_pk_add_f32 v[124:125], v[124:125], v[158:159]
	v_pk_add_f32 v[122:123], v[122:123], v[156:157]
	v_pk_add_f32 v[108:109], v[108:109], v[162:163]
	v_pk_add_f32 v[106:107], v[106:107], v[160:161]
	v_pk_add_f32 v[104:105], v[104:105], v[166:167]
	v_pk_add_f32 v[102:103], v[102:103], v[164:165]
	v_pk_add_f32 v[120:121], v[120:121], v[170:171]
	v_pk_add_f32 v[118:119], v[118:119], v[168:169]
	global_store_dwordx4 v[138:139], v[126:129], off nt
	global_store_dwordx4 v[138:139], v[122:125], off offset:64 nt
	global_store_dwordx4 v[138:139], v[106:109], off offset:512 nt
	global_store_dwordx4 v[138:139], v[102:105], off offset:576 nt
	v_pk_add_f32 v[116:117], v[116:117], v[174:175]
	v_pk_add_f32 v[114:115], v[114:115], v[172:173]
	v_pk_add_f32 v[100:101], v[100:101], v[178:179]
	v_pk_add_f32 v[98:99], v[98:99], v[176:177]
	v_pk_add_f32 v[96:97], v[96:97], v[182:183]
	v_pk_add_f32 v[94:95], v[94:95], v[180:181]
	global_load_dwordx4 v[102:105], v[222:223], off nt
	global_load_dwordx4 v[106:109], v[222:223], off offset:64 nt
	global_load_dwordx4 v[122:125], v[222:223], off offset:512 nt
	global_load_dwordx4 v[126:129], v[222:223], off offset:576 nt
	s_nop 0
	global_store_dwordx4 v[216:217], v[118:121], off nt
	global_store_dwordx4 v[216:217], v[114:117], off offset:64 nt
	global_store_dwordx4 v[216:217], v[98:101], off offset:512 nt
	global_store_dwordx4 v[216:217], v[94:97], off offset:576 nt
	v_lshl_add_u64 v[152:153], v[218:219], 0, v[136:137]
	v_pk_add_f32 v[80:81], v[80:81], v[198:199]
	v_pk_add_f32 v[78:79], v[78:79], v[196:197]
	global_load_dwordx4 v[94:97], v[230:231], off nt
	global_load_dwordx4 v[98:101], v[230:231], off offset:64 nt
	global_load_dwordx4 v[114:117], v[230:231], off offset:512 nt
	global_load_dwordx4 v[118:121], v[230:231], off offset:576 nt
	v_pk_add_f32 v[112:113], v[112:113], v[186:187]
	global_store_dwordx4 v[152:153], v[78:81], off offset:576 nt
; #define LAS __attribute__((address_space(3)))
; #define EPS_LOAD(g_) do { const size_t off_ = (size_t)(row0 + ((g_) >> 2) * HALF + ((g_) & 3) * 16) * ldc + col0; \
;             _Pragma("unroll") for (int bj = 0; bj < 2; ++bj) _Pragma("unroll") for (int n = 0; n < 2; ++n) rb[(g_) & 3][2 * bj + n] = *(const f32x4*)(base + off_ + bj * HALF + n * 16); } while (0)
;     DI void operator()(const f32x4 (&acc)[2][2][4][2], const Unit& u, int wr, int wc, int fr, int fq, const LAS unsigned char* st) const {
;         const int row0 = u.pm * BM + wr * 64 + fr, col0 = u.pn * BM + wc * 32 + 4 * fq;
;         f32x4 rb[4][4];
;     ...
;         EPS_LOAD(0); EPS_LOAD(1); EPS_LOAD(2);
; #pragma unroll
;         for (int ai = 0; ai < 2; ++ai)
; #pragma unroll
;             for (int m = 0; m < 4; ++m) { const int g = 4 * ai + m; const size_t off = (size_t)(row0 + ai * HALF + m * 16) * ldc + col0;
;                 if (g + 3 < 8) EPS_LOAD(g + 3);
; #pragma unroll
;                 for (int bj = 0; bj < 2; ++bj)
; #pragma unroll
;                     for (int n = 0; n < 2; ++n) *(f32x4*)(C + off + bj * HALF + n * 16) = rb[g & 3][2 * bj + n] + acc[ai][bj][m][n]; }
	v_pk_add_f32 v[110:111], v[110:111], v[184:185]
	v_pk_add_f32 v[92:93], v[92:93], v[190:191]
	v_add_u32_e32 v78, 0xa0, v140
	v_ashrrev_i32_e32 v79, 31, v78
	v_pk_add_f32 v[90:91], v[90:91], v[188:189]
	v_pk_add_f32 v[88:89], v[88:89], v[194:195]
	v_pk_add_f32 v[86:87], v[86:87], v[192:193]
	v_lshlrev_b64 v[78:79], 13, v[78:79]
	global_store_dwordx4 v[152:153], v[110:113], off nt
	global_store_dwordx4 v[152:153], v[90:93], off offset:64 nt
	global_store_dwordx4 v[152:153], v[86:89], off offset:512 nt
	v_lshl_add_u64 v[78:79], s[0:1], 0, v[78:79]
	v_lshl_add_u64 v[152:153], s[92:93], 0, v[220:221]
	v_lshl_add_u64 v[110:111], v[78:79], 0, v[136:137]
	v_lshl_add_u64 v[152:153], v[152:153], 0, v[136:137]
	v_pk_add_f32 v[68:69], v[68:69], v[214:215]
	v_pk_add_f32 v[66:67], v[66:67], v[212:213]
	global_load_dwordx4 v[78:81], v[110:111], off nt
	global_load_dwordx4 v[86:89], v[110:111], off offset:64 nt
	global_load_dwordx4 v[90:93], v[110:111], off offset:512 nt
	s_nop 0
	global_load_dwordx4 v[110:113], v[110:111], off offset:576 nt
	v_pk_add_f32 v[84:85], v[84:85], v[202:203]
	global_store_dwordx4 v[152:153], v[66:69], off offset:576 nt
	v_pk_add_f32 v[82:83], v[82:83], v[200:201]
	v_pk_add_f32 v[76:77], v[76:77], v[206:207]
	v_add_u32_e32 v66, 0xb0, v140
	v_ashrrev_i32_e32 v67, 31, v66
	v_lshlrev_b64 v[66:67], 13, v[66:67]
	v_pk_add_f32 v[74:75], v[74:75], v[204:205]
	v_pk_add_f32 v[72:73], v[72:73], v[210:211]
	v_pk_add_f32 v[70:71], v[70:71], v[208:209]
	v_lshl_add_u64 v[66:67], s[0:1], 0, v[66:67]
	global_store_dwordx4 v[152:153], v[82:85], off nt
	global_store_dwordx4 v[152:153], v[74:77], off offset:64 nt
	global_store_dwordx4 v[152:153], v[70:73], off offset:512 nt
	v_lshl_add_u64 v[82:83], v[66:67], 0, v[136:137]
	global_load_dwordx4 v[66:69], v[82:83], off nt
	global_load_dwordx4 v[70:73], v[82:83], off offset:64 nt
	global_load_dwordx4 v[74:77], v[82:83], off offset:512 nt
	s_nop 0
	global_load_dwordx4 v[82:85], v[82:83], off offset:576 nt
	v_lshl_add_u64 v[140:141], s[92:93], 0, v[226:227]
	v_lshl_add_u64 v[152:153], s[92:93], 0, v[228:229]
	v_lshl_add_u64 v[140:141], v[140:141], 0, v[136:137]
	v_lshl_add_u64 v[136:137], v[152:153], 0, v[136:137]
	v_add_co_u32_e32 v154, vcc, s52, v138
	v_lshl_add_u64 v[152:153], v[138:139], 0, s[16:17]
	s_nop 0
	v_addc_co_u32_e32 v155, vcc, 0, v139, vcc
	s_mov_b64 s[0:1], -1
	s_waitcnt vmcnt(27)
	v_pk_add_f32 v[64:65], v[64:65], v[104:105]
	v_pk_add_f32 v[62:63], v[62:63], v[102:103]
	s_waitcnt vmcnt(26)
	v_pk_add_f32 v[60:61], v[60:61], v[108:109]
	s_waitcnt vmcnt(24)
	v_pk_add_f32 v[40:41], v[40:41], v[128:129]
	v_pk_add_f32 v[38:39], v[38:39], v[126:127]
	v_pk_add_f32 v[58:59], v[58:59], v[106:107]
	v_pk_add_f32 v[48:49], v[48:49], v[124:125]
	v_pk_add_f32 v[46:47], v[46:47], v[122:123]
	global_store_dwordx4 v[140:141], v[62:65], off nt
	global_store_dwordx4 v[140:141], v[58:61], off offset:64 nt
	global_store_dwordx4 v[140:141], v[46:49], off offset:512 nt
	global_store_dwordx4 v[140:141], v[38:41], off offset:576 nt
	s_waitcnt vmcnt(20)
	v_pk_add_f32 v[28:29], v[28:29], v[120:121]
	v_pk_add_f32 v[26:27], v[26:27], v[118:119]
	v_pk_add_f32 v[40:41], v[56:57], v[96:97]
	v_pk_add_f32 v[38:39], v[54:55], v[94:95]
	v_pk_add_f32 v[48:49], v[52:53], v[100:101]
	v_pk_add_f32 v[46:47], v[50:51], v[98:99]
	v_pk_add_f32 v[32:33], v[32:33], v[116:117]
	v_pk_add_f32 v[30:31], v[30:31], v[114:115]
	global_store_dwordx4 v[136:137], v[38:41], off nt
	global_store_dwordx4 v[136:137], v[46:49], off offset:64 nt
	global_store_dwordx4 v[136:137], v[30:33], off offset:512 nt
	global_store_dwordx4 v[136:137], v[26:29], off offset:576 nt
	s_waitcnt vmcnt(17)
	v_pk_add_f32 v[20:21], v[20:21], v[92:93]
	v_pk_add_f32 v[28:29], v[44:45], v[80:81]
	v_pk_add_f32 v[26:27], v[42:43], v[78:79]
	v_pk_add_f32 v[18:19], v[18:19], v[90:91]
	v_pk_add_f32 v[32:33], v[36:37], v[88:89]
	v_pk_add_f32 v[30:31], v[34:35], v[86:87]
	global_store_dwordx4 v[154:155], v[26:29], off nt
	global_store_dwordx4 v[152:153], v[30:33], off offset:64 nt
	global_store_dwordx4 v[152:153], v[18:21], off offset:512 nt
	s_waitcnt vmcnt(19)
	v_pk_add_f32 v[16:17], v[16:17], v[112:113]
	v_pk_add_f32 v[14:15], v[14:15], v[110:111]
	v_add_co_u32_e32 v20, vcc, s53, v138
	global_store_dwordx4 v[152:153], v[14:17], off offset:576 nt
	s_nop 0
	v_addc_co_u32_e32 v21, vcc, 0, v139, vcc
	s_waitcnt vmcnt(15)
	v_pk_add_f32 v[16:17], v[24:25], v[68:69]
	v_pk_add_f32 v[14:15], v[22:23], v[66:67]
	v_lshl_add_u64 v[18:19], v[138:139], 0, s[18:19]
	s_waitcnt vmcnt(14)
	v_pk_add_f32 v[12:13], v[12:13], v[72:73]
	v_pk_add_f32 v[10:11], v[10:11], v[70:71]
	s_waitcnt vmcnt(13)
	v_pk_add_f32 v[8:9], v[8:9], v[76:77]
	v_pk_add_f32 v[6:7], v[6:7], v[74:75]
	s_waitcnt vmcnt(12)
	v_pk_add_f32 v[4:5], v[4:5], v[84:85]
	v_pk_add_f32 v[2:3], v[2:3], v[82:83]
	s_andn2_b64 vcc, exec, s[60:61]
	global_store_dwordx4 v[20:21], v[14:17], off nt
	global_store_dwordx4 v[18:19], v[10:13], off offset:64 nt
	global_store_dwordx4 v[18:19], v[6:9], off offset:512 nt
	global_store_dwordx4 v[18:19], v[2:5], off offset:576 nt
	s_cbranch_vccnz .LBB0_785
	s_andn2_b64 vcc, exec, s[64:65]
	s_cbranch_vccnz .LBB0_784
	s_barrier
	s_branch .LBB0_784

; #define LAS __attribute__((address_space(3)))
; DI unsigned pk4_fp8n(float a, float b, float c, float d) { int v = __builtin_amdgcn_cvt_pk_fp8_f32(a, b, 0, false); v = __builtin_amdgcn_cvt_pk_fp8_f32(c, d, v, true); return (unsigned)v; }
;     DI void operator()(const f32x4 (&acc)[2][2][4][2], const Unit& u, int wr, int wc, int fr, int fq, const LAS unsigned char* st) const {
;         const int row0 = u.pm * BM + wr * 64 + fr, f0 = u.pn * HALF + wc * 32 + 8 * fq;
;         f32x2 bg[4], bl[4];
;         { const LAS float* sb = (const LAS float*)(st + 512 + fq * 64);
; #pragma unroll
;           for (int p = 0; p < 4; ++p) { bg[p][0] = sb[4 * p]; bg[p][1] = sb[4 * p + 2]; bl[p][0] = sb[4 * p + 1]; bl[p][1] = sb[4 * p + 3]; } }
; #pragma unroll
;         for (int ai = 0; ai < 2; ++ai)
; #pragma unroll
;             for (int mp = 0; mp < 2; ++mp) {
;                 u32x2 w2[2];
; #pragma unroll
;                 for (int mm = 0; mm < 2; ++mm) { const int m = 2 * mp + mm; const float ws = *(const LAS float*)(st + ai * 256 + (m * 16 + fr) * 4) * (1.0f / 32.0f);
;                     const f32x4 g0 = acc[ai][0][m][0], g1 = acc[ai][0][m][1], l0 = acc[ai][1][m][0], l1 = acc[ai][1][m][1];
;                     f32x2 ws2; ws2[0] = ws; ws2[1] = ws;
;                     const f32x2 a01 = swiglu4_2(__builtin_shufflevector(g0, g0, 0, 1) * ws2 + bg[0], __builtin_shufflevector(l0, l0, 0, 1) * ws2 + bl[0]);
;                     const f32x2 a23 = swiglu4_2(__builtin_shufflevector(g0, g0, 2, 3) * ws2 + bg[1], __builtin_shufflevector(l0, l0, 2, 3) * ws2 + bl[1]);
;                     const f32x2 a45 = swiglu4_2(__builtin_shufflevector(g1, g1, 0, 1) * ws2 + bg[2], __builtin_shufflevector(l1, l1, 0, 1) * ws2 + bl[2]);
;                     const f32x2 a67 = swiglu4_2(__builtin_shufflevector(g1, g1, 2, 3) * ws2 + bg[3], __builtin_shufflevector(l1, l1, 2, 3) * ws2 + bl[3]);
;                     w2[mm].x = pk4_fp8n(a01[0], a01[1], a23[0], a23[1]); w2[mm].y = pk4_fp8n(a45[0], a45[1], a67[0], a67[1]); }
.LBB0_1091:
	v_mov_b32_e32 v110, v224
	s_lshl_b32 s1, s34, 7
	v_ashrrev_i32_e32 v168, 4, v110
	v_and_b32_e32 v146, 15, v110
	v_lshl_add_u32 v110, v168, 6, s35
	ds_read_b128 v[130:133], v110 offset:512
	ds_read_b128 v[126:129], v110 offset:528
	ds_read_b128 v[118:121], v110 offset:544
	ds_read_b128 v[110:113], v110 offset:560
	s_or_b32 s1, s1, s58
	s_lshl_b32 s0, s33, 8
	s_waitcnt lgkmcnt(0)
	v_mov_b32_e32 v154, v126
	v_lshl_add_u32 v126, v146, 2, s35
	v_mov_b32_e32 v156, v130
	v_mov_b32_e32 v157, v132
	v_mov_b32_e32 v132, v131
	ds_read2_b32 v[130:131], v126 offset1:16
	v_mov_b32_e32 v150, v110
	v_mov_b32_e32 v151, v112
	v_mov_b32_e32 v112, v111
	v_lshl_add_u32 v110, v168, 3, s1
	s_waitcnt lgkmcnt(0)
	v_mul_f32_e32 v130, 0x3d000000, v130
	v_pk_fma_f32 v[142:143], v[142:143], v[130:131], v[156:157] op_sel_hi:[1,0,1]
	v_and_b32_e32 v111, 1, v168
	v_min_f32_e32 v142, 0x40e00000, v142
	v_min_f32_e32 v143, 0x40e00000, v143
	v_pk_mul_f32 v[168:169], v[142:143], s[84:85] op_sel_hi:[1,0]
	v_mov_b32_e32 v155, v128
	v_exp_f32_e32 v168, v168
	v_exp_f32_e32 v169, v169
	v_pk_fma_f32 v[144:145], v[144:145], v[130:131], v[154:155] op_sel_hi:[1,0,1]
	v_pk_fma_f32 v[138:139], v[138:139], v[130:131], v[132:133] op_sel_hi:[1,0,1]
	v_min_f32_e32 v144, 0x40e00000, v144
	v_pk_add_f32 v[168:169], v[168:169], 1.0 op_sel_hi:[1,0]
	v_min_f32_e32 v145, 0x40e00000, v145
	v_rcp_f32_e32 v168, v168
	v_rcp_f32_e32 v169, v169
	v_pk_mul_f32 v[170:171], v[144:145], s[84:85] op_sel_hi:[1,0]
	v_med3_f32 v138, v138, s69, v167
	v_exp_f32_e32 v170, v170
	v_exp_f32_e32 v171, v171
	v_med3_f32 v139, v139, s69, v167
	v_pk_mul_f32 v[142:143], v[142:143], v[168:169]
	v_pk_fma_f32 v[138:139], v[138:139], 4.0, 4.0 op_sel_hi:[1,0,0]
	v_mov_b32_e32 v128, v127
	v_pk_mul_f32 v[138:139], v[138:139], v[142:143]
	v_pk_add_f32 v[142:143], v[170:171], 1.0 op_sel_hi:[1,0]
	v_mov_b32_e32 v152, v118
	v_rcp_f32_e32 v142, v142
	v_rcp_f32_e32 v143, v143
	v_mov_b32_e32 v153, v120
	v_pk_fma_f32 v[140:141], v[140:141], v[130:131], v[128:129] op_sel_hi:[1,0,1]
	v_pk_fma_f32 v[134:135], v[134:135], v[130:131], v[152:153] op_sel_hi:[1,0,1]
	v_med3_f32 v140, v140, s69, v167
	v_med3_f32 v141, v141, s69, v167
	v_pk_mul_f32 v[142:143], v[144:145], v[142:143]
	v_pk_fma_f32 v[140:141], v[140:141], 4.0, 4.0 op_sel_hi:[1,0,0]
	v_min_f32_e32 v134, 0x40e00000, v134
	v_min_f32_e32 v135, 0x40e00000, v135
	v_pk_mul_f32 v[140:141], v[140:141], v[142:143]
	v_pk_mul_f32 v[142:143], v[134:135], s[84:85] op_sel_hi:[1,0]
	v_pk_fma_f32 v[136:137], v[136:137], v[130:131], v[150:151] op_sel_hi:[1,0,1]
	v_exp_f32_e32 v142, v142
	v_exp_f32_e32 v143, v143
	v_min_f32_e32 v136, 0x40e00000, v136
	v_min_f32_e32 v137, 0x40e00000, v137
	v_pk_mul_f32 v[144:145], v[136:137], s[84:85] op_sel_hi:[1,0]
	v_pk_add_f32 v[142:143], v[142:143], 1.0 op_sel_hi:[1,0]
	v_mov_b32_e32 v120, v119
	v_rcp_f32_e32 v142, v142
	v_rcp_f32_e32 v143, v143
	v_exp_f32_e32 v144, v144
	v_exp_f32_e32 v145, v145
	v_pk_fma_f32 v[122:123], v[122:123], v[130:131], v[120:121] op_sel_hi:[1,0,1]
	v_pk_mul_f32 v[134:135], v[134:135], v[142:143]
	v_med3_f32 v122, v122, s69, v167
	v_med3_f32 v123, v123, s69, v167
	v_pk_fma_f32 v[122:123], v[122:123], 4.0, 4.0 op_sel_hi:[1,0,0]
	v_pk_fma_f32 v[124:125], v[124:125], v[130:131], v[112:113] op_sel_hi:[1,0,1]
	v_pk_mul_f32 v[134:135], v[122:123], v[134:135]
	v_pk_add_f32 v[122:123], v[144:145], 1.0 op_sel_hi:[1,0]
	v_med3_f32 v124, v124, s69, v167
	v_rcp_f32_e32 v122, v122
	v_rcp_f32_e32 v123, v123
	v_med3_f32 v125, v125, s69, v167
	v_pk_fma_f32 v[124:125], v[124:125], 4.0, 4.0 op_sel_hi:[1,0,0]
	s_add_i32 s0, s0, s47
	v_pk_mul_f32 v[136:137], v[136:137], v[122:123]
	v_mov_b32_e32 v123, v147
	v_cvt_pk_fp8_f32 v123, v134, v135
	v_pk_mul_f32 v[124:125], v[124:125], v[136:137]
	v_mov_b32_e32 v122, v147
	v_cvt_pk_fp8_f32 v122, v138, v139
	v_cvt_pk_fp8_f32 v123, v124, v125 op_sel:[0,0,1]
	v_mul_f32_e32 v124, 0x3d000000, v131
	v_pk_fma_f32 v[114:115], v[114:115], v[124:125], v[156:157] op_sel_hi:[1,0,1]
	v_pk_fma_f32 v[116:117], v[116:117], v[124:125], v[154:155] op_sel_hi:[1,0,1]
	v_min_f32_e32 v114, 0x40e00000, v114
	v_min_f32_e32 v115, 0x40e00000, v115
	v_pk_mul_f32 v[130:131], v[114:115], s[84:85] op_sel_hi:[1,0]
	v_min_f32_e32 v116, 0x40e00000, v116
	v_exp_f32_e32 v130, v130
	v_exp_f32_e32 v131, v131
	v_min_f32_e32 v117, 0x40e00000, v117
	v_pk_mul_f32 v[134:135], v[116:117], s[84:85] op_sel_hi:[1,0]
	v_pk_fma_f32 v[106:107], v[106:107], v[124:125], v[132:133] op_sel_hi:[1,0,1]
	v_pk_add_f32 v[130:131], v[130:131], 1.0 op_sel_hi:[1,0]
	v_exp_f32_e32 v134, v134
	v_rcp_f32_e32 v130, v130
	v_rcp_f32_e32 v131, v131
	v_exp_f32_e32 v135, v135
	v_med3_f32 v106, v106, s69, v167
	v_med3_f32 v107, v107, s69, v167
	v_pk_mul_f32 v[114:115], v[114:115], v[130:131]
	v_pk_fma_f32 v[106:107], v[106:107], 4.0, 4.0 op_sel_hi:[1,0,0]
	v_pk_fma_f32 v[108:109], v[108:109], v[124:125], v[128:129] op_sel_hi:[1,0,1]
	v_pk_mul_f32 v[106:107], v[106:107], v[114:115]
	v_pk_add_f32 v[114:115], v[134:135], 1.0 op_sel_hi:[1,0]
	v_med3_f32 v108, v108, s69, v167
	v_rcp_f32_e32 v114, v114
	v_rcp_f32_e32 v115, v115
	v_med3_f32 v109, v109, s69, v167
	v_pk_fma_f32 v[102:103], v[102:103], v[124:125], v[152:153] op_sel_hi:[1,0,1]
	v_pk_fma_f32 v[108:109], v[108:109], 4.0, 4.0 op_sel_hi:[1,0,0]
	v_pk_mul_f32 v[114:115], v[116:117], v[114:115]
	v_min_f32_e32 v102, 0x40e00000, v102
	v_min_f32_e32 v103, 0x40e00000, v103
	v_pk_mul_f32 v[108:109], v[108:109], v[114:115]
	v_pk_mul_f32 v[114:115], v[102:103], s[84:85] op_sel_hi:[1,0]
	v_pk_fma_f32 v[104:105], v[104:105], v[124:125], v[150:151] op_sel_hi:[1,0,1]
	v_exp_f32_e32 v114, v114
	v_exp_f32_e32 v115, v115
; #define LAS __attribute__((address_space(3)))
; DI unsigned pk4_fp8n(float a, float b, float c, float d) { int v = __builtin_amdgcn_cvt_pk_fp8_f32(a, b, 0, false); v = __builtin_amdgcn_cvt_pk_fp8_f32(c, d, v, true); return (unsigned)v; }
;     DI void operator()(const f32x4 (&acc)[2][2][4][2], const Unit& u, int wr, int wc, int fr, int fq, const LAS unsigned char* st) const {
;     ...
;                 for (int mm = 0; mm < 2; ++mm) { const int m = 2 * mp + mm; const float ws = *(const LAS float*)(st + ai * 256 + (m * 16 + fr) * 4) * (1.0f / 32.0f);
;                     const f32x4 g0 = acc[ai][0][m][0], g1 = acc[ai][0][m][1], l0 = acc[ai][1][m][0], l1 = acc[ai][1][m][1];
;                     f32x2 ws2; ws2[0] = ws; ws2[1] = ws;
;                     const f32x2 a01 = swiglu4_2(__builtin_shufflevector(g0, g0, 0, 1) * ws2 + bg[0], __builtin_shufflevector(l0, l0, 0, 1) * ws2 + bl[0]);
;                     const f32x2 a23 = swiglu4_2(__builtin_shufflevector(g0, g0, 2, 3) * ws2 + bg[1], __builtin_shufflevector(l0, l0, 2, 3) * ws2 + bl[1]);
;                     const f32x2 a45 = swiglu4_2(__builtin_shufflevector(g1, g1, 0, 1) * ws2 + bg[2], __builtin_shufflevector(l1, l1, 0, 1) * ws2 + bl[2]);
;                     const f32x2 a67 = swiglu4_2(__builtin_shufflevector(g1, g1, 2, 3) * ws2 + bg[3], __builtin_shufflevector(l1, l1, 2, 3) * ws2 + bl[3]);
;                     w2[mm].x = pk4_fp8n(a01[0], a01[1], a23[0], a23[1]); w2[mm].y = pk4_fp8n(a45[0], a45[1], a67[0], a67[1]); }
;                 const u32x4 w = pair16(w2[0], w2[1]);
;                 *(u32x4*)(ACT + (size_t)(row0 + ai * HALF + (2 * mp + (fq & 1)) * 16) * FF + (f0 - 8 * (fq & 1))) = w; }
	v_min_f32_e32 v104, 0x40e00000, v104
	v_min_f32_e32 v105, 0x40e00000, v105
	v_pk_mul_f32 v[116:117], v[104:105], s[84:85] op_sel_hi:[1,0]
	v_pk_add_f32 v[114:115], v[114:115], 1.0 op_sel_hi:[1,0]
	v_exp_f32_e32 v116, v116
	v_rcp_f32_e32 v114, v114
	v_rcp_f32_e32 v115, v115
	v_exp_f32_e32 v117, v117
	v_pk_fma_f32 v[98:99], v[98:99], v[124:125], v[120:121] op_sel_hi:[1,0,1]
	v_pk_fma_f32 v[100:101], v[100:101], v[124:125], v[112:113] op_sel_hi:[1,0,1]
	v_med3_f32 v98, v98, s69, v167
	v_med3_f32 v99, v99, s69, v167
	v_pk_mul_f32 v[102:103], v[102:103], v[114:115]
	v_pk_fma_f32 v[98:99], v[98:99], 4.0, 4.0 op_sel_hi:[1,0,0]
	v_mov_b32_e32 v125, v147
	v_pk_mul_f32 v[98:99], v[98:99], v[102:103]
	v_pk_add_f32 v[102:103], v[116:117], 1.0 op_sel_hi:[1,0]
	v_cvt_pk_fp8_f32 v125, v98, v99
	v_rcp_f32_e32 v102, v102
	v_rcp_f32_e32 v103, v103
	v_med3_f32 v100, v100, s69, v167
	v_med3_f32 v101, v101, s69, v167
	v_mov_b32_e32 v124, v147
	v_pk_mul_f32 v[102:103], v[104:105], v[102:103]
	v_pk_fma_f32 v[98:99], v[100:101], 4.0, 4.0 op_sel_hi:[1,0,0]
	v_cvt_pk_fp8_f32 v124, v106, v107
	v_pk_mul_f32 v[98:99], v[98:99], v[102:103]
	v_lshlrev_b32_e32 v118, 4, v111
	v_cvt_pk_fp8_f32 v125, v98, v99 op_sel:[0,0,1]
	ds_read2_b32 v[98:99], v126 offset0:32 offset1:48
	v_or3_b32 v118, v118, s0, v146
	v_cvt_pk_fp8_f32 v122, v140, v141 op_sel:[0,0,1]
	v_cvt_pk_fp8_f32 v124, v108, v109 op_sel:[0,0,1]
	v_lshlrev_b32_e32 v111, 3, v111
	v_ashrrev_i32_e32 v119, 31, v118
	v_sub_u32_e32 v110, v110, v111
	v_lshlrev_b64 v[100:101], 11, v[118:119]
	s_waitcnt lgkmcnt(0)
	v_mul_f32_e32 v98, 0x3d000000, v98
	v_ashrrev_i32_e32 v111, 31, v110
	v_lshl_add_u64 v[100:101], s[86:87], 0, v[100:101]
	v_pk_fma_f32 v[94:95], v[94:95], v[98:99], v[156:157] op_sel_hi:[1,0,1]
	v_permlane16_swap_b32_e32 v122, v124
	v_permlane16_swap_b32_e32 v123, v125
	v_lshl_add_u64 v[100:101], v[100:101], 0, v[110:111]
	v_min_f32_e32 v94, 0x40e00000, v94
	v_min_f32_e32 v95, 0x40e00000, v95
	global_store_dwordx4 v[100:101], v[122:125], off nt
	v_pk_mul_f32 v[100:101], v[94:95], s[84:85] op_sel_hi:[1,0]
	v_pk_fma_f32 v[96:97], v[96:97], v[98:99], v[154:155] op_sel_hi:[1,0,1]
	v_exp_f32_e32 v100, v100
	v_exp_f32_e32 v101, v101
	v_min_f32_e32 v96, 0x40e00000, v96
	v_min_f32_e32 v97, 0x40e00000, v97
	v_pk_mul_f32 v[102:103], v[96:97], s[84:85] op_sel_hi:[1,0]
	v_pk_add_f32 v[100:101], v[100:101], 1.0 op_sel_hi:[1,0]
	v_exp_f32_e32 v102, v102
	v_rcp_f32_e32 v100, v100
	v_rcp_f32_e32 v101, v101
	v_exp_f32_e32 v103, v103
	v_pk_fma_f32 v[90:91], v[90:91], v[98:99], v[132:133] op_sel_hi:[1,0,1]
	v_pk_fma_f32 v[92:93], v[92:93], v[98:99], v[128:129] op_sel_hi:[1,0,1]
	v_med3_f32 v90, v90, s69, v167
	v_med3_f32 v91, v91, s69, v167
	v_pk_mul_f32 v[94:95], v[94:95], v[100:101]
	v_pk_fma_f32 v[90:91], v[90:91], 4.0, 4.0 op_sel_hi:[1,0,0]
	v_med3_f32 v92, v92, s69, v167
	v_pk_mul_f32 v[90:91], v[90:91], v[94:95]
	v_pk_add_f32 v[94:95], v[102:103], 1.0 op_sel_hi:[1,0]
	v_med3_f32 v93, v93, s69, v167
	v_rcp_f32_e32 v94, v94
	v_rcp_f32_e32 v95, v95
	v_pk_fma_f32 v[86:87], v[86:87], v[98:99], v[152:153] op_sel_hi:[1,0,1]
	v_pk_fma_f32 v[92:93], v[92:93], 4.0, 4.0 op_sel_hi:[1,0,0]
	v_min_f32_e32 v86, 0x40e00000, v86
	v_pk_mul_f32 v[94:95], v[96:97], v[94:95]
	v_min_f32_e32 v87, 0x40e00000, v87
	v_pk_mul_f32 v[92:93], v[92:93], v[94:95]
	v_pk_mul_f32 v[94:95], v[86:87], s[84:85] op_sel_hi:[1,0]
	v_pk_fma_f32 v[88:89], v[88:89], v[98:99], v[150:151] op_sel_hi:[1,0,1]
	v_exp_f32_e32 v94, v94
	v_exp_f32_e32 v95, v95
	v_min_f32_e32 v88, 0x40e00000, v88
	v_min_f32_e32 v89, 0x40e00000, v89
	v_pk_mul_f32 v[96:97], v[88:89], s[84:85] op_sel_hi:[1,0]
	v_pk_add_f32 v[94:95], v[94:95], 1.0 op_sel_hi:[1,0]
	v_exp_f32_e32 v96, v96
	v_rcp_f32_e32 v94, v94
	v_rcp_f32_e32 v95, v95
	v_exp_f32_e32 v97, v97
	v_pk_fma_f32 v[82:83], v[82:83], v[98:99], v[120:121] op_sel_hi:[1,0,1]
	v_pk_fma_f32 v[84:85], v[84:85], v[98:99], v[112:113] op_sel_hi:[1,0,1]
	v_med3_f32 v82, v82, s69, v167
	v_med3_f32 v83, v83, s69, v167
	v_pk_mul_f32 v[86:87], v[86:87], v[94:95]
	v_pk_fma_f32 v[82:83], v[82:83], 4.0, 4.0 op_sel_hi:[1,0,0]
	v_med3_f32 v84, v84, s69, v167
	v_pk_mul_f32 v[86:87], v[82:83], v[86:87]
	v_pk_add_f32 v[82:83], v[96:97], 1.0 op_sel_hi:[1,0]
	v_med3_f32 v85, v85, s69, v167
	v_rcp_f32_e32 v82, v82
	v_rcp_f32_e32 v83, v83
	v_pk_fma_f32 v[84:85], v[84:85], 4.0, 4.0 op_sel_hi:[1,0,0]
	s_and_b64 vcc, exec, s[2:3]
	s_mov_b64 s[0:1], -1
	v_pk_mul_f32 v[88:89], v[88:89], v[82:83]
	v_mov_b32_e32 v83, v147
	v_cvt_pk_fp8_f32 v83, v86, v87
	v_pk_mul_f32 v[84:85], v[84:85], v[88:89]
	v_mov_b32_e32 v82, v147
	v_cvt_pk_fp8_f32 v82, v90, v91
	v_cvt_pk_fp8_f32 v83, v84, v85 op_sel:[0,0,1]
	v_mul_f32_e32 v84, 0x3d000000, v99
	v_pk_fma_f32 v[78:79], v[78:79], v[84:85], v[156:157] op_sel_hi:[1,0,1]
	v_pk_fma_f32 v[80:81], v[80:81], v[84:85], v[154:155] op_sel_hi:[1,0,1]
	v_min_f32_e32 v78, 0x40e00000, v78
	v_min_f32_e32 v79, 0x40e00000, v79
	v_pk_mul_f32 v[86:87], v[78:79], s[84:85] op_sel_hi:[1,0]
	v_min_f32_e32 v80, 0x40e00000, v80
	v_exp_f32_e32 v86, v86
	v_exp_f32_e32 v87, v87
	v_min_f32_e32 v81, 0x40e00000, v81
	v_pk_mul_f32 v[88:89], v[80:81], s[84:85] op_sel_hi:[1,0]
	v_pk_fma_f32 v[74:75], v[74:75], v[84:85], v[132:133] op_sel_hi:[1,0,1]
	v_pk_add_f32 v[86:87], v[86:87], 1.0 op_sel_hi:[1,0]
	v_exp_f32_e32 v88, v88
	v_rcp_f32_e32 v86, v86
	v_rcp_f32_e32 v87, v87
	v_exp_f32_e32 v89, v89
	v_med3_f32 v74, v74, s69, v167
	v_med3_f32 v75, v75, s69, v167
	v_pk_mul_f32 v[78:79], v[78:79], v[86:87]
	v_pk_fma_f32 v[74:75], v[74:75], 4.0, 4.0 op_sel_hi:[1,0,0]
	v_pk_fma_f32 v[76:77], v[76:77], v[84:85], v[128:129] op_sel_hi:[1,0,1]
	v_pk_mul_f32 v[74:75], v[74:75], v[78:79]
; #define LAS __attribute__((address_space(3)))
; DI unsigned pk4_fp8n(float a, float b, float c, float d) { int v = __builtin_amdgcn_cvt_pk_fp8_f32(a, b, 0, false); v = __builtin_amdgcn_cvt_pk_fp8_f32(c, d, v, true); return (unsigned)v; }
;     DI void operator()(const f32x4 (&acc)[2][2][4][2], const Unit& u, int wr, int wc, int fr, int fq, const LAS unsigned char* st) const {
;     ...
;                 for (int mm = 0; mm < 2; ++mm) { const int m = 2 * mp + mm; const float ws = *(const LAS float*)(st + ai * 256 + (m * 16 + fr) * 4) * (1.0f / 32.0f);
;                     const f32x4 g0 = acc[ai][0][m][0], g1 = acc[ai][0][m][1], l0 = acc[ai][1][m][0], l1 = acc[ai][1][m][1];
;                     f32x2 ws2; ws2[0] = ws; ws2[1] = ws;
;                     const f32x2 a01 = swiglu4_2(__builtin_shufflevector(g0, g0, 0, 1) * ws2 + bg[0], __builtin_shufflevector(l0, l0, 0, 1) * ws2 + bl[0]);
;                     const f32x2 a23 = swiglu4_2(__builtin_shufflevector(g0, g0, 2, 3) * ws2 + bg[1], __builtin_shufflevector(l0, l0, 2, 3) * ws2 + bl[1]);
;                     const f32x2 a45 = swiglu4_2(__builtin_shufflevector(g1, g1, 0, 1) * ws2 + bg[2], __builtin_shufflevector(l1, l1, 0, 1) * ws2 + bl[2]);
;                     const f32x2 a67 = swiglu4_2(__builtin_shufflevector(g1, g1, 2, 3) * ws2 + bg[3], __builtin_shufflevector(l1, l1, 2, 3) * ws2 + bl[3]);
;                     w2[mm].x = pk4_fp8n(a01[0], a01[1], a23[0], a23[1]); w2[mm].y = pk4_fp8n(a45[0], a45[1], a67[0], a67[1]); }
	v_pk_add_f32 v[78:79], v[88:89], 1.0 op_sel_hi:[1,0]
	v_med3_f32 v76, v76, s69, v167
	v_rcp_f32_e32 v78, v78
	v_rcp_f32_e32 v79, v79
	v_med3_f32 v77, v77, s69, v167
	v_pk_fma_f32 v[70:71], v[70:71], v[84:85], v[152:153] op_sel_hi:[1,0,1]
	v_pk_fma_f32 v[76:77], v[76:77], 4.0, 4.0 op_sel_hi:[1,0,0]
	v_pk_mul_f32 v[78:79], v[80:81], v[78:79]
	v_min_f32_e32 v70, 0x40e00000, v70
	v_min_f32_e32 v71, 0x40e00000, v71
	v_pk_mul_f32 v[76:77], v[76:77], v[78:79]
	v_pk_mul_f32 v[78:79], v[70:71], s[84:85] op_sel_hi:[1,0]
	v_pk_fma_f32 v[72:73], v[72:73], v[84:85], v[150:151] op_sel_hi:[1,0,1]
	v_exp_f32_e32 v78, v78
	v_exp_f32_e32 v79, v79
	v_pk_fma_f32 v[66:67], v[66:67], v[84:85], v[120:121] op_sel_hi:[1,0,1]
	v_min_f32_e32 v72, 0x40e00000, v72
	v_min_f32_e32 v73, 0x40e00000, v73
	v_pk_add_f32 v[78:79], v[78:79], 1.0 op_sel_hi:[1,0]
	v_med3_f32 v66, v66, s69, v167
	v_rcp_f32_e32 v78, v78
	v_rcp_f32_e32 v79, v79
	v_med3_f32 v67, v67, s69, v167
	v_pk_mul_f32 v[80:81], v[72:73], s[84:85] op_sel_hi:[1,0]
	v_pk_fma_f32 v[66:67], v[66:67], 4.0, 4.0 op_sel_hi:[1,0,0]
	v_exp_f32_e32 v80, v80
	v_exp_f32_e32 v81, v81
	v_pk_mul_f32 v[70:71], v[70:71], v[78:79]
	v_pk_fma_f32 v[68:69], v[68:69], v[84:85], v[112:113] op_sel_hi:[1,0,1]
	v_pk_mul_f32 v[66:67], v[66:67], v[70:71]
	v_med3_f32 v68, v68, s69, v167
	v_med3_f32 v69, v69, s69, v167
	v_mov_b32_e32 v85, v147
	v_cvt_pk_fp8_f32 v85, v66, v67
	v_pk_fma_f32 v[66:67], v[68:69], 4.0, 4.0 op_sel_hi:[1,0,0]
	ds_read2_b32 v[68:69], v126 offset0:64 offset1:80
	v_pk_add_f32 v[70:71], v[80:81], 1.0 op_sel_hi:[1,0]
	v_mov_b32_e32 v84, v147
	v_rcp_f32_e32 v70, v70
	v_rcp_f32_e32 v71, v71
	s_waitcnt lgkmcnt(0)
	v_mul_f32_e32 v68, 0x3d000000, v68
	v_pk_fma_f32 v[62:63], v[62:63], v[68:69], v[156:157] op_sel_hi:[1,0,1]
	v_pk_fma_f32 v[64:65], v[64:65], v[68:69], v[154:155] op_sel_hi:[1,0,1]
	v_pk_mul_f32 v[70:71], v[72:73], v[70:71]
	v_min_f32_e32 v62, 0x40e00000, v62
	v_min_f32_e32 v63, 0x40e00000, v63
	v_pk_mul_f32 v[66:67], v[66:67], v[70:71]
	v_pk_mul_f32 v[70:71], v[62:63], s[84:85] op_sel_hi:[1,0]
	v_min_f32_e32 v64, 0x40e00000, v64
	v_exp_f32_e32 v70, v70
	v_exp_f32_e32 v71, v71
	v_min_f32_e32 v65, 0x40e00000, v65
	v_pk_mul_f32 v[72:73], v[64:65], s[84:85] op_sel_hi:[1,0]
	v_pk_fma_f32 v[58:59], v[58:59], v[68:69], v[132:133] op_sel_hi:[1,0,1]
	v_pk_add_f32 v[70:71], v[70:71], 1.0 op_sel_hi:[1,0]
	v_exp_f32_e32 v72, v72
	v_rcp_f32_e32 v70, v70
	v_rcp_f32_e32 v71, v71
	v_exp_f32_e32 v73, v73
	v_med3_f32 v58, v58, s69, v167
	v_med3_f32 v59, v59, s69, v167
	v_pk_mul_f32 v[62:63], v[62:63], v[70:71]
	v_pk_fma_f32 v[58:59], v[58:59], 4.0, 4.0 op_sel_hi:[1,0,0]
	v_pk_fma_f32 v[60:61], v[60:61], v[68:69], v[128:129] op_sel_hi:[1,0,1]
	v_pk_mul_f32 v[58:59], v[58:59], v[62:63]
	v_pk_add_f32 v[62:63], v[72:73], 1.0 op_sel_hi:[1,0]
	v_med3_f32 v60, v60, s69, v167
	v_rcp_f32_e32 v62, v62
	v_rcp_f32_e32 v63, v63
	v_med3_f32 v61, v61, s69, v167
	v_pk_fma_f32 v[54:55], v[54:55], v[68:69], v[152:153] op_sel_hi:[1,0,1]
	v_pk_fma_f32 v[60:61], v[60:61], 4.0, 4.0 op_sel_hi:[1,0,0]
	v_pk_mul_f32 v[62:63], v[64:65], v[62:63]
	v_min_f32_e32 v54, 0x40e00000, v54
	v_min_f32_e32 v55, 0x40e00000, v55
	v_pk_mul_f32 v[60:61], v[60:61], v[62:63]
	v_pk_mul_f32 v[62:63], v[54:55], s[84:85] op_sel_hi:[1,0]
	v_pk_fma_f32 v[56:57], v[56:57], v[68:69], v[150:151] op_sel_hi:[1,0,1]
	v_exp_f32_e32 v62, v62
	v_exp_f32_e32 v63, v63
	v_min_f32_e32 v56, 0x40e00000, v56
	v_min_f32_e32 v57, 0x40e00000, v57
	v_pk_mul_f32 v[64:65], v[56:57], s[84:85] op_sel_hi:[1,0]
	v_pk_add_f32 v[62:63], v[62:63], 1.0 op_sel_hi:[1,0]
	v_exp_f32_e32 v64, v64
	v_rcp_f32_e32 v62, v62
	v_rcp_f32_e32 v63, v63
	v_exp_f32_e32 v65, v65
	v_pk_fma_f32 v[50:51], v[50:51], v[68:69], v[120:121] op_sel_hi:[1,0,1]
	v_pk_fma_f32 v[52:53], v[52:53], v[68:69], v[112:113] op_sel_hi:[1,0,1]
	v_med3_f32 v50, v50, s69, v167
	v_med3_f32 v51, v51, s69, v167
	v_pk_mul_f32 v[54:55], v[54:55], v[62:63]
	v_pk_fma_f32 v[50:51], v[50:51], 4.0, 4.0 op_sel_hi:[1,0,0]
	v_med3_f32 v52, v52, s69, v167
	v_pk_mul_f32 v[54:55], v[50:51], v[54:55]
	v_pk_add_f32 v[50:51], v[64:65], 1.0 op_sel_hi:[1,0]
	v_med3_f32 v53, v53, s69, v167
	v_rcp_f32_e32 v50, v50
	v_rcp_f32_e32 v51, v51
	v_pk_fma_f32 v[52:53], v[52:53], 4.0, 4.0 op_sel_hi:[1,0,0]
	v_cvt_pk_fp8_f32 v84, v74, v75
	v_cvt_pk_fp8_f32 v82, v92, v93 op_sel:[0,0,1]
	v_pk_mul_f32 v[56:57], v[56:57], v[50:51]
	v_mov_b32_e32 v51, v147
	v_cvt_pk_fp8_f32 v51, v54, v55
	v_pk_mul_f32 v[52:53], v[52:53], v[56:57]
	v_cvt_pk_fp8_f32 v84, v76, v77 op_sel:[0,0,1]
	v_cvt_pk_fp8_f32 v85, v66, v67 op_sel:[0,0,1]
	v_cvt_pk_fp8_f32 v51, v52, v53 op_sel:[0,0,1]
	v_mul_f32_e32 v52, 0x3d000000, v69
	v_pk_fma_f32 v[46:47], v[46:47], v[52:53], v[156:157] op_sel_hi:[1,0,1]
	v_pk_fma_f32 v[48:49], v[48:49], v[52:53], v[154:155] op_sel_hi:[1,0,1]
	v_min_f32_e32 v46, 0x40e00000, v46
	v_min_f32_e32 v47, 0x40e00000, v47
	v_pk_mul_f32 v[54:55], v[46:47], s[84:85] op_sel_hi:[1,0]
	v_min_f32_e32 v48, 0x40e00000, v48
	v_exp_f32_e32 v54, v54
	v_exp_f32_e32 v55, v55
	v_min_f32_e32 v49, 0x40e00000, v49
	v_pk_mul_f32 v[56:57], v[48:49], s[84:85] op_sel_hi:[1,0]
	v_pk_fma_f32 v[42:43], v[42:43], v[52:53], v[132:133] op_sel_hi:[1,0,1]
	v_pk_add_f32 v[54:55], v[54:55], 1.0 op_sel_hi:[1,0]
	v_exp_f32_e32 v56, v56
	v_rcp_f32_e32 v54, v54
	v_rcp_f32_e32 v55, v55
	v_exp_f32_e32 v57, v57
	v_med3_f32 v42, v42, s69, v167
	v_med3_f32 v43, v43, s69, v167
	v_pk_mul_f32 v[46:47], v[46:47], v[54:55]
	v_pk_fma_f32 v[42:43], v[42:43], 4.0, 4.0 op_sel_hi:[1,0,0]
	v_pk_fma_f32 v[44:45], v[44:45], v[52:53], v[128:129] op_sel_hi:[1,0,1]
	v_pk_mul_f32 v[42:43], v[42:43], v[46:47]
	v_pk_add_f32 v[46:47], v[56:57], 1.0 op_sel_hi:[1,0]
; #define LAS __attribute__((address_space(3)))
; DI unsigned pk4_fp8n(float a, float b, float c, float d) { int v = __builtin_amdgcn_cvt_pk_fp8_f32(a, b, 0, false); v = __builtin_amdgcn_cvt_pk_fp8_f32(c, d, v, true); return (unsigned)v; }
;     DI void operator()(const f32x4 (&acc)[2][2][4][2], const Unit& u, int wr, int wc, int fr, int fq, const LAS unsigned char* st) const {
;     ...
;                 for (int mm = 0; mm < 2; ++mm) { const int m = 2 * mp + mm; const float ws = *(const LAS float*)(st + ai * 256 + (m * 16 + fr) * 4) * (1.0f / 32.0f);
;                     const f32x4 g0 = acc[ai][0][m][0], g1 = acc[ai][0][m][1], l0 = acc[ai][1][m][0], l1 = acc[ai][1][m][1];
;                     f32x2 ws2; ws2[0] = ws; ws2[1] = ws;
;                     const f32x2 a01 = swiglu4_2(__builtin_shufflevector(g0, g0, 0, 1) * ws2 + bg[0], __builtin_shufflevector(l0, l0, 0, 1) * ws2 + bl[0]);
;                     const f32x2 a23 = swiglu4_2(__builtin_shufflevector(g0, g0, 2, 3) * ws2 + bg[1], __builtin_shufflevector(l0, l0, 2, 3) * ws2 + bl[1]);
;                     const f32x2 a45 = swiglu4_2(__builtin_shufflevector(g1, g1, 0, 1) * ws2 + bg[2], __builtin_shufflevector(l1, l1, 0, 1) * ws2 + bl[2]);
;                     const f32x2 a67 = swiglu4_2(__builtin_shufflevector(g1, g1, 2, 3) * ws2 + bg[3], __builtin_shufflevector(l1, l1, 2, 3) * ws2 + bl[3]);
;                     w2[mm].x = pk4_fp8n(a01[0], a01[1], a23[0], a23[1]); w2[mm].y = pk4_fp8n(a45[0], a45[1], a67[0], a67[1]); }
;                 const u32x4 w = pair16(w2[0], w2[1]);
;                 *(u32x4*)(ACT + (size_t)(row0 + ai * HALF + (2 * mp + (fq & 1)) * 16) * FF + (f0 - 8 * (fq & 1))) = w; }
	v_med3_f32 v44, v44, s69, v167
	v_rcp_f32_e32 v46, v46
	v_rcp_f32_e32 v47, v47
	v_med3_f32 v45, v45, s69, v167
	v_pk_fma_f32 v[38:39], v[38:39], v[52:53], v[152:153] op_sel_hi:[1,0,1]
	v_pk_fma_f32 v[44:45], v[44:45], 4.0, 4.0 op_sel_hi:[1,0,0]
	v_pk_mul_f32 v[46:47], v[48:49], v[46:47]
	v_min_f32_e32 v38, 0x40e00000, v38
	v_min_f32_e32 v39, 0x40e00000, v39
	v_pk_mul_f32 v[44:45], v[44:45], v[46:47]
	v_pk_mul_f32 v[46:47], v[38:39], s[84:85] op_sel_hi:[1,0]
	v_pk_fma_f32 v[40:41], v[40:41], v[52:53], v[150:151] op_sel_hi:[1,0,1]
	v_exp_f32_e32 v46, v46
	v_exp_f32_e32 v47, v47
	v_min_f32_e32 v40, 0x40e00000, v40
	v_min_f32_e32 v41, 0x40e00000, v41
	v_pk_mul_f32 v[48:49], v[40:41], s[84:85] op_sel_hi:[1,0]
	v_pk_add_f32 v[46:47], v[46:47], 1.0 op_sel_hi:[1,0]
	v_exp_f32_e32 v48, v48
	v_rcp_f32_e32 v46, v46
	v_rcp_f32_e32 v47, v47
	v_exp_f32_e32 v49, v49
	v_pk_fma_f32 v[34:35], v[34:35], v[52:53], v[120:121] op_sel_hi:[1,0,1]
	v_pk_fma_f32 v[36:37], v[36:37], v[52:53], v[112:113] op_sel_hi:[1,0,1]
	v_med3_f32 v34, v34, s69, v167
	v_med3_f32 v35, v35, s69, v167
	v_pk_mul_f32 v[38:39], v[38:39], v[46:47]
	v_pk_fma_f32 v[34:35], v[34:35], 4.0, 4.0 op_sel_hi:[1,0,0]
	v_mov_b32_e32 v53, v147
	v_pk_mul_f32 v[34:35], v[34:35], v[38:39]
	v_pk_add_f32 v[38:39], v[48:49], 1.0 op_sel_hi:[1,0]
	v_cvt_pk_fp8_f32 v53, v34, v35
	v_rcp_f32_e32 v38, v38
	v_rcp_f32_e32 v39, v39
	v_med3_f32 v36, v36, s69, v167
	v_med3_f32 v37, v37, s69, v167
	v_or_b32_e32 v66, 32, v118
	v_mov_b32_e32 v50, v147
	v_pk_mul_f32 v[38:39], v[40:41], v[38:39]
	v_mov_b32_e32 v52, v147
	v_pk_fma_f32 v[34:35], v[36:37], 4.0, 4.0 op_sel_hi:[1,0,0]
	v_ashrrev_i32_e32 v67, 31, v66
	v_cvt_pk_fp8_f32 v50, v58, v59
	v_cvt_pk_fp8_f32 v52, v42, v43
	v_pk_mul_f32 v[34:35], v[34:35], v[38:39]
	v_lshlrev_b64 v[66:67], 11, v[66:67]
	v_cvt_pk_fp8_f32 v53, v34, v35 op_sel:[0,0,1]
	ds_read2_b32 v[34:35], v126 offset0:96 offset1:112
	v_lshl_add_u64 v[66:67], s[86:87], 0, v[66:67]
	v_permlane16_swap_b32_e32 v82, v84
	v_permlane16_swap_b32_e32 v83, v85
	v_lshl_add_u64 v[66:67], v[66:67], 0, v[110:111]
	global_store_dwordx4 v[66:67], v[82:85], off nt
	v_add_u32_e32 v66, 0x80, v118
	v_cvt_pk_fp8_f32 v50, v60, v61 op_sel:[0,0,1]
	v_cvt_pk_fp8_f32 v52, v44, v45 op_sel:[0,0,1]
	v_ashrrev_i32_e32 v67, 31, v66
	v_lshlrev_b64 v[36:37], 11, v[66:67]
	s_waitcnt lgkmcnt(0)
	v_mul_f32_e32 v34, 0x3d000000, v34
	v_lshl_add_u64 v[36:37], s[86:87], 0, v[36:37]
	v_pk_fma_f32 v[30:31], v[30:31], v[34:35], v[156:157] op_sel_hi:[1,0,1]
	v_permlane16_swap_b32_e32 v50, v52
	v_permlane16_swap_b32_e32 v51, v53
	v_lshl_add_u64 v[36:37], v[36:37], 0, v[110:111]
	v_min_f32_e32 v30, 0x40e00000, v30
	v_min_f32_e32 v31, 0x40e00000, v31
	global_store_dwordx4 v[36:37], v[50:53], off nt
	v_pk_mul_f32 v[36:37], v[30:31], s[84:85] op_sel_hi:[1,0]
	v_pk_fma_f32 v[32:33], v[32:33], v[34:35], v[154:155] op_sel_hi:[1,0,1]
	v_exp_f32_e32 v36, v36
	v_exp_f32_e32 v37, v37
	v_min_f32_e32 v32, 0x40e00000, v32
	v_min_f32_e32 v33, 0x40e00000, v33
	v_pk_mul_f32 v[38:39], v[32:33], s[84:85] op_sel_hi:[1,0]
	v_pk_add_f32 v[36:37], v[36:37], 1.0 op_sel_hi:[1,0]
	v_exp_f32_e32 v38, v38
	v_rcp_f32_e32 v36, v36
	v_rcp_f32_e32 v37, v37
	v_exp_f32_e32 v39, v39
	v_pk_fma_f32 v[26:27], v[26:27], v[34:35], v[132:133] op_sel_hi:[1,0,1]
	v_pk_fma_f32 v[28:29], v[28:29], v[34:35], v[128:129] op_sel_hi:[1,0,1]
	v_med3_f32 v26, v26, s69, v167
	v_med3_f32 v27, v27, s69, v167
	v_pk_mul_f32 v[30:31], v[30:31], v[36:37]
	v_pk_fma_f32 v[26:27], v[26:27], 4.0, 4.0 op_sel_hi:[1,0,0]
	v_med3_f32 v28, v28, s69, v167
	v_pk_mul_f32 v[26:27], v[26:27], v[30:31]
	v_pk_add_f32 v[30:31], v[38:39], 1.0 op_sel_hi:[1,0]
	v_med3_f32 v29, v29, s69, v167
	v_rcp_f32_e32 v30, v30
	v_rcp_f32_e32 v31, v31
	v_pk_fma_f32 v[22:23], v[22:23], v[34:35], v[152:153] op_sel_hi:[1,0,1]
	v_pk_fma_f32 v[28:29], v[28:29], 4.0, 4.0 op_sel_hi:[1,0,0]
	v_min_f32_e32 v22, 0x40e00000, v22
	v_pk_mul_f32 v[30:31], v[32:33], v[30:31]
	v_min_f32_e32 v23, 0x40e00000, v23
	v_pk_mul_f32 v[28:29], v[28:29], v[30:31]
	v_pk_mul_f32 v[30:31], v[22:23], s[84:85] op_sel_hi:[1,0]
	v_pk_fma_f32 v[24:25], v[24:25], v[34:35], v[150:151] op_sel_hi:[1,0,1]
	v_exp_f32_e32 v30, v30
	v_exp_f32_e32 v31, v31
	v_min_f32_e32 v24, 0x40e00000, v24
	v_min_f32_e32 v25, 0x40e00000, v25
	v_pk_mul_f32 v[32:33], v[24:25], s[84:85] op_sel_hi:[1,0]
	v_pk_add_f32 v[30:31], v[30:31], 1.0 op_sel_hi:[1,0]
	v_exp_f32_e32 v32, v32
	v_rcp_f32_e32 v30, v30
	v_rcp_f32_e32 v31, v31
	v_exp_f32_e32 v33, v33
	v_pk_fma_f32 v[18:19], v[18:19], v[34:35], v[120:121] op_sel_hi:[1,0,1]
	v_pk_fma_f32 v[20:21], v[20:21], v[34:35], v[112:113] op_sel_hi:[1,0,1]
	v_med3_f32 v18, v18, s69, v167
	v_med3_f32 v19, v19, s69, v167
	v_pk_mul_f32 v[22:23], v[22:23], v[30:31]
	v_pk_fma_f32 v[18:19], v[18:19], 4.0, 4.0 op_sel_hi:[1,0,0]
	v_med3_f32 v20, v20, s69, v167
	v_pk_mul_f32 v[22:23], v[18:19], v[22:23]
; #define LAS __attribute__((address_space(3)))
; DI unsigned pk4_fp8n(float a, float b, float c, float d) { int v = __builtin_amdgcn_cvt_pk_fp8_f32(a, b, 0, false); v = __builtin_amdgcn_cvt_pk_fp8_f32(c, d, v, true); return (unsigned)v; }
; #define PG8_DMA4(gp, lp) __builtin_amdgcn_global_load_lds((const unsigned*)(gp), (LAS unsigned*)(lp), 4, 0, 0)
;     DI void prefetch(const Unit& u, int wr, int wc, int lane, LAS unsigned char* st) const {
;         const float* rp = rows + u.pm * BM + wr * 64 + lane;
;         PG8_DMA4(rp, st); PG8_DMA4(rp + HALF, st + 256);
;         PG8_DMA4(b_up + (size_t)u.e * UPW + 2 * (u.pn * HALF + wc * 32) + lane, st + 512);
;     }
;     DI void operator()(const f32x4 (&acc)[2][2][4][2], const Unit& u, int wr, int wc, int fr, int fq, const LAS unsigned char* st) const {
;     ...
;                 for (int mm = 0; mm < 2; ++mm) { const int m = 2 * mp + mm; const float ws = *(const LAS float*)(st + ai * 256 + (m * 16 + fr) * 4) * (1.0f / 32.0f);
;                     const f32x4 g0 = acc[ai][0][m][0], g1 = acc[ai][0][m][1], l0 = acc[ai][1][m][0], l1 = acc[ai][1][m][1];
;                     f32x2 ws2; ws2[0] = ws; ws2[1] = ws;
;                     const f32x2 a01 = swiglu4_2(__builtin_shufflevector(g0, g0, 0, 1) * ws2 + bg[0], __builtin_shufflevector(l0, l0, 0, 1) * ws2 + bl[0]);
;                     const f32x2 a23 = swiglu4_2(__builtin_shufflevector(g0, g0, 2, 3) * ws2 + bg[1], __builtin_shufflevector(l0, l0, 2, 3) * ws2 + bl[1]);
;                     const f32x2 a45 = swiglu4_2(__builtin_shufflevector(g1, g1, 0, 1) * ws2 + bg[2], __builtin_shufflevector(l1, l1, 0, 1) * ws2 + bl[2]);
;                     const f32x2 a67 = swiglu4_2(__builtin_shufflevector(g1, g1, 2, 3) * ws2 + bg[3], __builtin_shufflevector(l1, l1, 2, 3) * ws2 + bl[3]);
;                     w2[mm].x = pk4_fp8n(a01[0], a01[1], a23[0], a23[1]); w2[mm].y = pk4_fp8n(a45[0], a45[1], a67[0], a67[1]); }
;                 const u32x4 w = pair16(w2[0], w2[1]);
;                 *(u32x4*)(ACT + (size_t)(row0 + ai * HALF + (2 * mp + (fq & 1)) * 16) * FF + (f0 - 8 * (fq & 1))) = w; }
	v_pk_add_f32 v[18:19], v[32:33], 1.0 op_sel_hi:[1,0]
	v_med3_f32 v21, v21, s69, v167
	v_rcp_f32_e32 v18, v18
	v_rcp_f32_e32 v19, v19
	v_pk_fma_f32 v[20:21], v[20:21], 4.0, 4.0 op_sel_hi:[1,0,0]
	v_pk_mul_f32 v[24:25], v[24:25], v[18:19]
	v_mov_b32_e32 v19, v147
	v_cvt_pk_fp8_f32 v19, v22, v23
	v_pk_mul_f32 v[20:21], v[20:21], v[24:25]
	v_mov_b32_e32 v18, v147
	v_cvt_pk_fp8_f32 v18, v26, v27
	v_cvt_pk_fp8_f32 v19, v20, v21 op_sel:[0,0,1]
	v_mul_f32_e32 v20, 0x3d000000, v35
	v_pk_fma_f32 v[14:15], v[14:15], v[20:21], v[156:157] op_sel_hi:[1,0,1]
	v_pk_fma_f32 v[16:17], v[16:17], v[20:21], v[154:155] op_sel_hi:[1,0,1]
	v_min_f32_e32 v14, 0x40e00000, v14
	v_min_f32_e32 v15, 0x40e00000, v15
	v_pk_mul_f32 v[22:23], v[14:15], s[84:85] op_sel_hi:[1,0]
	v_min_f32_e32 v16, 0x40e00000, v16
	v_exp_f32_e32 v22, v22
	v_exp_f32_e32 v23, v23
	v_min_f32_e32 v17, 0x40e00000, v17
	v_pk_mul_f32 v[24:25], v[16:17], s[84:85] op_sel_hi:[1,0]
	v_pk_fma_f32 v[10:11], v[10:11], v[20:21], v[132:133] op_sel_hi:[1,0,1]
	v_pk_add_f32 v[22:23], v[22:23], 1.0 op_sel_hi:[1,0]
	v_exp_f32_e32 v24, v24
	v_rcp_f32_e32 v22, v22
	v_rcp_f32_e32 v23, v23
	v_exp_f32_e32 v25, v25
	v_med3_f32 v10, v10, s69, v167
	v_med3_f32 v11, v11, s69, v167
	v_pk_mul_f32 v[14:15], v[14:15], v[22:23]
	v_pk_fma_f32 v[10:11], v[10:11], 4.0, 4.0 op_sel_hi:[1,0,0]
	v_pk_fma_f32 v[12:13], v[12:13], v[20:21], v[128:129] op_sel_hi:[1,0,1]
	v_pk_mul_f32 v[10:11], v[10:11], v[14:15]
	v_pk_add_f32 v[14:15], v[24:25], 1.0 op_sel_hi:[1,0]
	v_med3_f32 v12, v12, s69, v167
	v_rcp_f32_e32 v14, v14
	v_rcp_f32_e32 v15, v15
	v_med3_f32 v13, v13, s69, v167
	v_pk_fma_f32 v[6:7], v[6:7], v[20:21], v[152:153] op_sel_hi:[1,0,1]
	v_pk_fma_f32 v[12:13], v[12:13], 4.0, 4.0 op_sel_hi:[1,0,0]
	v_pk_mul_f32 v[14:15], v[16:17], v[14:15]
	v_min_f32_e32 v6, 0x40e00000, v6
	v_min_f32_e32 v7, 0x40e00000, v7
	v_pk_mul_f32 v[12:13], v[12:13], v[14:15]
	v_pk_mul_f32 v[14:15], v[6:7], s[84:85] op_sel_hi:[1,0]
	v_pk_fma_f32 v[8:9], v[8:9], v[20:21], v[150:151] op_sel_hi:[1,0,1]
	v_exp_f32_e32 v14, v14
	v_exp_f32_e32 v15, v15
	v_min_f32_e32 v8, 0x40e00000, v8
	v_min_f32_e32 v9, 0x40e00000, v9
	v_pk_mul_f32 v[16:17], v[8:9], s[84:85] op_sel_hi:[1,0]
	v_pk_add_f32 v[14:15], v[14:15], 1.0 op_sel_hi:[1,0]
	v_exp_f32_e32 v16, v16
	v_rcp_f32_e32 v14, v14
	v_rcp_f32_e32 v15, v15
	v_exp_f32_e32 v17, v17
	v_pk_fma_f32 v[2:3], v[2:3], v[20:21], v[120:121] op_sel_hi:[1,0,1]
	v_pk_fma_f32 v[4:5], v[4:5], v[20:21], v[112:113] op_sel_hi:[1,0,1]
	v_med3_f32 v2, v2, s69, v167
	v_med3_f32 v3, v3, s69, v167
	v_pk_mul_f32 v[6:7], v[6:7], v[14:15]
	v_pk_fma_f32 v[2:3], v[2:3], 4.0, 4.0 op_sel_hi:[1,0,0]
	v_mov_b32_e32 v20, v147
	v_pk_mul_f32 v[2:3], v[2:3], v[6:7]
	v_pk_add_f32 v[6:7], v[16:17], 1.0 op_sel_hi:[1,0]
	v_mov_b32_e32 v21, v147
	v_rcp_f32_e32 v6, v6
	v_rcp_f32_e32 v7, v7
	v_cvt_pk_fp8_f32 v20, v10, v11
	v_cvt_pk_fp8_f32 v21, v2, v3
	v_med3_f32 v4, v4, s69, v167
	v_med3_f32 v5, v5, s69, v167
	v_pk_mul_f32 v[6:7], v[8:9], v[6:7]
	v_pk_fma_f32 v[2:3], v[4:5], 4.0, 4.0 op_sel_hi:[1,0,0]
	v_cvt_pk_fp8_f32 v18, v28, v29 op_sel:[0,0,1]
	v_pk_mul_f32 v[2:3], v[2:3], v[6:7]
	v_cvt_pk_fp8_f32 v20, v12, v13 op_sel:[0,0,1]
	v_cvt_pk_fp8_f32 v21, v2, v3 op_sel:[0,0,1]
	v_add_u32_e32 v2, 0xa0, v118
	v_ashrrev_i32_e32 v3, 31, v2
	v_lshlrev_b64 v[2:3], 11, v[2:3]
	v_lshl_add_u64 v[2:3], s[86:87], 0, v[2:3]
	v_permlane16_swap_b32_e32 v18, v20
	v_permlane16_swap_b32_e32 v19, v21
	v_lshl_add_u64 v[2:3], v[2:3], 0, v[110:111]
	global_store_dwordx4 v[2:3], v[18:21], off nt
	s_cbranch_vccnz .LBB0_1076
	s_lshl_b32 s0, s71, 8
	s_ashr_i32 s1, s0, 31
	v_mov_b32_e32 v2, v224
	s_lshl_b64 s[0:1], s[0:1], 2
	s_add_u32 s0, s62, s0
	v_ashrrev_i32_e32 v3, 31, v2
	s_addc_u32 s1, s63, s1
	v_lshlrev_b64 v[2:3], 2, v[2:3]
	s_mov_b32 m0, s35
	v_lshl_add_u64 v[4:5], s[0:1], 0, v[2:3]
	s_lshl_b64 s[0:1], s[30:31], 14
	v_readlane_b32 s16, v254, 25
	global_load_lds_dword v[4:5], off
	s_add_i32 m0, s35, 0x100
	v_readlane_b32 s30, v254, 39
	v_readlane_b32 s31, v254, 40
	s_add_u32 s2, s30, s0
	s_addc_u32 s3, s31, s1
	s_lshl_b32 s0, s76, 8
	s_or_b32 s0, s0, s51
	s_ashr_i32 s1, s0, 31
	s_lshl_b64 s[0:1], s[0:1], 2
	s_add_u32 s0, s2, s0
	v_lshl_add_u64 v[4:5], v[4:5], 0, s[12:13]
	s_addc_u32 s1, s3, s1
	global_load_lds_dword v[4:5], off
	v_lshl_add_u64 v[2:3], s[0:1], 0, v[2:3]
	s_mov_b32 m0, s70
	s_andn2_b64 vcc, exec, s[14:15]
	global_load_lds_dword v[2:3], off
	v_readlane_b32 s17, v254, 26
	v_readlane_b32 s18, v254, 27
	v_readlane_b32 s19, v254, 28
	v_readlane_b32 s20, v254, 29
	v_readlane_b32 s21, v254, 30
	v_readlane_b32 s22, v254, 31
	v_readlane_b32 s23, v254, 32
	v_readlane_b32 s24, v254, 33
	v_readlane_b32 s25, v254, 34
	v_readlane_b32 s26, v254, 35
	v_readlane_b32 s27, v254, 36
	v_readlane_b32 s28, v254, 37
	v_readlane_b32 s29, v254, 38
	s_cbranch_vccnz .LBB0_1075
	s_barrier
	s_branch .LBB0_1075

; #define LAS __attribute__((address_space(3)))
;     DI void operator()(const f32x4 (&acc)[2][2][4][2], const Unit& u, int wr, int wc, int fr, int fq, const LAS unsigned char* st) const {
;         const int row0 = u.pm * BM + wr * 64 + fr, col0 = u.pn * BM + wc * 32 + 8 * fq;
;         f32x4 bv[2][2];
; #pragma unroll
;         for (int bj = 0; bj < 2; ++bj)
; #pragma unroll
;             for (int n = 0; n < 2; ++n) bv[bj][n] = *(const LAS f32x4*)(st + 512 + bj * 128 + fq * 32 + 16 * n);
; #pragma unroll
;         for (int ai = 0; ai < 2; ++ai)
; #pragma unroll
;             for (int mp = 0; mp < 2; ++mp) {
;                 const float wA = *(const LAS float*)(st + ai * 256 + ((2 * mp) * 16 + fr) * 4) * 16.0f, wB = *(const LAS float*)(st + ai * 256 + ((2 * mp + 1) * 16 + fr) * 4) * 16.0f;
;                 unsigned char* rowp = YB + (size_t)(row0 + ai * HALF + (2 * mp + (fq & 1)) * 16) * DM + (col0 - 8 * (fq & 1));
; #pragma unroll
;                 for (int bj = 0; bj < 2; ++bj) { u32x2 w2[2];
; #pragma unroll
;                     for (int mm = 0; mm < 2; ++mm) { const int m = 2 * mp + mm; const float w8 = mm ? wB : wA;
;                         const f32x4 v0 = (acc[ai][bj][m][0] * (1.0f / 128.0f) + bv[bj][0]) * w8, v1 = (acc[ai][bj][m][1] * (1.0f / 128.0f) + bv[bj][1]) * w8;
;                         w2[mm].x = pk4_fp8m(v0[0], v0[1], v0[2], v0[3]); w2[mm].y = pk4_fp8m(v1[0], v1[1], v1[2], v1[3]); }
.LBB0_1164:
	v_mov_b32_e32 v128, v224
	s_lshl_b32 s0, s30, 8
	v_and_b32_e32 v144, 15, v128
	v_ashrrev_i32_e32 v148, 4, v128
	v_lshl_add_u32 v128, v148, 5, s29
	v_lshl_add_u32 v169, v144, 2, s29
	ds_read_b128 v[140:143], v128 offset:512
	ds_read_b128 v[136:139], v128 offset:528
	ds_read_b128 v[132:135], v128 offset:640
	ds_read_b128 v[128:131], v128 offset:656
	ds_read2_b32 v[162:163], v169 offset1:16
	s_add_i32 s0, s0, s44
	v_or_b32_e32 v168, s0, v144
	s_lshl_b32 s0, s28, 8
	s_or_b32 s0, s0, s45
	v_and_b32_e32 v144, 1, v148
	v_lshl_add_u32 v149, v148, 3, s0
	v_lshlrev_b32_e32 v148, 3, v144
	v_lshlrev_b32_e32 v170, 4, v144
	s_waitcnt lgkmcnt(0)
	v_mul_f32_e32 v144, 0x41800000, v162
	v_pk_fma_f32 v[124:125], v[124:125], s[18:19], v[140:141] op_sel_hi:[1,0,1]
	v_pk_fma_f32 v[126:127], v[126:127], s[18:19], v[142:143] op_sel_hi:[1,0,1]
	v_pk_mul_f32 v[124:125], v[124:125], v[144:145] op_sel_hi:[1,0]
	v_pk_fma_f32 v[120:121], v[120:121], s[18:19], v[136:137] op_sel_hi:[1,0,1]
	v_pk_mul_f32 v[126:127], v[126:127], v[144:145] op_sel_hi:[1,0]
	v_pk_mul_f32 v[166:167], v[120:121], v[144:145] op_sel_hi:[1,0]
	v_med3_f32 v121, v124, s59, v161
	v_med3_f32 v124, v125, s59, v161
	v_mov_b32_e32 v120, v145
	v_med3_f32 v125, v126, s59, v161
	v_med3_f32 v126, v127, s59, v161
	v_cvt_pk_fp8_f32 v120, v121, v124
	v_med3_f32 v124, v166, s59, v161
	v_med3_f32 v127, v167, s59, v161
	v_mov_b32_e32 v121, v145
	v_cvt_pk_fp8_f32 v121, v124, v127
	v_pk_fma_f32 v[122:123], v[122:123], s[18:19], v[138:139] op_sel_hi:[1,0,1]
	v_mul_f32_e32 v124, 0x41800000, v163
	v_pk_mul_f32 v[122:123], v[122:123], v[144:145] op_sel_hi:[1,0]
	v_pk_fma_f32 v[112:113], v[112:113], s[18:19], v[136:137] op_sel_hi:[1,0,1]
	v_med3_f32 v122, v122, s59, v161
	v_med3_f32 v123, v123, s59, v161
	v_pk_mul_f32 v[112:113], v[112:113], v[124:125] op_sel_hi:[1,0]
	v_cvt_pk_fp8_f32 v121, v122, v123 op_sel:[0,0,1]
	v_med3_f32 v112, v112, s59, v161
	v_med3_f32 v113, v113, s59, v161
	v_mov_b32_e32 v123, v145
	v_cvt_pk_fp8_f32 v123, v112, v113
	v_pk_fma_f32 v[114:115], v[114:115], s[18:19], v[138:139] op_sel_hi:[1,0,1]
	v_pk_fma_f32 v[108:109], v[108:109], s[18:19], v[132:133] op_sel_hi:[1,0,1]
	v_pk_mul_f32 v[114:115], v[114:115], v[124:125] op_sel_hi:[1,0]
	v_pk_fma_f32 v[110:111], v[110:111], s[18:19], v[134:135] op_sel_hi:[1,0,1]
	v_med3_f32 v112, v114, s59, v161
	v_med3_f32 v113, v115, s59, v161
	v_pk_mul_f32 v[108:109], v[108:109], v[144:145] op_sel_hi:[1,0]
	v_pk_fma_f32 v[104:105], v[104:105], s[18:19], v[128:129] op_sel_hi:[1,0,1]
	v_cvt_pk_fp8_f32 v123, v112, v113 op_sel:[0,0,1]
	v_pk_mul_f32 v[110:111], v[110:111], v[144:145] op_sel_hi:[1,0]
	v_pk_mul_f32 v[112:113], v[104:105], v[144:145] op_sel_hi:[1,0]
	v_med3_f32 v105, v108, s59, v161
	v_med3_f32 v108, v109, s59, v161
	v_mov_b32_e32 v104, v145
	v_med3_f32 v109, v110, s59, v161
	v_med3_f32 v110, v111, s59, v161
	v_cvt_pk_fp8_f32 v104, v105, v108
	v_med3_f32 v108, v112, s59, v161
	v_med3_f32 v111, v113, s59, v161
	v_mov_b32_e32 v105, v145
	v_cvt_pk_fp8_f32 v105, v108, v111
	v_pk_fma_f32 v[106:107], v[106:107], s[18:19], v[130:131] op_sel_hi:[1,0,1]
	v_pk_fma_f32 v[96:97], v[96:97], s[18:19], v[128:129] op_sel_hi:[1,0,1]
	v_pk_mul_f32 v[106:107], v[106:107], v[144:145] op_sel_hi:[1,0]
	v_pk_mul_f32 v[96:97], v[96:97], v[124:125] op_sel_hi:[1,0]
	v_med3_f32 v106, v106, s59, v161
	v_med3_f32 v107, v107, s59, v161
	v_cvt_pk_fp8_f32 v105, v106, v107 op_sel:[0,0,1]
	v_med3_f32 v96, v96, s59, v161
	v_med3_f32 v97, v97, s59, v161
	v_mov_b32_e32 v107, v145
	v_cvt_pk_fp8_f32 v107, v96, v97
	v_pk_fma_f32 v[98:99], v[98:99], s[18:19], v[130:131] op_sel_hi:[1,0,1]
	v_pk_fma_f32 v[100:101], v[100:101], s[18:19], v[132:133] op_sel_hi:[1,0,1]
	v_pk_mul_f32 v[98:99], v[98:99], v[124:125] op_sel_hi:[1,0]
	v_pk_mul_f32 v[100:101], v[100:101], v[124:125] op_sel_hi:[1,0]
	v_med3_f32 v96, v98, s59, v161
	v_med3_f32 v97, v99, s59, v161
	v_cvt_pk_fp8_f32 v107, v96, v97 op_sel:[0,0,1]
	ds_read2_b32 v[96:97], v169 offset0:32 offset1:48
	v_pk_fma_f32 v[92:93], v[92:93], s[18:19], v[140:141] op_sel_hi:[1,0,1]
	v_med3_f32 v100, v100, s59, v161
	v_med3_f32 v101, v101, s59, v161
	v_mov_b32_e32 v106, v145
	s_waitcnt lgkmcnt(0)
	v_mul_f32_e32 v96, 0x41800000, v96
	v_pk_fma_f32 v[94:95], v[94:95], s[18:19], v[142:143] op_sel_hi:[1,0,1]
	v_pk_mul_f32 v[92:93], v[92:93], v[96:97] op_sel_hi:[1,0]
	v_pk_fma_f32 v[88:89], v[88:89], s[18:19], v[136:137] op_sel_hi:[1,0,1]
	v_cvt_pk_fp8_f32 v106, v100, v101
	v_pk_mul_f32 v[94:95], v[94:95], v[96:97] op_sel_hi:[1,0]
	v_pk_mul_f32 v[100:101], v[88:89], v[96:97] op_sel_hi:[1,0]
	v_med3_f32 v89, v92, s59, v161
	v_med3_f32 v92, v93, s59, v161
	v_mov_b32_e32 v88, v145
	v_med3_f32 v93, v94, s59, v161
	v_med3_f32 v94, v95, s59, v161
	v_cvt_pk_fp8_f32 v88, v89, v92
	v_med3_f32 v92, v100, s59, v161
	v_med3_f32 v95, v101, s59, v161
	v_mov_b32_e32 v89, v145
	v_cvt_pk_fp8_f32 v89, v92, v95
	v_pk_fma_f32 v[90:91], v[90:91], s[18:19], v[138:139] op_sel_hi:[1,0,1]
	v_mul_f32_e32 v92, 0x41800000, v97
	v_pk_mul_f32 v[90:91], v[90:91], v[96:97] op_sel_hi:[1,0]
	v_pk_fma_f32 v[80:81], v[80:81], s[18:19], v[136:137] op_sel_hi:[1,0,1]
	v_med3_f32 v90, v90, s59, v161
	v_med3_f32 v91, v91, s59, v161
	v_pk_mul_f32 v[80:81], v[80:81], v[92:93] op_sel_hi:[1,0]
	v_cvt_pk_fp8_f32 v89, v90, v91 op_sel:[0,0,1]
	v_med3_f32 v80, v80, s59, v161
	v_med3_f32 v81, v81, s59, v161
	v_mov_b32_e32 v91, v145
	v_cvt_pk_fp8_f32 v91, v80, v81
	v_pk_fma_f32 v[82:83], v[82:83], s[18:19], v[138:139] op_sel_hi:[1,0,1]
	v_pk_fma_f32 v[76:77], v[76:77], s[18:19], v[132:133] op_sel_hi:[1,0,1]
	v_pk_mul_f32 v[82:83], v[82:83], v[92:93] op_sel_hi:[1,0]
; #define LAS __attribute__((address_space(3)))
;     DI void operator()(const f32x4 (&acc)[2][2][4][2], const Unit& u, int wr, int wc, int fr, int fq, const LAS unsigned char* st) const {
;     ...
;                 const float wA = *(const LAS float*)(st + ai * 256 + ((2 * mp) * 16 + fr) * 4) * 16.0f, wB = *(const LAS float*)(st + ai * 256 + ((2 * mp + 1) * 16 + fr) * 4) * 16.0f;
;                 unsigned char* rowp = YB + (size_t)(row0 + ai * HALF + (2 * mp + (fq & 1)) * 16) * DM + (col0 - 8 * (fq & 1));
; #pragma unroll
;                 for (int bj = 0; bj < 2; ++bj) { u32x2 w2[2];
; #pragma unroll
;                     for (int mm = 0; mm < 2; ++mm) { const int m = 2 * mp + mm; const float w8 = mm ? wB : wA;
;                         const f32x4 v0 = (acc[ai][bj][m][0] * (1.0f / 128.0f) + bv[bj][0]) * w8, v1 = (acc[ai][bj][m][1] * (1.0f / 128.0f) + bv[bj][1]) * w8;
;                         w2[mm].x = pk4_fp8m(v0[0], v0[1], v0[2], v0[3]); w2[mm].y = pk4_fp8m(v1[0], v1[1], v1[2], v1[3]); }
	v_pk_fma_f32 v[78:79], v[78:79], s[18:19], v[134:135] op_sel_hi:[1,0,1]
	v_med3_f32 v80, v82, s59, v161
	v_med3_f32 v81, v83, s59, v161
	v_pk_mul_f32 v[76:77], v[76:77], v[96:97] op_sel_hi:[1,0]
	v_pk_fma_f32 v[72:73], v[72:73], s[18:19], v[128:129] op_sel_hi:[1,0,1]
	v_cvt_pk_fp8_f32 v91, v80, v81 op_sel:[0,0,1]
	v_pk_mul_f32 v[78:79], v[78:79], v[96:97] op_sel_hi:[1,0]
	v_pk_mul_f32 v[80:81], v[72:73], v[96:97] op_sel_hi:[1,0]
	v_med3_f32 v73, v76, s59, v161
	v_med3_f32 v76, v77, s59, v161
	v_mov_b32_e32 v72, v145
	v_med3_f32 v77, v78, s59, v161
	v_med3_f32 v78, v79, s59, v161
	v_cvt_pk_fp8_f32 v72, v73, v76
	v_med3_f32 v76, v80, s59, v161
	v_med3_f32 v79, v81, s59, v161
	v_mov_b32_e32 v73, v145
	v_cvt_pk_fp8_f32 v73, v76, v79
	v_pk_fma_f32 v[74:75], v[74:75], s[18:19], v[130:131] op_sel_hi:[1,0,1]
	v_pk_fma_f32 v[64:65], v[64:65], s[18:19], v[128:129] op_sel_hi:[1,0,1]
	v_pk_mul_f32 v[74:75], v[74:75], v[96:97] op_sel_hi:[1,0]
	v_pk_mul_f32 v[64:65], v[64:65], v[92:93] op_sel_hi:[1,0]
	v_med3_f32 v74, v74, s59, v161
	v_med3_f32 v75, v75, s59, v161
	v_cvt_pk_fp8_f32 v73, v74, v75 op_sel:[0,0,1]
	v_med3_f32 v64, v64, s59, v161
	v_med3_f32 v65, v65, s59, v161
	v_mov_b32_e32 v75, v145
	v_cvt_pk_fp8_f32 v75, v64, v65
	v_pk_fma_f32 v[66:67], v[66:67], s[18:19], v[130:131] op_sel_hi:[1,0,1]
	v_pk_fma_f32 v[68:69], v[68:69], s[18:19], v[132:133] op_sel_hi:[1,0,1]
	v_pk_mul_f32 v[66:67], v[66:67], v[92:93] op_sel_hi:[1,0]
	v_pk_mul_f32 v[68:69], v[68:69], v[92:93] op_sel_hi:[1,0]
	v_med3_f32 v64, v66, s59, v161
	v_med3_f32 v65, v67, s59, v161
	v_cvt_pk_fp8_f32 v75, v64, v65 op_sel:[0,0,1]
	ds_read2_b32 v[64:65], v169 offset0:64 offset1:80
	v_pk_fma_f32 v[60:61], v[60:61], s[18:19], v[140:141] op_sel_hi:[1,0,1]
	v_med3_f32 v68, v68, s59, v161
	v_med3_f32 v69, v69, s59, v161
	v_mov_b32_e32 v74, v145
	s_waitcnt lgkmcnt(0)
	v_mul_f32_e32 v64, 0x41800000, v64
	v_pk_fma_f32 v[62:63], v[62:63], s[18:19], v[142:143] op_sel_hi:[1,0,1]
	v_pk_mul_f32 v[60:61], v[60:61], v[64:65] op_sel_hi:[1,0]
	v_pk_fma_f32 v[56:57], v[56:57], s[18:19], v[136:137] op_sel_hi:[1,0,1]
	v_cvt_pk_fp8_f32 v74, v68, v69
	v_pk_mul_f32 v[62:63], v[62:63], v[64:65] op_sel_hi:[1,0]
	v_pk_mul_f32 v[68:69], v[56:57], v[64:65] op_sel_hi:[1,0]
	v_med3_f32 v57, v60, s59, v161
	v_med3_f32 v60, v61, s59, v161
	v_mov_b32_e32 v56, v145
	v_med3_f32 v61, v62, s59, v161
	v_med3_f32 v62, v63, s59, v161
	v_cvt_pk_fp8_f32 v56, v57, v60
	v_med3_f32 v60, v68, s59, v161
	v_med3_f32 v63, v69, s59, v161
	v_mov_b32_e32 v57, v145
	v_cvt_pk_fp8_f32 v57, v60, v63
	v_pk_fma_f32 v[58:59], v[58:59], s[18:19], v[138:139] op_sel_hi:[1,0,1]
	v_mul_f32_e32 v60, 0x41800000, v65
	v_pk_mul_f32 v[58:59], v[58:59], v[64:65] op_sel_hi:[1,0]
	v_pk_fma_f32 v[48:49], v[48:49], s[18:19], v[136:137] op_sel_hi:[1,0,1]
	v_med3_f32 v58, v58, s59, v161
	v_med3_f32 v59, v59, s59, v161
	v_pk_mul_f32 v[48:49], v[48:49], v[60:61] op_sel_hi:[1,0]
	v_cvt_pk_fp8_f32 v57, v58, v59 op_sel:[0,0,1]
	v_med3_f32 v48, v48, s59, v161
	v_med3_f32 v49, v49, s59, v161
	v_mov_b32_e32 v59, v145
	v_cvt_pk_fp8_f32 v59, v48, v49
	v_pk_fma_f32 v[50:51], v[50:51], s[18:19], v[138:139] op_sel_hi:[1,0,1]
	v_pk_fma_f32 v[44:45], v[44:45], s[18:19], v[132:133] op_sel_hi:[1,0,1]
	v_pk_mul_f32 v[50:51], v[50:51], v[60:61] op_sel_hi:[1,0]
	v_pk_fma_f32 v[46:47], v[46:47], s[18:19], v[134:135] op_sel_hi:[1,0,1]
	v_med3_f32 v48, v50, s59, v161
	v_med3_f32 v49, v51, s59, v161
	v_pk_mul_f32 v[44:45], v[44:45], v[64:65] op_sel_hi:[1,0]
	v_pk_fma_f32 v[40:41], v[40:41], s[18:19], v[128:129] op_sel_hi:[1,0,1]
	v_cvt_pk_fp8_f32 v59, v48, v49 op_sel:[0,0,1]
	v_pk_mul_f32 v[46:47], v[46:47], v[64:65] op_sel_hi:[1,0]
	v_pk_mul_f32 v[48:49], v[40:41], v[64:65] op_sel_hi:[1,0]
	v_med3_f32 v41, v44, s59, v161
	v_med3_f32 v44, v45, s59, v161
	v_mov_b32_e32 v40, v145
	v_med3_f32 v45, v46, s59, v161
	v_med3_f32 v46, v47, s59, v161
	v_cvt_pk_fp8_f32 v40, v41, v44
	v_med3_f32 v44, v48, s59, v161
	v_med3_f32 v47, v49, s59, v161
	v_mov_b32_e32 v41, v145
	v_cvt_pk_fp8_f32 v41, v44, v47
	v_pk_fma_f32 v[42:43], v[42:43], s[18:19], v[130:131] op_sel_hi:[1,0,1]
	v_pk_fma_f32 v[32:33], v[32:33], s[18:19], v[128:129] op_sel_hi:[1,0,1]
	v_pk_mul_f32 v[42:43], v[42:43], v[64:65] op_sel_hi:[1,0]
	v_pk_mul_f32 v[32:33], v[32:33], v[60:61] op_sel_hi:[1,0]
	v_med3_f32 v42, v42, s59, v161
	v_med3_f32 v43, v43, s59, v161
	v_cvt_pk_fp8_f32 v41, v42, v43 op_sel:[0,0,1]
	v_med3_f32 v32, v32, s59, v161
	v_med3_f32 v33, v33, s59, v161
	v_mov_b32_e32 v43, v145
	v_cvt_pk_fp8_f32 v43, v32, v33
	v_pk_fma_f32 v[34:35], v[34:35], s[18:19], v[130:131] op_sel_hi:[1,0,1]
	v_pk_fma_f32 v[36:37], v[36:37], s[18:19], v[132:133] op_sel_hi:[1,0,1]
	v_pk_mul_f32 v[34:35], v[34:35], v[60:61] op_sel_hi:[1,0]
	v_pk_mul_f32 v[36:37], v[36:37], v[60:61] op_sel_hi:[1,0]
	v_med3_f32 v32, v34, s59, v161
	v_med3_f32 v33, v35, s59, v161
	v_cvt_pk_fp8_f32 v43, v32, v33 op_sel:[0,0,1]
	ds_read2_b32 v[32:33], v169 offset0:96 offset1:112
	v_pk_fma_f32 v[28:29], v[28:29], s[18:19], v[140:141] op_sel_hi:[1,0,1]
	v_med3_f32 v36, v36, s59, v161
	v_med3_f32 v37, v37, s59, v161
	v_mov_b32_e32 v42, v145
	s_waitcnt lgkmcnt(0)
;     DI void operator()(const f32x4 (&acc)[2][2][4][2], const Unit& u, int wr, int wc, int fr, int fq, const LAS unsigned char* st) const {
;     ...
;                 for (int bj = 0; bj < 2; ++bj) { u32x2 w2[2];
; #pragma unroll
;                     for (int mm = 0; mm < 2; ++mm) { const int m = 2 * mp + mm; const float w8 = mm ? wB : wA;
;                         const f32x4 v0 = (acc[ai][bj][m][0] * (1.0f / 128.0f) + bv[bj][0]) * w8, v1 = (acc[ai][bj][m][1] * (1.0f / 128.0f) + bv[bj][1]) * w8;
;                         w2[mm].x = pk4_fp8m(v0[0], v0[1], v0[2], v0[3]); w2[mm].y = pk4_fp8m(v1[0], v1[1], v1[2], v1[3]); }
	v_mul_f32_e32 v32, 0x41800000, v32
	v_pk_fma_f32 v[30:31], v[30:31], s[18:19], v[142:143] op_sel_hi:[1,0,1]
	v_pk_mul_f32 v[28:29], v[28:29], v[32:33] op_sel_hi:[1,0]
	v_pk_fma_f32 v[24:25], v[24:25], s[18:19], v[136:137] op_sel_hi:[1,0,1]
	v_cvt_pk_fp8_f32 v42, v36, v37
	v_pk_mul_f32 v[30:31], v[30:31], v[32:33] op_sel_hi:[1,0]
	v_pk_mul_f32 v[36:37], v[24:25], v[32:33] op_sel_hi:[1,0]
	v_med3_f32 v25, v28, s59, v161
	v_med3_f32 v28, v29, s59, v161
	v_mov_b32_e32 v24, v145
	v_med3_f32 v29, v30, s59, v161
	v_med3_f32 v30, v31, s59, v161
	v_cvt_pk_fp8_f32 v24, v25, v28
	v_med3_f32 v28, v36, s59, v161
	v_med3_f32 v31, v37, s59, v161
	v_mov_b32_e32 v25, v145
	v_cvt_pk_fp8_f32 v25, v28, v31
	v_pk_fma_f32 v[26:27], v[26:27], s[18:19], v[138:139] op_sel_hi:[1,0,1]
	v_mul_f32_e32 v28, 0x41800000, v33
	v_pk_mul_f32 v[26:27], v[26:27], v[32:33] op_sel_hi:[1,0]
	v_pk_fma_f32 v[16:17], v[16:17], s[18:19], v[136:137] op_sel_hi:[1,0,1]
	v_med3_f32 v26, v26, s59, v161
	v_med3_f32 v27, v27, s59, v161
	v_pk_mul_f32 v[16:17], v[16:17], v[28:29] op_sel_hi:[1,0]
	v_cvt_pk_fp8_f32 v25, v26, v27 op_sel:[0,0,1]
	v_med3_f32 v16, v16, s59, v161
	v_med3_f32 v17, v17, s59, v161
	v_mov_b32_e32 v27, v145
	v_cvt_pk_fp8_f32 v27, v16, v17
	v_pk_fma_f32 v[18:19], v[18:19], s[18:19], v[138:139] op_sel_hi:[1,0,1]
	v_pk_fma_f32 v[12:13], v[12:13], s[18:19], v[132:133] op_sel_hi:[1,0,1]
	v_pk_mul_f32 v[18:19], v[18:19], v[28:29] op_sel_hi:[1,0]
	v_pk_fma_f32 v[14:15], v[14:15], s[18:19], v[134:135] op_sel_hi:[1,0,1]
	v_med3_f32 v16, v18, s59, v161
	v_med3_f32 v17, v19, s59, v161
	v_pk_mul_f32 v[12:13], v[12:13], v[32:33] op_sel_hi:[1,0]
	v_pk_fma_f32 v[8:9], v[8:9], s[18:19], v[128:129] op_sel_hi:[1,0,1]
	v_cvt_pk_fp8_f32 v27, v16, v17 op_sel:[0,0,1]
	v_pk_mul_f32 v[14:15], v[14:15], v[32:33] op_sel_hi:[1,0]
	v_pk_mul_f32 v[16:17], v[8:9], v[32:33] op_sel_hi:[1,0]
	v_med3_f32 v9, v12, s59, v161
	v_med3_f32 v12, v13, s59, v161
	v_mov_b32_e32 v8, v145
	v_med3_f32 v13, v14, s59, v161
	v_med3_f32 v14, v15, s59, v161
	v_cvt_pk_fp8_f32 v8, v9, v12
	v_med3_f32 v12, v16, s59, v161
	v_med3_f32 v15, v17, s59, v161
	v_mov_b32_e32 v9, v145
	v_cvt_pk_fp8_f32 v9, v12, v15
	v_pk_fma_f32 v[10:11], v[10:11], s[18:19], v[130:131] op_sel_hi:[1,0,1]
	v_pk_fma_f32 v[116:117], v[116:117], s[18:19], v[140:141] op_sel_hi:[1,0,1]
	v_pk_fma_f32 v[84:85], v[84:85], s[18:19], v[140:141] op_sel_hi:[1,0,1]
	v_pk_fma_f32 v[52:53], v[52:53], s[18:19], v[140:141] op_sel_hi:[1,0,1]
	v_pk_fma_f32 v[20:21], v[20:21], s[18:19], v[140:141] op_sel_hi:[1,0,1]
	v_pk_mul_f32 v[10:11], v[10:11], v[32:33] op_sel_hi:[1,0]
	v_pk_fma_f32 v[4:5], v[4:5], s[18:19], v[132:133] op_sel_hi:[1,0,1]
	v_pk_fma_f32 v[0:1], v[0:1], s[18:19], v[128:129] op_sel_hi:[1,0,1]
	v_pk_mul_f32 v[116:117], v[116:117], v[124:125] op_sel_hi:[1,0]
	v_pk_mul_f32 v[84:85], v[84:85], v[92:93] op_sel_hi:[1,0]
	v_pk_mul_f32 v[52:53], v[52:53], v[60:61] op_sel_hi:[1,0]
	v_pk_mul_f32 v[20:21], v[20:21], v[28:29] op_sel_hi:[1,0]
	v_med3_f32 v10, v10, s59, v161
	v_med3_f32 v11, v11, s59, v161
	v_pk_mul_f32 v[4:5], v[4:5], v[28:29] op_sel_hi:[1,0]
	v_pk_mul_f32 v[0:1], v[0:1], v[28:29] op_sel_hi:[1,0]
	v_med3_f32 v116, v116, s59, v161
	v_med3_f32 v117, v117, s59, v161
	v_mov_b32_e32 v122, v145
	v_med3_f32 v84, v84, s59, v161
	v_med3_f32 v85, v85, s59, v161
	v_mov_b32_e32 v90, v145
	v_med3_f32 v52, v52, s59, v161
	v_med3_f32 v53, v53, s59, v161
	v_mov_b32_e32 v58, v145
	v_med3_f32 v20, v20, s59, v161
	v_med3_f32 v21, v21, s59, v161
	v_mov_b32_e32 v26, v145
	v_cvt_pk_fp8_f32 v9, v10, v11 op_sel:[0,0,1]
	v_med3_f32 v4, v4, s59, v161
	v_med3_f32 v5, v5, s59, v161
	v_mov_b32_e32 v10, v145
	v_med3_f32 v0, v0, s59, v161
	v_med3_f32 v1, v1, s59, v161
	v_mov_b32_e32 v11, v145
	v_cvt_pk_fp8_f32 v122, v116, v117
	v_pk_fma_f32 v[102:103], v[102:103], s[18:19], v[134:135] op_sel_hi:[1,0,1]
	v_cvt_pk_fp8_f32 v90, v84, v85
	v_pk_fma_f32 v[70:71], v[70:71], s[18:19], v[134:135] op_sel_hi:[1,0,1]
	v_cvt_pk_fp8_f32 v58, v52, v53
	v_cvt_pk_fp8_f32 v26, v20, v21
	v_cvt_pk_fp8_f32 v10, v4, v5
	v_cvt_pk_fp8_f32 v11, v0, v1
	v_pk_fma_f32 v[118:119], v[118:119], s[18:19], v[142:143] op_sel_hi:[1,0,1]
	v_pk_mul_f32 v[102:103], v[102:103], v[124:125] op_sel_hi:[1,0]
	v_pk_fma_f32 v[86:87], v[86:87], s[18:19], v[142:143] op_sel_hi:[1,0,1]
	v_pk_mul_f32 v[70:71], v[70:71], v[92:93] op_sel_hi:[1,0]
	v_pk_fma_f32 v[54:55], v[54:55], s[18:19], v[142:143] op_sel_hi:[1,0,1]
	v_pk_fma_f32 v[38:39], v[38:39], s[18:19], v[134:135] op_sel_hi:[1,0,1]
	v_pk_fma_f32 v[22:23], v[22:23], s[18:19], v[142:143] op_sel_hi:[1,0,1]
	v_pk_fma_f32 v[6:7], v[6:7], s[18:19], v[134:135] op_sel_hi:[1,0,1]
	v_pk_fma_f32 v[2:3], v[2:3], s[18:19], v[130:131] op_sel_hi:[1,0,1]
	v_pk_mul_f32 v[118:119], v[118:119], v[124:125] op_sel_hi:[1,0]
; #define LAS __attribute__((address_space(3)))
; #define PG8_DMA4(gp, lp) __builtin_amdgcn_global_load_lds((const unsigned*)(gp), (LAS unsigned*)(lp), 4, 0, 0)
;     DI void prefetch(const Unit& u, int wr, int wc, int lane, LAS unsigned char* st) const {
;         const float* rp = roww + u.pm * BM + wr * 64 + lane;
;         PG8_DMA4(rp, st); PG8_DMA4(rp + HALF, st + 256);
;         PG8_DMA4(b_down + (size_t)u.e * DM + u.pn * BM + (lane >> 5) * HALF + wc * 32 + (lane & 31), st + 512);
;     }
;     DI void operator()(const f32x4 (&acc)[2][2][4][2], const Unit& u, int wr, int wc, int fr, int fq, const LAS unsigned char* st) const {
;     ...
;                 for (int bj = 0; bj < 2; ++bj) { u32x2 w2[2];
; #pragma unroll
;                     for (int mm = 0; mm < 2; ++mm) { const int m = 2 * mp + mm; const float w8 = mm ? wB : wA;
;                         const f32x4 v0 = (acc[ai][bj][m][0] * (1.0f / 128.0f) + bv[bj][0]) * w8, v1 = (acc[ai][bj][m][1] * (1.0f / 128.0f) + bv[bj][1]) * w8;
;                         w2[mm].x = pk4_fp8m(v0[0], v0[1], v0[2], v0[3]); w2[mm].y = pk4_fp8m(v1[0], v1[1], v1[2], v1[3]); }
;                     *(u32x4*)(rowp + bj * HALF) = pair16(w2[0], w2[1]); } }
	v_med3_f32 v102, v102, s59, v161
	v_med3_f32 v103, v103, s59, v161
	v_pk_mul_f32 v[86:87], v[86:87], v[92:93] op_sel_hi:[1,0]
	v_med3_f32 v70, v70, s59, v161
	v_med3_f32 v71, v71, s59, v161
	v_pk_mul_f32 v[54:55], v[54:55], v[60:61] op_sel_hi:[1,0]
	v_pk_mul_f32 v[38:39], v[38:39], v[60:61] op_sel_hi:[1,0]
	v_pk_mul_f32 v[22:23], v[22:23], v[28:29] op_sel_hi:[1,0]
	v_pk_mul_f32 v[6:7], v[6:7], v[28:29] op_sel_hi:[1,0]
	v_pk_mul_f32 v[2:3], v[2:3], v[28:29] op_sel_hi:[1,0]
	v_med3_f32 v118, v118, s59, v161
	v_med3_f32 v119, v119, s59, v161
	v_cvt_pk_fp8_f32 v106, v102, v103 op_sel:[0,0,1]
	v_or_b32_e32 v102, 32, v170
	v_med3_f32 v86, v86, s59, v161
	v_med3_f32 v87, v87, s59, v161
	v_cvt_pk_fp8_f32 v74, v70, v71 op_sel:[0,0,1]
	v_add_u32_e32 v70, 0x80, v168
	v_med3_f32 v54, v54, s59, v161
	v_med3_f32 v55, v55, s59, v161
	v_med3_f32 v38, v38, s59, v161
	v_med3_f32 v39, v39, s59, v161
	v_med3_f32 v22, v22, s59, v161
	v_med3_f32 v23, v23, s59, v161
	v_med3_f32 v6, v6, s59, v161
	v_med3_f32 v7, v7, s59, v161
	v_med3_f32 v0, v2, s59, v161
	v_med3_f32 v1, v3, s59, v161
	v_or_b32_e32 v164, v170, v168
	v_cvt_pk_fp8_f32 v120, v125, v126 op_sel:[0,0,1]
	v_cvt_pk_fp8_f32 v122, v118, v119 op_sel:[0,0,1]
	v_cvt_pk_fp8_f32 v104, v109, v110 op_sel:[0,0,1]
	v_or_b32_e32 v98, v102, v168
	v_cvt_pk_fp8_f32 v88, v93, v94 op_sel:[0,0,1]
	v_cvt_pk_fp8_f32 v90, v86, v87 op_sel:[0,0,1]
	v_cvt_pk_fp8_f32 v72, v77, v78 op_sel:[0,0,1]
	v_or_b32_e32 v66, v170, v70
	v_cvt_pk_fp8_f32 v56, v61, v62 op_sel:[0,0,1]
	v_cvt_pk_fp8_f32 v58, v54, v55 op_sel:[0,0,1]
	v_cvt_pk_fp8_f32 v40, v45, v46 op_sel:[0,0,1]
	v_cvt_pk_fp8_f32 v42, v38, v39 op_sel:[0,0,1]
	v_or_b32_e32 v34, v102, v70
	v_cvt_pk_fp8_f32 v24, v29, v30 op_sel:[0,0,1]
	v_cvt_pk_fp8_f32 v26, v22, v23 op_sel:[0,0,1]
	v_cvt_pk_fp8_f32 v8, v13, v14 op_sel:[0,0,1]
	v_cvt_pk_fp8_f32 v10, v6, v7 op_sel:[0,0,1]
	v_cvt_pk_fp8_f32 v11, v0, v1 op_sel:[0,0,1]
	v_ashrrev_i32_e32 v165, 31, v164
	v_ashrrev_i32_e32 v99, 31, v98
	v_ashrrev_i32_e32 v67, 31, v66
	v_ashrrev_i32_e32 v35, 31, v34
	v_sub_u32_e32 v148, v149, v148
	v_lshlrev_b64 v[164:165], 11, v[164:165]
	v_lshlrev_b64 v[98:99], 11, v[98:99]
	v_lshlrev_b64 v[66:67], 11, v[66:67]
	v_lshlrev_b64 v[34:35], 11, v[34:35]
	v_ashrrev_i32_e32 v149, 31, v148
	v_lshl_add_u64 v[164:165], s[12:13], 0, v[164:165]
	v_lshl_add_u64 v[98:99], s[12:13], 0, v[98:99]
	v_lshl_add_u64 v[66:67], s[12:13], 0, v[66:67]
	v_lshl_add_u64 v[34:35], s[12:13], 0, v[34:35]
	v_lshl_add_u64 v[164:165], v[164:165], 0, v[148:149]
	v_permlane16_swap_b32_e32 v120, v122
	v_permlane16_swap_b32_e32 v121, v123
	v_permlane16_swap_b32_e32 v104, v106
	v_permlane16_swap_b32_e32 v105, v107
	v_lshl_add_u64 v[98:99], v[98:99], 0, v[148:149]
	v_permlane16_swap_b32_e32 v88, v90
	v_permlane16_swap_b32_e32 v89, v91
	v_permlane16_swap_b32_e32 v72, v74
	v_permlane16_swap_b32_e32 v73, v75
	v_lshl_add_u64 v[66:67], v[66:67], 0, v[148:149]
	v_permlane16_swap_b32_e32 v56, v58
	v_permlane16_swap_b32_e32 v57, v59
	v_permlane16_swap_b32_e32 v40, v42
	v_permlane16_swap_b32_e32 v41, v43
	v_lshl_add_u64 v[34:35], v[34:35], 0, v[148:149]
	v_permlane16_swap_b32_e32 v24, v26
	v_permlane16_swap_b32_e32 v25, v27
	v_permlane16_swap_b32_e32 v8, v10
	v_permlane16_swap_b32_e32 v9, v11
	s_and_b64 vcc, exec, s[2:3]
	s_mov_b64 s[0:1], -1
	global_store_dwordx4 v[164:165], v[120:123], off nt
	global_store_dwordx4 v[164:165], v[104:107], off offset:128 nt
	global_store_dwordx4 v[98:99], v[88:91], off nt
	global_store_dwordx4 v[98:99], v[72:75], off offset:128 nt
	global_store_dwordx4 v[66:67], v[56:59], off nt
	global_store_dwordx4 v[66:67], v[40:43], off offset:128 nt
	global_store_dwordx4 v[34:35], v[24:27], off nt
	global_store_dwordx4 v[34:35], v[8:11], off offset:128 nt
	s_cbranch_vccnz .LBB0_1155
	s_lshl_b32 s0, s22, 8
	s_ashr_i32 s1, s0, 31
	s_lshl_b64 s[0:1], s[0:1], 2
	v_mov_b32_e32 v0, v224
	s_add_u32 s0, s55, s0
	s_addc_u32 s1, s56, s1
	v_ashrrev_i32_e32 v1, 31, v0
	s_mov_b32 m0, s29
	v_lshl_add_u64 v[2:3], v[0:1], 2, s[0:1]
	global_load_lds_dword v[2:3], off
	s_add_i32 m0, s29, 0x100
	s_lshl_b64 s[0:1], s[26:27], 13
	s_add_u32 s2, s90, s0
	s_addc_u32 s3, s91, s1
	s_lshl_b32 s0, s20, 8
	s_ashr_i32 s1, s0, 31
	v_lshl_add_u64 v[2:3], v[2:3], 0, s[8:9]
	s_lshl_b64 s[0:1], s[0:1], 2
	v_lshlrev_b32_e32 v1, 2, v0
	global_load_lds_dword v[2:3], off
	s_add_u32 s0, s2, s0
	v_and_b32_e32 v2, 0xffffff80, v1
	s_addc_u32 s1, s3, s1
	v_ashrrev_i32_e32 v3, 31, v2
	v_lshl_add_u64 v[2:3], v[2:3], 2, s[0:1]
	v_and_b32_e32 v0, 31, v0
	v_lshl_add_u64 v[2:3], v[2:3], 0, s[6:7]
	v_lshlrev_b32_e32 v144, 2, v0
	v_lshl_add_u64 v[0:1], v[2:3], 0, v[144:145]
	s_mov_b32 m0, s60
	s_andn2_b64 vcc, exec, s[10:11]
	global_load_lds_dword v[0:1], off
	s_cbranch_vccnz .LBB0_1154
	s_barrier
	s_branch .LBB0_1154
